# all GEMM K-loops: last iteration of a workgroup's last unit skips the 12 next-unit LDS-DMA pieces per wave that re-load its own K-tiles (separate copy of the iteration)
# speedup vs baseline: 1.0154x; 1.0154x over previous
.LBB0_225:
	ds_read_b128 v[2:5], v169
	ds_read_b128 v[6:9], v169 offset:1024
	ds_read_b128 v[10:13], v169 offset:2048
	ds_read_b128 v[14:17], v169 offset:3072
	ds_read_b128 v[18:21], v170
	ds_read_b128 v[22:25], v170 offset:1024
	ds_read_b128 v[26:29], v170 offset:2048
	ds_read_b128 v[30:33], v170 offset:3072
	s_add_i32 s15, s29, 0xfffc0080
	s_cmp_eq_u32 s62, 12
	s_cselect_b32 s14, vcc_hi, s28
	s_cselect_b32 s15, vcc_lo, s15
	s_cbranch_scc0 .Lnx_0
	s_cmp_eq_u64 s[38:39], 0
	s_cbranch_scc1 .Lfin_0
.Lnx_0:
	s_add_i32 s63, s29, 0xfffc0000
	s_mov_b32 m0, s79
	ds_read_b128 v[174:177], v171
	ds_read_b128 v[178:181], v171 offset:1024
	ds_read_b128 v[182:185], v171 offset:2048
	ds_read_b128 v[186:189], v171 offset:3072
	ds_read_b128 v[190:193], v171 offset:4096
	ds_read_b128 v[194:197], v171 offset:5120
	ds_read_b128 v[204:207], v171 offset:6144
	ds_read_b128 v[208:211], v171 offset:7168
	buffer_load_dwordx4 v163, s[64:67], s63 offen lds
	s_mov_b32 m0, s81
	s_nop 0
	buffer_load_dwordx4 v165, s[64:67], s63 offen lds
	s_mov_b32 m0, s80
	s_nop 0
	buffer_load_dwordx4 v163, s[64:67], s29 offen lds
	s_mov_b32 m0, s82
	s_nop 0
	buffer_load_dwordx4 v165, s[64:67], s29 offen lds
	s_waitcnt vmcnt(8)
	s_waitcnt lgkmcnt(0)
	s_barrier
	s_setprio 1
	s_waitcnt lgkmcnt(6)
	v_mfma_scale_f32_16x16x128_f8f6f4 v[150:153], v[2:9], v[174:181], v[150:153], v234, v234 op_sel_hi:[0,0,0]
	v_mfma_scale_f32_16x16x128_f8f6f4 v[146:149], v[10:17], v[174:181], v[146:149], v234, v234 op_sel_hi:[0,0,0]
	s_waitcnt lgkmcnt(4)
	v_mfma_scale_f32_16x16x128_f8f6f4 v[134:137], v[2:9], v[182:189], v[134:137], v234, v234 op_sel_hi:[0,0,0]
	v_mfma_scale_f32_16x16x128_f8f6f4 v[130:133], v[10:17], v[182:189], v[130:133], v234, v234 op_sel_hi:[0,0,0]
	s_waitcnt lgkmcnt(2)
	v_mfma_scale_f32_16x16x128_f8f6f4 v[118:121], v[2:9], v[190:197], v[118:121], v234, v234 op_sel_hi:[0,0,0]
	v_mfma_scale_f32_16x16x128_f8f6f4 v[114:117], v[10:17], v[190:197], v[114:117], v234, v234 op_sel_hi:[0,0,0]
	s_waitcnt lgkmcnt(0)
	v_mfma_scale_f32_16x16x128_f8f6f4 v[98:101], v[2:9], v[204:211], v[98:101], v234, v234 op_sel_hi:[0,0,0]
	v_mfma_scale_f32_16x16x128_f8f6f4 v[90:93], v[10:17], v[204:211], v[90:93], v234, v234 op_sel_hi:[0,0,0]
	v_mfma_scale_f32_16x16x128_f8f6f4 v[158:161], v[18:25], v[174:181], v[158:161], v234, v234 op_sel_hi:[0,0,0]
	v_mfma_scale_f32_16x16x128_f8f6f4 v[154:157], v[26:33], v[174:181], v[154:157], v234, v234 op_sel_hi:[0,0,0]
	v_mfma_scale_f32_16x16x128_f8f6f4 v[142:145], v[18:25], v[182:189], v[142:145], v234, v234 op_sel_hi:[0,0,0]
	v_mfma_scale_f32_16x16x128_f8f6f4 v[138:141], v[26:33], v[182:189], v[138:141], v234, v234 op_sel_hi:[0,0,0]
	v_mfma_scale_f32_16x16x128_f8f6f4 v[126:129], v[18:25], v[190:197], v[126:129], v234, v234 op_sel_hi:[0,0,0]
	v_mfma_scale_f32_16x16x128_f8f6f4 v[122:125], v[26:33], v[190:197], v[122:125], v234, v234 op_sel_hi:[0,0,0]
	v_mfma_scale_f32_16x16x128_f8f6f4 v[110:113], v[18:25], v[204:211], v[110:113], v234, v234 op_sel_hi:[0,0,0]
	v_mfma_scale_f32_16x16x128_f8f6f4 v[106:109], v[26:33], v[204:211], v[106:109], v234, v234 op_sel_hi:[0,0,0]
	s_setprio 0
	s_barrier
	s_mov_b32 m0, s9
	ds_read_b128 v[174:177], v171 offset:16384
	ds_read_b128 v[178:181], v171 offset:17408
	ds_read_b128 v[182:185], v171 offset:18432
	ds_read_b128 v[186:189], v171 offset:19456
	ds_read_b128 v[190:193], v171 offset:20480
	ds_read_b128 v[194:197], v171 offset:21504
	ds_read_b128 v[204:207], v171 offset:22528
	ds_read_b128 v[208:211], v171 offset:23552
	buffer_load_dwordx4 v164, s[4:7], s14 offen lds
	s_mov_b32 m0, s10
	s_add_i32 s63, s14, 0x40000
	buffer_load_dwordx4 v166, s[4:7], s14 offen lds
	s_mov_b32 m0, s11
	s_nop 0
	buffer_load_dwordx4 v164, s[4:7], s63 offen lds
	s_mov_b32 m0, s12
	s_nop 0
	buffer_load_dwordx4 v166, s[4:7], s63 offen lds
	s_waitcnt vmcnt(6)
	s_waitcnt lgkmcnt(0)
	s_barrier
	s_setprio 1
	s_waitcnt lgkmcnt(6)
	v_mfma_scale_f32_16x16x128_f8f6f4 v[86:89], v[2:9], v[174:181], v[86:89], v234, v234 op_sel_hi:[0,0,0]
	v_mfma_scale_f32_16x16x128_f8f6f4 v[82:85], v[10:17], v[174:181], v[82:85], v234, v234 op_sel_hi:[0,0,0]
	s_waitcnt lgkmcnt(4)
	v_mfma_scale_f32_16x16x128_f8f6f4 v[70:73], v[2:9], v[182:189], v[70:73], v234, v234 op_sel_hi:[0,0,0]
	v_mfma_scale_f32_16x16x128_f8f6f4 v[66:69], v[10:17], v[182:189], v[66:69], v234, v234 op_sel_hi:[0,0,0]
	s_waitcnt lgkmcnt(2)
	v_mfma_scale_f32_16x16x128_f8f6f4 v[58:61], v[2:9], v[190:197], v[58:61], v234, v234 op_sel_hi:[0,0,0]
	v_mfma_scale_f32_16x16x128_f8f6f4 v[50:53], v[10:17], v[190:197], v[50:53], v234, v234 op_sel_hi:[0,0,0]
	s_waitcnt lgkmcnt(0)
	v_mfma_scale_f32_16x16x128_f8f6f4 v[42:45], v[2:9], v[204:211], v[42:45], v234, v234 op_sel_hi:[0,0,0]
	v_mfma_scale_f32_16x16x128_f8f6f4 v[34:37], v[10:17], v[204:211], v[34:37], v234, v234 op_sel_hi:[0,0,0]
	v_mfma_scale_f32_16x16x128_f8f6f4 v[102:105], v[18:25], v[174:181], v[102:105], v234, v234 op_sel_hi:[0,0,0]
	v_mfma_scale_f32_16x16x128_f8f6f4 v[94:97], v[26:33], v[174:181], v[94:97], v234, v234 op_sel_hi:[0,0,0]
	v_mfma_scale_f32_16x16x128_f8f6f4 v[78:81], v[18:25], v[182:189], v[78:81], v234, v234 op_sel_hi:[0,0,0]
	v_mfma_scale_f32_16x16x128_f8f6f4 v[74:77], v[26:33], v[182:189], v[74:77], v234, v234 op_sel_hi:[0,0,0]
	v_mfma_scale_f32_16x16x128_f8f6f4 v[62:65], v[18:25], v[190:197], v[62:65], v234, v234 op_sel_hi:[0,0,0]
	v_mfma_scale_f32_16x16x128_f8f6f4 v[54:57], v[26:33], v[190:197], v[54:57], v234, v234 op_sel_hi:[0,0,0]
	v_mfma_scale_f32_16x16x128_f8f6f4 v[46:49], v[18:25], v[204:211], v[46:49], v234, v234 op_sel_hi:[0,0,0]
	v_mfma_scale_f32_16x16x128_f8f6f4 v[38:41], v[26:33], v[204:211], v[38:41], v234, v234 op_sel_hi:[0,0,0]
	s_setprio 0
	s_barrier
	ds_read_b128 v[18:21], v172
	ds_read_b128 v[22:25], v172 offset:1024
	ds_read_b128 v[26:29], v172 offset:2048
	ds_read_b128 v[30:33], v172 offset:3072
	ds_read_b128 v[10:13], v173
	ds_read_b128 v[14:17], v173 offset:1024
	ds_read_b128 v[2:5], v173 offset:2048
	ds_read_b128 v[6:9], v173 offset:3072
	s_mov_b32 m0, s8
	ds_read_b128 v[174:177], v171 offset:32768
	ds_read_b128 v[178:181], v171 offset:33792
	ds_read_b128 v[182:185], v171 offset:34816
	ds_read_b128 v[186:189], v171 offset:35840
	ds_read_b128 v[190:193], v171 offset:36864
	ds_read_b128 v[194:197], v171 offset:37888
	ds_read_b128 v[204:207], v171 offset:38912
	ds_read_b128 v[208:211], v171 offset:39936
	buffer_load_dwordx4 v163, s[64:67], s15 offen lds
	s_mov_b32 m0, s13
	s_nop 0
	buffer_load_dwordx4 v165, s[64:67], s15 offen lds
	s_add_i32 s15, s15, 0x40000
	s_mov_b32 m0, s20
	s_nop 0
	buffer_load_dwordx4 v163, s[64:67], s15 offen lds
	s_mov_b32 m0, s21
	s_nop 0
	buffer_load_dwordx4 v165, s[64:67], s15 offen lds
	s_waitcnt vmcnt(8)
	s_waitcnt lgkmcnt(0)
	s_barrier
	s_setprio 1
	s_waitcnt lgkmcnt(6)
	v_mfma_scale_f32_16x16x128_f8f6f4 v[150:153], v[18:25], v[174:181], v[150:153], v234, v234 op_sel_hi:[0,0,0]
	v_mfma_scale_f32_16x16x128_f8f6f4 v[146:149], v[26:33], v[174:181], v[146:149], v234, v234 op_sel_hi:[0,0,0]
	s_waitcnt lgkmcnt(4)
	v_mfma_scale_f32_16x16x128_f8f6f4 v[134:137], v[18:25], v[182:189], v[134:137], v234, v234 op_sel_hi:[0,0,0]
	v_mfma_scale_f32_16x16x128_f8f6f4 v[130:133], v[26:33], v[182:189], v[130:133], v234, v234 op_sel_hi:[0,0,0]
	s_waitcnt lgkmcnt(2)
	v_mfma_scale_f32_16x16x128_f8f6f4 v[118:121], v[18:25], v[190:197], v[118:121], v234, v234 op_sel_hi:[0,0,0]
	v_mfma_scale_f32_16x16x128_f8f6f4 v[114:117], v[26:33], v[190:197], v[114:117], v234, v234 op_sel_hi:[0,0,0]
	s_waitcnt lgkmcnt(0)
	v_mfma_scale_f32_16x16x128_f8f6f4 v[98:101], v[18:25], v[204:211], v[98:101], v234, v234 op_sel_hi:[0,0,0]
	v_mfma_scale_f32_16x16x128_f8f6f4 v[90:93], v[26:33], v[204:211], v[90:93], v234, v234 op_sel_hi:[0,0,0]
	v_mfma_scale_f32_16x16x128_f8f6f4 v[158:161], v[10:17], v[174:181], v[158:161], v234, v234 op_sel_hi:[0,0,0]
	v_mfma_scale_f32_16x16x128_f8f6f4 v[154:157], v[2:9], v[174:181], v[154:157], v234, v234 op_sel_hi:[0,0,0]
	v_mfma_scale_f32_16x16x128_f8f6f4 v[142:145], v[10:17], v[182:189], v[142:145], v234, v234 op_sel_hi:[0,0,0]
	v_mfma_scale_f32_16x16x128_f8f6f4 v[138:141], v[2:9], v[182:189], v[138:141], v234, v234 op_sel_hi:[0,0,0]
	v_mfma_scale_f32_16x16x128_f8f6f4 v[126:129], v[10:17], v[190:197], v[126:129], v234, v234 op_sel_hi:[0,0,0]
	v_mfma_scale_f32_16x16x128_f8f6f4 v[122:125], v[2:9], v[190:197], v[122:125], v234, v234 op_sel_hi:[0,0,0]
	v_mfma_scale_f32_16x16x128_f8f6f4 v[110:113], v[10:17], v[204:211], v[110:113], v234, v234 op_sel_hi:[0,0,0]
	v_mfma_scale_f32_16x16x128_f8f6f4 v[106:109], v[2:9], v[204:211], v[106:109], v234, v234 op_sel_hi:[0,0,0]
	s_setprio 0
	s_barrier
	s_mov_b32 m0, s26
	s_or_b32 s15, s14, 0x80
	ds_read_b128 v[174:177], v171 offset:49152
	ds_read_b128 v[178:181], v171 offset:50176
	ds_read_b128 v[182:185], v171 offset:51200
	ds_read_b128 v[186:189], v171 offset:52224
	ds_read_b128 v[190:193], v171 offset:53248
	ds_read_b128 v[194:197], v171 offset:54272
	ds_read_b128 v[204:207], v171 offset:55296
	ds_read_b128 v[208:211], v171 offset:56320
	buffer_load_dwordx4 v164, s[4:7], s15 offen lds
	s_mov_b32 m0, s27
	s_add_i32 s14, s14, 0x40080
	buffer_load_dwordx4 v166, s[4:7], s15 offen lds
	s_mov_b32 m0, s40
	s_nop 0
	buffer_load_dwordx4 v164, s[4:7], s14 offen lds
	s_mov_b32 m0, s76
	s_nop 0
	buffer_load_dwordx4 v166, s[4:7], s14 offen lds
	s_waitcnt vmcnt(6)
	s_waitcnt lgkmcnt(0)
	s_barrier
	s_setprio 1
	s_waitcnt lgkmcnt(6)
	v_mfma_scale_f32_16x16x128_f8f6f4 v[86:89], v[18:25], v[174:181], v[86:89], v234, v234 op_sel_hi:[0,0,0]
	v_mfma_scale_f32_16x16x128_f8f6f4 v[82:85], v[26:33], v[174:181], v[82:85], v234, v234 op_sel_hi:[0,0,0]
	s_waitcnt lgkmcnt(4)
	v_mfma_scale_f32_16x16x128_f8f6f4 v[70:73], v[18:25], v[182:189], v[70:73], v234, v234 op_sel_hi:[0,0,0]
	v_mfma_scale_f32_16x16x128_f8f6f4 v[66:69], v[26:33], v[182:189], v[66:69], v234, v234 op_sel_hi:[0,0,0]
	s_waitcnt lgkmcnt(2)
	v_mfma_scale_f32_16x16x128_f8f6f4 v[58:61], v[18:25], v[190:197], v[58:61], v234, v234 op_sel_hi:[0,0,0]
	v_mfma_scale_f32_16x16x128_f8f6f4 v[50:53], v[26:33], v[190:197], v[50:53], v234, v234 op_sel_hi:[0,0,0]
	s_waitcnt lgkmcnt(0)
	v_mfma_scale_f32_16x16x128_f8f6f4 v[42:45], v[18:25], v[204:211], v[42:45], v234, v234 op_sel_hi:[0,0,0]
	v_mfma_scale_f32_16x16x128_f8f6f4 v[34:37], v[26:33], v[204:211], v[34:37], v234, v234 op_sel_hi:[0,0,0]
	v_mfma_scale_f32_16x16x128_f8f6f4 v[102:105], v[10:17], v[174:181], v[102:105], v234, v234 op_sel_hi:[0,0,0]
	v_mfma_scale_f32_16x16x128_f8f6f4 v[94:97], v[2:9], v[174:181], v[94:97], v234, v234 op_sel_hi:[0,0,0]
	v_mfma_scale_f32_16x16x128_f8f6f4 v[78:81], v[10:17], v[182:189], v[78:81], v234, v234 op_sel_hi:[0,0,0]
	v_mfma_scale_f32_16x16x128_f8f6f4 v[74:77], v[2:9], v[182:189], v[74:77], v234, v234 op_sel_hi:[0,0,0]
	v_mfma_scale_f32_16x16x128_f8f6f4 v[62:65], v[10:17], v[190:197], v[62:65], v234, v234 op_sel_hi:[0,0,0]
	v_mfma_scale_f32_16x16x128_f8f6f4 v[54:57], v[2:9], v[190:197], v[54:57], v234, v234 op_sel_hi:[0,0,0]
	v_mfma_scale_f32_16x16x128_f8f6f4 v[46:49], v[10:17], v[204:211], v[46:49], v234, v234 op_sel_hi:[0,0,0]
	v_mfma_scale_f32_16x16x128_f8f6f4 v[38:41], v[2:9], v[204:211], v[38:41], v234, v234 op_sel_hi:[0,0,0]
	s_setprio 0
	s_barrier
	s_add_i32 s62, s62, 2
	s_addk_i32 s28, 0x100
	s_addk_i32 s29, 0x100
	s_cmp_gt_u32 s62, 13
	s_cbranch_scc0 .LBB0_225
	s_branch .Lex_0
.Lfin_0:
	s_add_i32 s63, s29, 0xfffc0000
	s_mov_b32 m0, s79
	ds_read_b128 v[174:177], v171
	ds_read_b128 v[178:181], v171 offset:1024
	ds_read_b128 v[182:185], v171 offset:2048
	ds_read_b128 v[186:189], v171 offset:3072
	ds_read_b128 v[190:193], v171 offset:4096
	ds_read_b128 v[194:197], v171 offset:5120
	ds_read_b128 v[204:207], v171 offset:6144
	ds_read_b128 v[208:211], v171 offset:7168
	buffer_load_dwordx4 v163, s[64:67], s63 offen lds
	s_mov_b32 m0, s81
	s_nop 0
	buffer_load_dwordx4 v165, s[64:67], s63 offen lds
	s_mov_b32 m0, s80
	s_nop 0
	buffer_load_dwordx4 v163, s[64:67], s29 offen lds
	s_mov_b32 m0, s82
	s_nop 0
	buffer_load_dwordx4 v165, s[64:67], s29 offen lds
	s_waitcnt vmcnt(8)
	s_waitcnt lgkmcnt(0)
	s_barrier
	s_setprio 1
	s_waitcnt lgkmcnt(6)
	v_mfma_scale_f32_16x16x128_f8f6f4 v[150:153], v[2:9], v[174:181], v[150:153], v234, v234 op_sel_hi:[0,0,0]
	v_mfma_scale_f32_16x16x128_f8f6f4 v[146:149], v[10:17], v[174:181], v[146:149], v234, v234 op_sel_hi:[0,0,0]
	s_waitcnt lgkmcnt(4)
	v_mfma_scale_f32_16x16x128_f8f6f4 v[134:137], v[2:9], v[182:189], v[134:137], v234, v234 op_sel_hi:[0,0,0]
	v_mfma_scale_f32_16x16x128_f8f6f4 v[130:133], v[10:17], v[182:189], v[130:133], v234, v234 op_sel_hi:[0,0,0]
	s_waitcnt lgkmcnt(2)
	v_mfma_scale_f32_16x16x128_f8f6f4 v[118:121], v[2:9], v[190:197], v[118:121], v234, v234 op_sel_hi:[0,0,0]
	v_mfma_scale_f32_16x16x128_f8f6f4 v[114:117], v[10:17], v[190:197], v[114:117], v234, v234 op_sel_hi:[0,0,0]
	s_waitcnt lgkmcnt(0)
	v_mfma_scale_f32_16x16x128_f8f6f4 v[98:101], v[2:9], v[204:211], v[98:101], v234, v234 op_sel_hi:[0,0,0]
	v_mfma_scale_f32_16x16x128_f8f6f4 v[90:93], v[10:17], v[204:211], v[90:93], v234, v234 op_sel_hi:[0,0,0]
	v_mfma_scale_f32_16x16x128_f8f6f4 v[158:161], v[18:25], v[174:181], v[158:161], v234, v234 op_sel_hi:[0,0,0]
	v_mfma_scale_f32_16x16x128_f8f6f4 v[154:157], v[26:33], v[174:181], v[154:157], v234, v234 op_sel_hi:[0,0,0]
	v_mfma_scale_f32_16x16x128_f8f6f4 v[142:145], v[18:25], v[182:189], v[142:145], v234, v234 op_sel_hi:[0,0,0]
	v_mfma_scale_f32_16x16x128_f8f6f4 v[138:141], v[26:33], v[182:189], v[138:141], v234, v234 op_sel_hi:[0,0,0]
	v_mfma_scale_f32_16x16x128_f8f6f4 v[126:129], v[18:25], v[190:197], v[126:129], v234, v234 op_sel_hi:[0,0,0]
	v_mfma_scale_f32_16x16x128_f8f6f4 v[122:125], v[26:33], v[190:197], v[122:125], v234, v234 op_sel_hi:[0,0,0]
	v_mfma_scale_f32_16x16x128_f8f6f4 v[110:113], v[18:25], v[204:211], v[110:113], v234, v234 op_sel_hi:[0,0,0]
	v_mfma_scale_f32_16x16x128_f8f6f4 v[106:109], v[26:33], v[204:211], v[106:109], v234, v234 op_sel_hi:[0,0,0]
	s_setprio 0
	s_barrier
	s_mov_b32 m0, s9
	ds_read_b128 v[174:177], v171 offset:16384
	ds_read_b128 v[178:181], v171 offset:17408
	ds_read_b128 v[182:185], v171 offset:18432
	ds_read_b128 v[186:189], v171 offset:19456
	ds_read_b128 v[190:193], v171 offset:20480
	ds_read_b128 v[194:197], v171 offset:21504
	ds_read_b128 v[204:207], v171 offset:22528
	ds_read_b128 v[208:211], v171 offset:23552
	s_mov_b32 m0, s10
	s_add_i32 s63, s14, 0x40000
	s_mov_b32 m0, s11
	s_nop 0
	s_mov_b32 m0, s12
	s_nop 0
	s_waitcnt vmcnt(0)
	s_waitcnt lgkmcnt(0)
	s_barrier
	s_setprio 1
	s_waitcnt lgkmcnt(6)
	v_mfma_scale_f32_16x16x128_f8f6f4 v[86:89], v[2:9], v[174:181], v[86:89], v234, v234 op_sel_hi:[0,0,0]
	v_mfma_scale_f32_16x16x128_f8f6f4 v[82:85], v[10:17], v[174:181], v[82:85], v234, v234 op_sel_hi:[0,0,0]
	s_waitcnt lgkmcnt(4)
	v_mfma_scale_f32_16x16x128_f8f6f4 v[70:73], v[2:9], v[182:189], v[70:73], v234, v234 op_sel_hi:[0,0,0]
	v_mfma_scale_f32_16x16x128_f8f6f4 v[66:69], v[10:17], v[182:189], v[66:69], v234, v234 op_sel_hi:[0,0,0]
	s_waitcnt lgkmcnt(2)
	v_mfma_scale_f32_16x16x128_f8f6f4 v[58:61], v[2:9], v[190:197], v[58:61], v234, v234 op_sel_hi:[0,0,0]
	v_mfma_scale_f32_16x16x128_f8f6f4 v[50:53], v[10:17], v[190:197], v[50:53], v234, v234 op_sel_hi:[0,0,0]
	s_waitcnt lgkmcnt(0)
	v_mfma_scale_f32_16x16x128_f8f6f4 v[42:45], v[2:9], v[204:211], v[42:45], v234, v234 op_sel_hi:[0,0,0]
	v_mfma_scale_f32_16x16x128_f8f6f4 v[34:37], v[10:17], v[204:211], v[34:37], v234, v234 op_sel_hi:[0,0,0]
	v_mfma_scale_f32_16x16x128_f8f6f4 v[102:105], v[18:25], v[174:181], v[102:105], v234, v234 op_sel_hi:[0,0,0]
	v_mfma_scale_f32_16x16x128_f8f6f4 v[94:97], v[26:33], v[174:181], v[94:97], v234, v234 op_sel_hi:[0,0,0]
	v_mfma_scale_f32_16x16x128_f8f6f4 v[78:81], v[18:25], v[182:189], v[78:81], v234, v234 op_sel_hi:[0,0,0]
	v_mfma_scale_f32_16x16x128_f8f6f4 v[74:77], v[26:33], v[182:189], v[74:77], v234, v234 op_sel_hi:[0,0,0]
	v_mfma_scale_f32_16x16x128_f8f6f4 v[62:65], v[18:25], v[190:197], v[62:65], v234, v234 op_sel_hi:[0,0,0]
	v_mfma_scale_f32_16x16x128_f8f6f4 v[54:57], v[26:33], v[190:197], v[54:57], v234, v234 op_sel_hi:[0,0,0]
	v_mfma_scale_f32_16x16x128_f8f6f4 v[46:49], v[18:25], v[204:211], v[46:49], v234, v234 op_sel_hi:[0,0,0]
	v_mfma_scale_f32_16x16x128_f8f6f4 v[38:41], v[26:33], v[204:211], v[38:41], v234, v234 op_sel_hi:[0,0,0]
	s_setprio 0
	s_barrier
	ds_read_b128 v[18:21], v172
	ds_read_b128 v[22:25], v172 offset:1024
	ds_read_b128 v[26:29], v172 offset:2048
	ds_read_b128 v[30:33], v172 offset:3072
	ds_read_b128 v[10:13], v173
	ds_read_b128 v[14:17], v173 offset:1024
	ds_read_b128 v[2:5], v173 offset:2048
	ds_read_b128 v[6:9], v173 offset:3072
	s_mov_b32 m0, s8
	ds_read_b128 v[174:177], v171 offset:32768
	ds_read_b128 v[178:181], v171 offset:33792
	ds_read_b128 v[182:185], v171 offset:34816
	ds_read_b128 v[186:189], v171 offset:35840
	ds_read_b128 v[190:193], v171 offset:36864
	ds_read_b128 v[194:197], v171 offset:37888
	ds_read_b128 v[204:207], v171 offset:38912
	ds_read_b128 v[208:211], v171 offset:39936
	s_mov_b32 m0, s13
	s_nop 0
	s_add_i32 s15, s15, 0x40000
	s_mov_b32 m0, s20
	s_nop 0
	s_mov_b32 m0, s21
	s_nop 0
	s_waitcnt vmcnt(8)
	s_waitcnt lgkmcnt(0)
	s_barrier
	s_setprio 1
	s_waitcnt lgkmcnt(6)
	v_mfma_scale_f32_16x16x128_f8f6f4 v[150:153], v[18:25], v[174:181], v[150:153], v234, v234 op_sel_hi:[0,0,0]
	v_mfma_scale_f32_16x16x128_f8f6f4 v[146:149], v[26:33], v[174:181], v[146:149], v234, v234 op_sel_hi:[0,0,0]
	s_waitcnt lgkmcnt(4)
	v_mfma_scale_f32_16x16x128_f8f6f4 v[134:137], v[18:25], v[182:189], v[134:137], v234, v234 op_sel_hi:[0,0,0]
	v_mfma_scale_f32_16x16x128_f8f6f4 v[130:133], v[26:33], v[182:189], v[130:133], v234, v234 op_sel_hi:[0,0,0]
	s_waitcnt lgkmcnt(2)
	v_mfma_scale_f32_16x16x128_f8f6f4 v[118:121], v[18:25], v[190:197], v[118:121], v234, v234 op_sel_hi:[0,0,0]
	v_mfma_scale_f32_16x16x128_f8f6f4 v[114:117], v[26:33], v[190:197], v[114:117], v234, v234 op_sel_hi:[0,0,0]
	s_waitcnt lgkmcnt(0)
	v_mfma_scale_f32_16x16x128_f8f6f4 v[98:101], v[18:25], v[204:211], v[98:101], v234, v234 op_sel_hi:[0,0,0]
	v_mfma_scale_f32_16x16x128_f8f6f4 v[90:93], v[26:33], v[204:211], v[90:93], v234, v234 op_sel_hi:[0,0,0]
	v_mfma_scale_f32_16x16x128_f8f6f4 v[158:161], v[10:17], v[174:181], v[158:161], v234, v234 op_sel_hi:[0,0,0]
	v_mfma_scale_f32_16x16x128_f8f6f4 v[154:157], v[2:9], v[174:181], v[154:157], v234, v234 op_sel_hi:[0,0,0]
	v_mfma_scale_f32_16x16x128_f8f6f4 v[142:145], v[10:17], v[182:189], v[142:145], v234, v234 op_sel_hi:[0,0,0]
	v_mfma_scale_f32_16x16x128_f8f6f4 v[138:141], v[2:9], v[182:189], v[138:141], v234, v234 op_sel_hi:[0,0,0]
	v_mfma_scale_f32_16x16x128_f8f6f4 v[126:129], v[10:17], v[190:197], v[126:129], v234, v234 op_sel_hi:[0,0,0]
	v_mfma_scale_f32_16x16x128_f8f6f4 v[122:125], v[2:9], v[190:197], v[122:125], v234, v234 op_sel_hi:[0,0,0]
	v_mfma_scale_f32_16x16x128_f8f6f4 v[110:113], v[10:17], v[204:211], v[110:113], v234, v234 op_sel_hi:[0,0,0]
	v_mfma_scale_f32_16x16x128_f8f6f4 v[106:109], v[2:9], v[204:211], v[106:109], v234, v234 op_sel_hi:[0,0,0]
	s_setprio 0
	s_barrier
	s_mov_b32 m0, s26
	s_or_b32 s15, s14, 0x80
	ds_read_b128 v[174:177], v171 offset:49152
	ds_read_b128 v[178:181], v171 offset:50176
	ds_read_b128 v[182:185], v171 offset:51200
	ds_read_b128 v[186:189], v171 offset:52224
	ds_read_b128 v[190:193], v171 offset:53248
	ds_read_b128 v[194:197], v171 offset:54272
	ds_read_b128 v[204:207], v171 offset:55296
	ds_read_b128 v[208:211], v171 offset:56320
	s_mov_b32 m0, s27
	s_add_i32 s14, s14, 0x40080
	s_mov_b32 m0, s40
	s_nop 0
	s_mov_b32 m0, s76
	s_nop 0
	s_waitcnt vmcnt(6)
	s_waitcnt lgkmcnt(0)
	s_barrier
	s_setprio 1
	s_waitcnt lgkmcnt(6)
	v_mfma_scale_f32_16x16x128_f8f6f4 v[86:89], v[18:25], v[174:181], v[86:89], v234, v234 op_sel_hi:[0,0,0]
	v_mfma_scale_f32_16x16x128_f8f6f4 v[82:85], v[26:33], v[174:181], v[82:85], v234, v234 op_sel_hi:[0,0,0]
	s_waitcnt lgkmcnt(4)
	v_mfma_scale_f32_16x16x128_f8f6f4 v[70:73], v[18:25], v[182:189], v[70:73], v234, v234 op_sel_hi:[0,0,0]
	v_mfma_scale_f32_16x16x128_f8f6f4 v[66:69], v[26:33], v[182:189], v[66:69], v234, v234 op_sel_hi:[0,0,0]
	s_waitcnt lgkmcnt(2)
	v_mfma_scale_f32_16x16x128_f8f6f4 v[58:61], v[18:25], v[190:197], v[58:61], v234, v234 op_sel_hi:[0,0,0]
	v_mfma_scale_f32_16x16x128_f8f6f4 v[50:53], v[26:33], v[190:197], v[50:53], v234, v234 op_sel_hi:[0,0,0]
	s_waitcnt lgkmcnt(0)
	v_mfma_scale_f32_16x16x128_f8f6f4 v[42:45], v[18:25], v[204:211], v[42:45], v234, v234 op_sel_hi:[0,0,0]
	v_mfma_scale_f32_16x16x128_f8f6f4 v[34:37], v[26:33], v[204:211], v[34:37], v234, v234 op_sel_hi:[0,0,0]
	v_mfma_scale_f32_16x16x128_f8f6f4 v[102:105], v[10:17], v[174:181], v[102:105], v234, v234 op_sel_hi:[0,0,0]
	v_mfma_scale_f32_16x16x128_f8f6f4 v[94:97], v[2:9], v[174:181], v[94:97], v234, v234 op_sel_hi:[0,0,0]
	v_mfma_scale_f32_16x16x128_f8f6f4 v[78:81], v[10:17], v[182:189], v[78:81], v234, v234 op_sel_hi:[0,0,0]
	v_mfma_scale_f32_16x16x128_f8f6f4 v[74:77], v[2:9], v[182:189], v[74:77], v234, v234 op_sel_hi:[0,0,0]
	v_mfma_scale_f32_16x16x128_f8f6f4 v[62:65], v[10:17], v[190:197], v[62:65], v234, v234 op_sel_hi:[0,0,0]
	v_mfma_scale_f32_16x16x128_f8f6f4 v[54:57], v[2:9], v[190:197], v[54:57], v234, v234 op_sel_hi:[0,0,0]
	v_mfma_scale_f32_16x16x128_f8f6f4 v[46:49], v[10:17], v[204:211], v[46:49], v234, v234 op_sel_hi:[0,0,0]
	v_mfma_scale_f32_16x16x128_f8f6f4 v[38:41], v[2:9], v[204:211], v[38:41], v234, v234 op_sel_hi:[0,0,0]
	s_setprio 0
	s_barrier
	s_add_i32 s62, s62, 2
	s_addk_i32 s28, 0x100
	s_addk_i32 s29, 0x100
	s_cmp_gt_u32 s62, 13
.Lex_0:
	s_nop 15
	s_nop 15
	s_and_b64 vcc, exec, s[36:37]
	s_cbranch_vccz .LBB0_228
	s_barrier

.LBB0_243:
	ds_read_b128 v[142:145], v130
	ds_read_b128 v[146:149], v130 offset:1024
	ds_read_b128 v[150:153], v130 offset:2048
	ds_read_b128 v[154:157], v130 offset:3072
	ds_read_b128 v[158:161], v131
	ds_read_b128 v[162:165], v131 offset:1024
	ds_read_b128 v[166:169], v131 offset:2048
	ds_read_b128 v[170:173], v131 offset:3072
	s_add_i32 s52, s15, 0xfff80080
	s_cmp_eq_u32 s43, 28
	s_cselect_b32 s62, s29, s14
	s_cselect_b32 s52, s28, s52
	s_cbranch_scc0 .Lnx_1
	s_cmp_eq_u64 s[36:37], 0
	s_cbranch_scc1 .Lfin_1
.Lnx_1:
	s_add_i32 s63, s15, 0xfff80000
	s_mov_b32 m0, s38
	ds_read_b128 v[174:177], v141
	ds_read_b128 v[178:181], v141 offset:1024
	ds_read_b128 v[182:185], v141 offset:2048
	ds_read_b128 v[186:189], v141 offset:3072
	ds_read_b128 v[190:193], v141 offset:4096
	ds_read_b128 v[194:197], v141 offset:5120
	ds_read_b128 v[198:201], v141 offset:6144
	ds_read_b128 v[204:207], v141 offset:7168
	buffer_load_dwordx4 v134, s[64:67], s63 offen lds
	s_mov_b32 m0, s10
	s_nop 0
	buffer_load_dwordx4 v136, s[64:67], s63 offen lds
	s_mov_b32 m0, s11
	s_nop 0
	buffer_load_dwordx4 v134, s[64:67], s15 offen lds
	s_mov_b32 m0, s13
	s_nop 0
	buffer_load_dwordx4 v136, s[64:67], s15 offen lds
	s_waitcnt vmcnt(8)
	s_waitcnt lgkmcnt(0)
	s_barrier
	s_setprio 1
	s_waitcnt lgkmcnt(7)
	v_mfma_f32_16x16x32_bf16 v[122:125], v[142:145], v[174:177], v[122:125]
	v_mfma_f32_16x16x32_bf16 v[114:117], v[150:153], v[174:177], v[114:117]
	s_waitcnt lgkmcnt(5)
	v_mfma_f32_16x16x32_bf16 v[106:109], v[142:145], v[182:185], v[106:109]
	v_mfma_f32_16x16x32_bf16 v[98:101], v[150:153], v[182:185], v[98:101]
	s_waitcnt lgkmcnt(3)
	v_mfma_f32_16x16x32_bf16 v[90:93], v[142:145], v[190:193], v[90:93]
	v_mfma_f32_16x16x32_bf16 v[82:85], v[150:153], v[190:193], v[82:85]
	s_waitcnt lgkmcnt(1)
	v_mfma_f32_16x16x32_bf16 v[74:77], v[142:145], v[198:201], v[74:77]
	v_mfma_f32_16x16x32_bf16 v[66:69], v[150:153], v[198:201], v[66:69]
	v_mfma_f32_16x16x32_bf16 v[126:129], v[158:161], v[174:177], v[126:129]
	v_mfma_f32_16x16x32_bf16 v[118:121], v[166:169], v[174:177], v[118:121]
	v_mfma_f32_16x16x32_bf16 v[110:113], v[158:161], v[182:185], v[110:113]
	v_mfma_f32_16x16x32_bf16 v[102:105], v[166:169], v[182:185], v[102:105]
	v_mfma_f32_16x16x32_bf16 v[94:97], v[158:161], v[190:193], v[94:97]
	v_mfma_f32_16x16x32_bf16 v[86:89], v[166:169], v[190:193], v[86:89]
	v_mfma_f32_16x16x32_bf16 v[78:81], v[158:161], v[198:201], v[78:81]
	v_mfma_f32_16x16x32_bf16 v[70:73], v[166:169], v[198:201], v[70:73]
	v_mfma_f32_16x16x32_bf16 v[122:125], v[146:149], v[178:181], v[122:125]
	v_mfma_f32_16x16x32_bf16 v[114:117], v[154:157], v[178:181], v[114:117]
	v_mfma_f32_16x16x32_bf16 v[106:109], v[146:149], v[186:189], v[106:109]
	v_mfma_f32_16x16x32_bf16 v[98:101], v[154:157], v[186:189], v[98:101]
	v_mfma_f32_16x16x32_bf16 v[90:93], v[146:149], v[194:197], v[90:93]
	v_mfma_f32_16x16x32_bf16 v[82:85], v[154:157], v[194:197], v[82:85]
	s_waitcnt lgkmcnt(0)
	v_mfma_f32_16x16x32_bf16 v[74:77], v[146:149], v[204:207], v[74:77]
	v_mfma_f32_16x16x32_bf16 v[66:69], v[154:157], v[204:207], v[66:69]
	v_mfma_f32_16x16x32_bf16 v[126:129], v[162:165], v[178:181], v[126:129]
	v_mfma_f32_16x16x32_bf16 v[118:121], v[170:173], v[178:181], v[118:121]
	v_mfma_f32_16x16x32_bf16 v[110:113], v[162:165], v[186:189], v[110:113]
	v_mfma_f32_16x16x32_bf16 v[102:105], v[170:173], v[186:189], v[102:105]
	v_mfma_f32_16x16x32_bf16 v[94:97], v[162:165], v[194:197], v[94:97]
	v_mfma_f32_16x16x32_bf16 v[86:89], v[170:173], v[194:197], v[86:89]
	v_mfma_f32_16x16x32_bf16 v[78:81], v[162:165], v[204:207], v[78:81]
	v_mfma_f32_16x16x32_bf16 v[70:73], v[170:173], v[204:207], v[70:73]
	s_setprio 0
	s_barrier
	s_mov_b32 m0, s39
	ds_read_b128 v[174:177], v141 offset:16384
	ds_read_b128 v[178:181], v141 offset:17408
	ds_read_b128 v[182:185], v141 offset:18432
	ds_read_b128 v[186:189], v141 offset:19456
	ds_read_b128 v[190:193], v141 offset:20480
	ds_read_b128 v[194:197], v141 offset:21504
	ds_read_b128 v[198:201], v141 offset:22528
	ds_read_b128 v[204:207], v141 offset:23552
	buffer_load_dwordx4 v135, s[0:3], s62 offen lds
	s_mov_b32 m0, s76
	s_add_i32 s63, s62, 0x80000
	buffer_load_dwordx4 v137, s[0:3], s62 offen lds
	s_mov_b32 m0, s77
	s_nop 0
	buffer_load_dwordx4 v135, s[0:3], s63 offen lds
	s_mov_b32 m0, s78
	s_nop 0
	buffer_load_dwordx4 v137, s[0:3], s63 offen lds
	s_waitcnt vmcnt(6)
	s_waitcnt lgkmcnt(0)
	s_barrier
	s_setprio 1
	s_waitcnt lgkmcnt(7)
	v_mfma_f32_16x16x32_bf16 v[58:61], v[142:145], v[174:177], v[58:61]
	v_mfma_f32_16x16x32_bf16 v[50:53], v[150:153], v[174:177], v[50:53]
	s_waitcnt lgkmcnt(5)
	v_mfma_f32_16x16x32_bf16 v[42:45], v[142:145], v[182:185], v[42:45]
	v_mfma_f32_16x16x32_bf16 v[34:37], v[150:153], v[182:185], v[34:37]
	s_waitcnt lgkmcnt(3)
	v_mfma_f32_16x16x32_bf16 v[26:29], v[142:145], v[190:193], v[26:29]
	v_mfma_f32_16x16x32_bf16 v[18:21], v[150:153], v[190:193], v[18:21]
	s_waitcnt lgkmcnt(1)
	v_mfma_f32_16x16x32_bf16 v[10:13], v[142:145], v[198:201], v[10:13]
	v_mfma_f32_16x16x32_bf16 v[2:5], v[150:153], v[198:201], v[2:5]
	v_mfma_f32_16x16x32_bf16 v[62:65], v[158:161], v[174:177], v[62:65]
	v_mfma_f32_16x16x32_bf16 v[54:57], v[166:169], v[174:177], v[54:57]
	v_mfma_f32_16x16x32_bf16 v[46:49], v[158:161], v[182:185], v[46:49]
	v_mfma_f32_16x16x32_bf16 v[38:41], v[166:169], v[182:185], v[38:41]
	v_mfma_f32_16x16x32_bf16 v[30:33], v[158:161], v[190:193], v[30:33]
	v_mfma_f32_16x16x32_bf16 v[22:25], v[166:169], v[190:193], v[22:25]
	v_mfma_f32_16x16x32_bf16 v[14:17], v[158:161], v[198:201], v[14:17]
	v_mfma_f32_16x16x32_bf16 v[6:9], v[166:169], v[198:201], v[6:9]
	v_mfma_f32_16x16x32_bf16 v[58:61], v[146:149], v[178:181], v[58:61]
	v_mfma_f32_16x16x32_bf16 v[50:53], v[154:157], v[178:181], v[50:53]
	v_mfma_f32_16x16x32_bf16 v[42:45], v[146:149], v[186:189], v[42:45]
	v_mfma_f32_16x16x32_bf16 v[34:37], v[154:157], v[186:189], v[34:37]
	v_mfma_f32_16x16x32_bf16 v[26:29], v[146:149], v[194:197], v[26:29]
	v_mfma_f32_16x16x32_bf16 v[18:21], v[154:157], v[194:197], v[18:21]
	s_waitcnt lgkmcnt(0)
	v_mfma_f32_16x16x32_bf16 v[10:13], v[146:149], v[204:207], v[10:13]
	v_mfma_f32_16x16x32_bf16 v[2:5], v[154:157], v[204:207], v[2:5]
	v_mfma_f32_16x16x32_bf16 v[62:65], v[162:165], v[178:181], v[62:65]
	v_mfma_f32_16x16x32_bf16 v[54:57], v[170:173], v[178:181], v[54:57]
	v_mfma_f32_16x16x32_bf16 v[46:49], v[162:165], v[186:189], v[46:49]
	v_mfma_f32_16x16x32_bf16 v[38:41], v[170:173], v[186:189], v[38:41]
	v_mfma_f32_16x16x32_bf16 v[30:33], v[162:165], v[194:197], v[30:33]
	v_mfma_f32_16x16x32_bf16 v[22:25], v[170:173], v[194:197], v[22:25]
	v_mfma_f32_16x16x32_bf16 v[14:17], v[162:165], v[204:207], v[14:17]
	v_mfma_f32_16x16x32_bf16 v[6:9], v[170:173], v[204:207], v[6:9]
	s_setprio 0
	s_barrier
	ds_read_b128 v[142:145], v132
	ds_read_b128 v[146:149], v132 offset:1024
	ds_read_b128 v[150:153], v132 offset:2048
	ds_read_b128 v[154:157], v132 offset:3072
	ds_read_b128 v[158:161], v133
	ds_read_b128 v[162:165], v133 offset:1024
	ds_read_b128 v[166:169], v133 offset:2048
	ds_read_b128 v[170:173], v133 offset:3072
	s_mov_b32 m0, s12
	ds_read_b128 v[174:177], v141 offset:32768
	ds_read_b128 v[178:181], v141 offset:33792
	ds_read_b128 v[182:185], v141 offset:34816
	ds_read_b128 v[186:189], v141 offset:35840
	ds_read_b128 v[190:193], v141 offset:36864
	ds_read_b128 v[194:197], v141 offset:37888
	ds_read_b128 v[198:201], v141 offset:38912
	ds_read_b128 v[204:207], v141 offset:39936
	buffer_load_dwordx4 v134, s[64:67], s52 offen lds
	s_mov_b32 m0, s79
	s_nop 0
	buffer_load_dwordx4 v136, s[64:67], s52 offen lds
	s_add_i32 s52, s52, 0x80000
	s_mov_b32 m0, s80
	s_nop 0
	buffer_load_dwordx4 v134, s[64:67], s52 offen lds
	s_mov_b32 m0, s81
	s_nop 0
	buffer_load_dwordx4 v136, s[64:67], s52 offen lds
	s_waitcnt vmcnt(8)
	s_waitcnt lgkmcnt(0)
	s_barrier
	s_setprio 1
	s_waitcnt lgkmcnt(7)
	v_mfma_f32_16x16x32_bf16 v[122:125], v[142:145], v[174:177], v[122:125]
	v_mfma_f32_16x16x32_bf16 v[114:117], v[150:153], v[174:177], v[114:117]
	s_waitcnt lgkmcnt(5)
	v_mfma_f32_16x16x32_bf16 v[106:109], v[142:145], v[182:185], v[106:109]
	v_mfma_f32_16x16x32_bf16 v[98:101], v[150:153], v[182:185], v[98:101]
	s_waitcnt lgkmcnt(3)
	v_mfma_f32_16x16x32_bf16 v[90:93], v[142:145], v[190:193], v[90:93]
	v_mfma_f32_16x16x32_bf16 v[82:85], v[150:153], v[190:193], v[82:85]
	s_waitcnt lgkmcnt(1)
	v_mfma_f32_16x16x32_bf16 v[74:77], v[142:145], v[198:201], v[74:77]
	v_mfma_f32_16x16x32_bf16 v[66:69], v[150:153], v[198:201], v[66:69]
	v_mfma_f32_16x16x32_bf16 v[126:129], v[158:161], v[174:177], v[126:129]
	v_mfma_f32_16x16x32_bf16 v[118:121], v[166:169], v[174:177], v[118:121]
	v_mfma_f32_16x16x32_bf16 v[110:113], v[158:161], v[182:185], v[110:113]
	v_mfma_f32_16x16x32_bf16 v[102:105], v[166:169], v[182:185], v[102:105]
	v_mfma_f32_16x16x32_bf16 v[94:97], v[158:161], v[190:193], v[94:97]
	v_mfma_f32_16x16x32_bf16 v[86:89], v[166:169], v[190:193], v[86:89]
	v_mfma_f32_16x16x32_bf16 v[78:81], v[158:161], v[198:201], v[78:81]
	v_mfma_f32_16x16x32_bf16 v[70:73], v[166:169], v[198:201], v[70:73]
	v_mfma_f32_16x16x32_bf16 v[122:125], v[146:149], v[178:181], v[122:125]
	v_mfma_f32_16x16x32_bf16 v[114:117], v[154:157], v[178:181], v[114:117]
	v_mfma_f32_16x16x32_bf16 v[106:109], v[146:149], v[186:189], v[106:109]
	v_mfma_f32_16x16x32_bf16 v[98:101], v[154:157], v[186:189], v[98:101]
	v_mfma_f32_16x16x32_bf16 v[90:93], v[146:149], v[194:197], v[90:93]
	v_mfma_f32_16x16x32_bf16 v[82:85], v[154:157], v[194:197], v[82:85]
	s_waitcnt lgkmcnt(0)
	v_mfma_f32_16x16x32_bf16 v[74:77], v[146:149], v[204:207], v[74:77]
	v_mfma_f32_16x16x32_bf16 v[66:69], v[154:157], v[204:207], v[66:69]
	v_mfma_f32_16x16x32_bf16 v[126:129], v[162:165], v[178:181], v[126:129]
	v_mfma_f32_16x16x32_bf16 v[118:121], v[170:173], v[178:181], v[118:121]
	v_mfma_f32_16x16x32_bf16 v[110:113], v[162:165], v[186:189], v[110:113]
	v_mfma_f32_16x16x32_bf16 v[102:105], v[170:173], v[186:189], v[102:105]
	v_mfma_f32_16x16x32_bf16 v[94:97], v[162:165], v[194:197], v[94:97]
	v_mfma_f32_16x16x32_bf16 v[86:89], v[170:173], v[194:197], v[86:89]
	v_mfma_f32_16x16x32_bf16 v[78:81], v[162:165], v[204:207], v[78:81]
	v_mfma_f32_16x16x32_bf16 v[70:73], v[170:173], v[204:207], v[70:73]
	s_setprio 0
	s_barrier
	s_mov_b32 m0, s82
	s_or_b32 s52, s62, 0x80
	ds_read_b128 v[174:177], v141 offset:49152
	ds_read_b128 v[178:181], v141 offset:50176
	ds_read_b128 v[182:185], v141 offset:51200
	ds_read_b128 v[186:189], v141 offset:52224
	ds_read_b128 v[190:193], v141 offset:53248
	ds_read_b128 v[194:197], v141 offset:54272
	ds_read_b128 v[198:201], v141 offset:55296
	ds_read_b128 v[204:207], v141 offset:56320
	buffer_load_dwordx4 v135, s[0:3], s52 offen lds
	s_mov_b32 m0, s83
	s_add_i32 s62, s62, 0x80080
	buffer_load_dwordx4 v137, s[0:3], s52 offen lds
	s_mov_b32 m0, s84
	s_nop 0
	buffer_load_dwordx4 v135, s[0:3], s62 offen lds
	s_mov_b32 m0, s85
	s_nop 0
	buffer_load_dwordx4 v137, s[0:3], s62 offen lds
	s_waitcnt vmcnt(6)
	s_waitcnt lgkmcnt(0)
	s_barrier
	s_setprio 1
	s_waitcnt lgkmcnt(7)
	v_mfma_f32_16x16x32_bf16 v[58:61], v[142:145], v[174:177], v[58:61]
	v_mfma_f32_16x16x32_bf16 v[50:53], v[150:153], v[174:177], v[50:53]
	s_waitcnt lgkmcnt(5)
	v_mfma_f32_16x16x32_bf16 v[42:45], v[142:145], v[182:185], v[42:45]
	v_mfma_f32_16x16x32_bf16 v[34:37], v[150:153], v[182:185], v[34:37]
	s_waitcnt lgkmcnt(3)
	v_mfma_f32_16x16x32_bf16 v[26:29], v[142:145], v[190:193], v[26:29]
	v_mfma_f32_16x16x32_bf16 v[18:21], v[150:153], v[190:193], v[18:21]
	s_waitcnt lgkmcnt(1)
	v_mfma_f32_16x16x32_bf16 v[10:13], v[142:145], v[198:201], v[10:13]
	v_mfma_f32_16x16x32_bf16 v[2:5], v[150:153], v[198:201], v[2:5]
	v_mfma_f32_16x16x32_bf16 v[62:65], v[158:161], v[174:177], v[62:65]
	v_mfma_f32_16x16x32_bf16 v[54:57], v[166:169], v[174:177], v[54:57]
	v_mfma_f32_16x16x32_bf16 v[46:49], v[158:161], v[182:185], v[46:49]
	v_mfma_f32_16x16x32_bf16 v[38:41], v[166:169], v[182:185], v[38:41]
	v_mfma_f32_16x16x32_bf16 v[30:33], v[158:161], v[190:193], v[30:33]
	v_mfma_f32_16x16x32_bf16 v[22:25], v[166:169], v[190:193], v[22:25]
	v_mfma_f32_16x16x32_bf16 v[14:17], v[158:161], v[198:201], v[14:17]
	v_mfma_f32_16x16x32_bf16 v[6:9], v[166:169], v[198:201], v[6:9]
	v_mfma_f32_16x16x32_bf16 v[58:61], v[146:149], v[178:181], v[58:61]
	v_mfma_f32_16x16x32_bf16 v[50:53], v[154:157], v[178:181], v[50:53]
	v_mfma_f32_16x16x32_bf16 v[42:45], v[146:149], v[186:189], v[42:45]
	v_mfma_f32_16x16x32_bf16 v[34:37], v[154:157], v[186:189], v[34:37]
	v_mfma_f32_16x16x32_bf16 v[26:29], v[146:149], v[194:197], v[26:29]
	v_mfma_f32_16x16x32_bf16 v[18:21], v[154:157], v[194:197], v[18:21]
	s_waitcnt lgkmcnt(0)
	v_mfma_f32_16x16x32_bf16 v[10:13], v[146:149], v[204:207], v[10:13]
	v_mfma_f32_16x16x32_bf16 v[2:5], v[154:157], v[204:207], v[2:5]
	v_mfma_f32_16x16x32_bf16 v[62:65], v[162:165], v[178:181], v[62:65]
	v_mfma_f32_16x16x32_bf16 v[54:57], v[170:173], v[178:181], v[54:57]
	v_mfma_f32_16x16x32_bf16 v[46:49], v[162:165], v[186:189], v[46:49]
	v_mfma_f32_16x16x32_bf16 v[38:41], v[170:173], v[186:189], v[38:41]
	v_mfma_f32_16x16x32_bf16 v[30:33], v[162:165], v[194:197], v[30:33]
	v_mfma_f32_16x16x32_bf16 v[22:25], v[170:173], v[194:197], v[22:25]
	v_mfma_f32_16x16x32_bf16 v[14:17], v[162:165], v[204:207], v[14:17]
	v_mfma_f32_16x16x32_bf16 v[6:9], v[170:173], v[204:207], v[6:9]
	s_setprio 0
	s_barrier
	s_add_i32 s43, s43, 2
	s_addk_i32 s14, 0x100
	s_addk_i32 s15, 0x100
	s_cmp_gt_u32 s43, 29
	s_cbranch_scc0 .LBB0_243
	s_branch .Lex_1
.Lfin_1:
	s_add_i32 s63, s15, 0xfff80000
	s_mov_b32 m0, s38
	ds_read_b128 v[174:177], v141
	ds_read_b128 v[178:181], v141 offset:1024
	ds_read_b128 v[182:185], v141 offset:2048
	ds_read_b128 v[186:189], v141 offset:3072
	ds_read_b128 v[190:193], v141 offset:4096
	ds_read_b128 v[194:197], v141 offset:5120
	ds_read_b128 v[198:201], v141 offset:6144
	ds_read_b128 v[204:207], v141 offset:7168
	buffer_load_dwordx4 v134, s[64:67], s63 offen lds
	s_mov_b32 m0, s10
	s_nop 0
	buffer_load_dwordx4 v136, s[64:67], s63 offen lds
	s_mov_b32 m0, s11
	s_nop 0
	buffer_load_dwordx4 v134, s[64:67], s15 offen lds
	s_mov_b32 m0, s13
	s_nop 0
	buffer_load_dwordx4 v136, s[64:67], s15 offen lds
	s_waitcnt vmcnt(8)
	s_waitcnt lgkmcnt(0)
	s_barrier
	s_setprio 1
	s_waitcnt lgkmcnt(7)
	v_mfma_f32_16x16x32_bf16 v[122:125], v[142:145], v[174:177], v[122:125]
	v_mfma_f32_16x16x32_bf16 v[114:117], v[150:153], v[174:177], v[114:117]
	s_waitcnt lgkmcnt(5)
	v_mfma_f32_16x16x32_bf16 v[106:109], v[142:145], v[182:185], v[106:109]
	v_mfma_f32_16x16x32_bf16 v[98:101], v[150:153], v[182:185], v[98:101]
	s_waitcnt lgkmcnt(3)
	v_mfma_f32_16x16x32_bf16 v[90:93], v[142:145], v[190:193], v[90:93]
	v_mfma_f32_16x16x32_bf16 v[82:85], v[150:153], v[190:193], v[82:85]
	s_waitcnt lgkmcnt(1)
	v_mfma_f32_16x16x32_bf16 v[74:77], v[142:145], v[198:201], v[74:77]
	v_mfma_f32_16x16x32_bf16 v[66:69], v[150:153], v[198:201], v[66:69]
	v_mfma_f32_16x16x32_bf16 v[126:129], v[158:161], v[174:177], v[126:129]
	v_mfma_f32_16x16x32_bf16 v[118:121], v[166:169], v[174:177], v[118:121]
	v_mfma_f32_16x16x32_bf16 v[110:113], v[158:161], v[182:185], v[110:113]
	v_mfma_f32_16x16x32_bf16 v[102:105], v[166:169], v[182:185], v[102:105]
	v_mfma_f32_16x16x32_bf16 v[94:97], v[158:161], v[190:193], v[94:97]
	v_mfma_f32_16x16x32_bf16 v[86:89], v[166:169], v[190:193], v[86:89]
	v_mfma_f32_16x16x32_bf16 v[78:81], v[158:161], v[198:201], v[78:81]
	v_mfma_f32_16x16x32_bf16 v[70:73], v[166:169], v[198:201], v[70:73]
	v_mfma_f32_16x16x32_bf16 v[122:125], v[146:149], v[178:181], v[122:125]
	v_mfma_f32_16x16x32_bf16 v[114:117], v[154:157], v[178:181], v[114:117]
	v_mfma_f32_16x16x32_bf16 v[106:109], v[146:149], v[186:189], v[106:109]
	v_mfma_f32_16x16x32_bf16 v[98:101], v[154:157], v[186:189], v[98:101]
	v_mfma_f32_16x16x32_bf16 v[90:93], v[146:149], v[194:197], v[90:93]
	v_mfma_f32_16x16x32_bf16 v[82:85], v[154:157], v[194:197], v[82:85]
	s_waitcnt lgkmcnt(0)
	v_mfma_f32_16x16x32_bf16 v[74:77], v[146:149], v[204:207], v[74:77]
	v_mfma_f32_16x16x32_bf16 v[66:69], v[154:157], v[204:207], v[66:69]
	v_mfma_f32_16x16x32_bf16 v[126:129], v[162:165], v[178:181], v[126:129]
	v_mfma_f32_16x16x32_bf16 v[118:121], v[170:173], v[178:181], v[118:121]
	v_mfma_f32_16x16x32_bf16 v[110:113], v[162:165], v[186:189], v[110:113]
	v_mfma_f32_16x16x32_bf16 v[102:105], v[170:173], v[186:189], v[102:105]
	v_mfma_f32_16x16x32_bf16 v[94:97], v[162:165], v[194:197], v[94:97]
	v_mfma_f32_16x16x32_bf16 v[86:89], v[170:173], v[194:197], v[86:89]
	v_mfma_f32_16x16x32_bf16 v[78:81], v[162:165], v[204:207], v[78:81]
	v_mfma_f32_16x16x32_bf16 v[70:73], v[170:173], v[204:207], v[70:73]
	s_setprio 0
	s_barrier
	s_mov_b32 m0, s39
	ds_read_b128 v[174:177], v141 offset:16384
	ds_read_b128 v[178:181], v141 offset:17408
	ds_read_b128 v[182:185], v141 offset:18432
	ds_read_b128 v[186:189], v141 offset:19456
	ds_read_b128 v[190:193], v141 offset:20480
	ds_read_b128 v[194:197], v141 offset:21504
	ds_read_b128 v[198:201], v141 offset:22528
	ds_read_b128 v[204:207], v141 offset:23552
	s_mov_b32 m0, s76
	s_add_i32 s63, s62, 0x80000
	s_mov_b32 m0, s77
	s_nop 0
	s_mov_b32 m0, s78
	s_nop 0
	s_waitcnt vmcnt(0)
	s_waitcnt lgkmcnt(0)
	s_barrier
	s_setprio 1
	s_waitcnt lgkmcnt(7)
	v_mfma_f32_16x16x32_bf16 v[58:61], v[142:145], v[174:177], v[58:61]
	v_mfma_f32_16x16x32_bf16 v[50:53], v[150:153], v[174:177], v[50:53]
	s_waitcnt lgkmcnt(5)
	v_mfma_f32_16x16x32_bf16 v[42:45], v[142:145], v[182:185], v[42:45]
	v_mfma_f32_16x16x32_bf16 v[34:37], v[150:153], v[182:185], v[34:37]
	s_waitcnt lgkmcnt(3)
	v_mfma_f32_16x16x32_bf16 v[26:29], v[142:145], v[190:193], v[26:29]
	v_mfma_f32_16x16x32_bf16 v[18:21], v[150:153], v[190:193], v[18:21]
	s_waitcnt lgkmcnt(1)
	v_mfma_f32_16x16x32_bf16 v[10:13], v[142:145], v[198:201], v[10:13]
	v_mfma_f32_16x16x32_bf16 v[2:5], v[150:153], v[198:201], v[2:5]
	v_mfma_f32_16x16x32_bf16 v[62:65], v[158:161], v[174:177], v[62:65]
	v_mfma_f32_16x16x32_bf16 v[54:57], v[166:169], v[174:177], v[54:57]
	v_mfma_f32_16x16x32_bf16 v[46:49], v[158:161], v[182:185], v[46:49]
	v_mfma_f32_16x16x32_bf16 v[38:41], v[166:169], v[182:185], v[38:41]
	v_mfma_f32_16x16x32_bf16 v[30:33], v[158:161], v[190:193], v[30:33]
	v_mfma_f32_16x16x32_bf16 v[22:25], v[166:169], v[190:193], v[22:25]
	v_mfma_f32_16x16x32_bf16 v[14:17], v[158:161], v[198:201], v[14:17]
	v_mfma_f32_16x16x32_bf16 v[6:9], v[166:169], v[198:201], v[6:9]
	v_mfma_f32_16x16x32_bf16 v[58:61], v[146:149], v[178:181], v[58:61]
	v_mfma_f32_16x16x32_bf16 v[50:53], v[154:157], v[178:181], v[50:53]
	v_mfma_f32_16x16x32_bf16 v[42:45], v[146:149], v[186:189], v[42:45]
	v_mfma_f32_16x16x32_bf16 v[34:37], v[154:157], v[186:189], v[34:37]
	v_mfma_f32_16x16x32_bf16 v[26:29], v[146:149], v[194:197], v[26:29]
	v_mfma_f32_16x16x32_bf16 v[18:21], v[154:157], v[194:197], v[18:21]
	s_waitcnt lgkmcnt(0)
	v_mfma_f32_16x16x32_bf16 v[10:13], v[146:149], v[204:207], v[10:13]
	v_mfma_f32_16x16x32_bf16 v[2:5], v[154:157], v[204:207], v[2:5]
	v_mfma_f32_16x16x32_bf16 v[62:65], v[162:165], v[178:181], v[62:65]
	v_mfma_f32_16x16x32_bf16 v[54:57], v[170:173], v[178:181], v[54:57]
	v_mfma_f32_16x16x32_bf16 v[46:49], v[162:165], v[186:189], v[46:49]
	v_mfma_f32_16x16x32_bf16 v[38:41], v[170:173], v[186:189], v[38:41]
	v_mfma_f32_16x16x32_bf16 v[30:33], v[162:165], v[194:197], v[30:33]
	v_mfma_f32_16x16x32_bf16 v[22:25], v[170:173], v[194:197], v[22:25]
	v_mfma_f32_16x16x32_bf16 v[14:17], v[162:165], v[204:207], v[14:17]
	v_mfma_f32_16x16x32_bf16 v[6:9], v[170:173], v[204:207], v[6:9]
	s_setprio 0
	s_barrier
	ds_read_b128 v[142:145], v132
	ds_read_b128 v[146:149], v132 offset:1024
	ds_read_b128 v[150:153], v132 offset:2048
	ds_read_b128 v[154:157], v132 offset:3072
	ds_read_b128 v[158:161], v133
	ds_read_b128 v[162:165], v133 offset:1024
	ds_read_b128 v[166:169], v133 offset:2048
	ds_read_b128 v[170:173], v133 offset:3072
	s_mov_b32 m0, s12
	ds_read_b128 v[174:177], v141 offset:32768
	ds_read_b128 v[178:181], v141 offset:33792
	ds_read_b128 v[182:185], v141 offset:34816
	ds_read_b128 v[186:189], v141 offset:35840
	ds_read_b128 v[190:193], v141 offset:36864
	ds_read_b128 v[194:197], v141 offset:37888
	ds_read_b128 v[198:201], v141 offset:38912
	ds_read_b128 v[204:207], v141 offset:39936
	s_mov_b32 m0, s79
	s_nop 0
	s_add_i32 s52, s52, 0x80000
	s_mov_b32 m0, s80
	s_nop 0
	s_mov_b32 m0, s81
	s_nop 0
	s_waitcnt vmcnt(8)
	s_waitcnt lgkmcnt(0)
	s_barrier
	s_setprio 1
	s_waitcnt lgkmcnt(7)
	v_mfma_f32_16x16x32_bf16 v[122:125], v[142:145], v[174:177], v[122:125]
	v_mfma_f32_16x16x32_bf16 v[114:117], v[150:153], v[174:177], v[114:117]
	s_waitcnt lgkmcnt(5)
	v_mfma_f32_16x16x32_bf16 v[106:109], v[142:145], v[182:185], v[106:109]
	v_mfma_f32_16x16x32_bf16 v[98:101], v[150:153], v[182:185], v[98:101]
	s_waitcnt lgkmcnt(3)
	v_mfma_f32_16x16x32_bf16 v[90:93], v[142:145], v[190:193], v[90:93]
	v_mfma_f32_16x16x32_bf16 v[82:85], v[150:153], v[190:193], v[82:85]
	s_waitcnt lgkmcnt(1)
	v_mfma_f32_16x16x32_bf16 v[74:77], v[142:145], v[198:201], v[74:77]
	v_mfma_f32_16x16x32_bf16 v[66:69], v[150:153], v[198:201], v[66:69]
	v_mfma_f32_16x16x32_bf16 v[126:129], v[158:161], v[174:177], v[126:129]
	v_mfma_f32_16x16x32_bf16 v[118:121], v[166:169], v[174:177], v[118:121]
	v_mfma_f32_16x16x32_bf16 v[110:113], v[158:161], v[182:185], v[110:113]
	v_mfma_f32_16x16x32_bf16 v[102:105], v[166:169], v[182:185], v[102:105]
	v_mfma_f32_16x16x32_bf16 v[94:97], v[158:161], v[190:193], v[94:97]
	v_mfma_f32_16x16x32_bf16 v[86:89], v[166:169], v[190:193], v[86:89]
	v_mfma_f32_16x16x32_bf16 v[78:81], v[158:161], v[198:201], v[78:81]
	v_mfma_f32_16x16x32_bf16 v[70:73], v[166:169], v[198:201], v[70:73]
	v_mfma_f32_16x16x32_bf16 v[122:125], v[146:149], v[178:181], v[122:125]
	v_mfma_f32_16x16x32_bf16 v[114:117], v[154:157], v[178:181], v[114:117]
	v_mfma_f32_16x16x32_bf16 v[106:109], v[146:149], v[186:189], v[106:109]
	v_mfma_f32_16x16x32_bf16 v[98:101], v[154:157], v[186:189], v[98:101]
	v_mfma_f32_16x16x32_bf16 v[90:93], v[146:149], v[194:197], v[90:93]
	v_mfma_f32_16x16x32_bf16 v[82:85], v[154:157], v[194:197], v[82:85]
	s_waitcnt lgkmcnt(0)
	v_mfma_f32_16x16x32_bf16 v[74:77], v[146:149], v[204:207], v[74:77]
	v_mfma_f32_16x16x32_bf16 v[66:69], v[154:157], v[204:207], v[66:69]
	v_mfma_f32_16x16x32_bf16 v[126:129], v[162:165], v[178:181], v[126:129]
	v_mfma_f32_16x16x32_bf16 v[118:121], v[170:173], v[178:181], v[118:121]
	v_mfma_f32_16x16x32_bf16 v[110:113], v[162:165], v[186:189], v[110:113]
	v_mfma_f32_16x16x32_bf16 v[102:105], v[170:173], v[186:189], v[102:105]
	v_mfma_f32_16x16x32_bf16 v[94:97], v[162:165], v[194:197], v[94:97]
	v_mfma_f32_16x16x32_bf16 v[86:89], v[170:173], v[194:197], v[86:89]
	v_mfma_f32_16x16x32_bf16 v[78:81], v[162:165], v[204:207], v[78:81]
	v_mfma_f32_16x16x32_bf16 v[70:73], v[170:173], v[204:207], v[70:73]
	s_setprio 0
	s_barrier
	s_mov_b32 m0, s82
	s_or_b32 s52, s62, 0x80
	ds_read_b128 v[174:177], v141 offset:49152
	ds_read_b128 v[178:181], v141 offset:50176
	ds_read_b128 v[182:185], v141 offset:51200
	ds_read_b128 v[186:189], v141 offset:52224
	ds_read_b128 v[190:193], v141 offset:53248
	ds_read_b128 v[194:197], v141 offset:54272
	ds_read_b128 v[198:201], v141 offset:55296
	ds_read_b128 v[204:207], v141 offset:56320
	s_mov_b32 m0, s83
	s_add_i32 s62, s62, 0x80080
	s_mov_b32 m0, s84
	s_nop 0
	s_mov_b32 m0, s85
	s_nop 0
	s_waitcnt vmcnt(6)
	s_waitcnt lgkmcnt(0)
	s_barrier
	s_setprio 1
	s_waitcnt lgkmcnt(7)
	v_mfma_f32_16x16x32_bf16 v[58:61], v[142:145], v[174:177], v[58:61]
	v_mfma_f32_16x16x32_bf16 v[50:53], v[150:153], v[174:177], v[50:53]
	s_waitcnt lgkmcnt(5)
	v_mfma_f32_16x16x32_bf16 v[42:45], v[142:145], v[182:185], v[42:45]
	v_mfma_f32_16x16x32_bf16 v[34:37], v[150:153], v[182:185], v[34:37]
	s_waitcnt lgkmcnt(3)
	v_mfma_f32_16x16x32_bf16 v[26:29], v[142:145], v[190:193], v[26:29]
	v_mfma_f32_16x16x32_bf16 v[18:21], v[150:153], v[190:193], v[18:21]
	s_waitcnt lgkmcnt(1)
	v_mfma_f32_16x16x32_bf16 v[10:13], v[142:145], v[198:201], v[10:13]
	v_mfma_f32_16x16x32_bf16 v[2:5], v[150:153], v[198:201], v[2:5]
	v_mfma_f32_16x16x32_bf16 v[62:65], v[158:161], v[174:177], v[62:65]
	v_mfma_f32_16x16x32_bf16 v[54:57], v[166:169], v[174:177], v[54:57]
	v_mfma_f32_16x16x32_bf16 v[46:49], v[158:161], v[182:185], v[46:49]
	v_mfma_f32_16x16x32_bf16 v[38:41], v[166:169], v[182:185], v[38:41]
	v_mfma_f32_16x16x32_bf16 v[30:33], v[158:161], v[190:193], v[30:33]
	v_mfma_f32_16x16x32_bf16 v[22:25], v[166:169], v[190:193], v[22:25]
	v_mfma_f32_16x16x32_bf16 v[14:17], v[158:161], v[198:201], v[14:17]
	v_mfma_f32_16x16x32_bf16 v[6:9], v[166:169], v[198:201], v[6:9]
	v_mfma_f32_16x16x32_bf16 v[58:61], v[146:149], v[178:181], v[58:61]
	v_mfma_f32_16x16x32_bf16 v[50:53], v[154:157], v[178:181], v[50:53]
	v_mfma_f32_16x16x32_bf16 v[42:45], v[146:149], v[186:189], v[42:45]
	v_mfma_f32_16x16x32_bf16 v[34:37], v[154:157], v[186:189], v[34:37]
	v_mfma_f32_16x16x32_bf16 v[26:29], v[146:149], v[194:197], v[26:29]
	v_mfma_f32_16x16x32_bf16 v[18:21], v[154:157], v[194:197], v[18:21]
	s_waitcnt lgkmcnt(0)
	v_mfma_f32_16x16x32_bf16 v[10:13], v[146:149], v[204:207], v[10:13]
	v_mfma_f32_16x16x32_bf16 v[2:5], v[154:157], v[204:207], v[2:5]
	v_mfma_f32_16x16x32_bf16 v[62:65], v[162:165], v[178:181], v[62:65]
	v_mfma_f32_16x16x32_bf16 v[54:57], v[170:173], v[178:181], v[54:57]
	v_mfma_f32_16x16x32_bf16 v[46:49], v[162:165], v[186:189], v[46:49]
	v_mfma_f32_16x16x32_bf16 v[38:41], v[170:173], v[186:189], v[38:41]
	v_mfma_f32_16x16x32_bf16 v[30:33], v[162:165], v[194:197], v[30:33]
	v_mfma_f32_16x16x32_bf16 v[22:25], v[170:173], v[194:197], v[22:25]
	v_mfma_f32_16x16x32_bf16 v[14:17], v[162:165], v[204:207], v[14:17]
	v_mfma_f32_16x16x32_bf16 v[6:9], v[170:173], v[204:207], v[6:9]
	s_setprio 0
	s_barrier
	s_add_i32 s43, s43, 2
	s_addk_i32 s14, 0x100
	s_addk_i32 s15, 0x100
	s_cmp_gt_u32 s43, 29
.Lex_1:
	s_and_b64 vcc, exec, s[6:7]
	s_cbranch_vccz .LBB0_246
	s_barrier

.LBB0_334:
	ds_read_b128 v[2:5], v105
	ds_read_b128 v[6:9], v105 offset:1024
	ds_read_b128 v[10:13], v105 offset:2048
	ds_read_b128 v[14:17], v105 offset:3072
	ds_read_b128 v[18:21], v170
	ds_read_b128 v[22:25], v170 offset:1024
	ds_read_b128 v[26:29], v170 offset:2048
	ds_read_b128 v[30:33], v170 offset:3072
	s_add_i32 s80, s46, s77
	s_add_i32 s78, s13, s77
	s_add_i32 s79, s80, 0x1600
	s_addk_i32 s78, 0x1600
	s_cmp_eq_u32 s77, 0
	s_cselect_b32 s78, s73, s78
	s_cselect_b32 s79, s72, s79
	s_cbranch_scc0 .Lnx_2
	s_cmp_eq_u64 s[36:37], 0
	s_cbranch_scc1 .Lfin_2
.Lnx_2:
	s_add_i32 s81, s80, 0x1580
	s_mov_b32 m0, s54
	ds_read_b128 v[174:177], v104
	ds_read_b128 v[178:181], v104 offset:1024
	ds_read_b128 v[182:185], v104 offset:2048
	ds_read_b128 v[186:189], v104 offset:3072
	ds_read_b128 v[190:193], v104 offset:4096
	ds_read_b128 v[194:197], v104 offset:5120
	ds_read_b128 v[204:207], v104 offset:6144
	ds_read_b128 v[208:211], v104 offset:7168
	buffer_load_dwordx4 v99, s[64:67], s81 offen lds
	s_mov_b32 m0, s56
	s_add_i32 s80, s80, 0xb1580
	buffer_load_dwordx4 v101, s[64:67], s81 offen lds
	s_mov_b32 m0, s55
	s_nop 0
	buffer_load_dwordx4 v99, s[64:67], s80 offen lds
	s_mov_b32 m0, s57
	s_nop 0
	buffer_load_dwordx4 v101, s[64:67], s80 offen lds
	s_waitcnt vmcnt(8)
	s_waitcnt lgkmcnt(0)
	s_barrier
	s_setprio 1
	s_waitcnt lgkmcnt(6)
	v_mfma_scale_f32_16x16x128_f8f6f4 v[34:37], v[2:9], v[174:181], v[34:37], v237, v237 op_sel_hi:[0,0,0]
	v_mfma_scale_f32_16x16x128_f8f6f4 v[38:41], v[10:17], v[174:181], v[38:41], v237, v237 op_sel_hi:[0,0,0]
	s_waitcnt lgkmcnt(4)
	v_mfma_scale_f32_16x16x128_f8f6f4 v[70:73], v[2:9], v[182:189], v[70:73], v237, v237 op_sel_hi:[0,0,0]
	v_mfma_scale_f32_16x16x128_f8f6f4 v[66:69], v[10:17], v[182:189], v[66:69], v237, v237 op_sel_hi:[0,0,0]
	s_waitcnt lgkmcnt(2)
	v_mfma_scale_f32_16x16x128_f8f6f4 v[78:81], v[2:9], v[190:197], v[78:81], v237, v237 op_sel_hi:[0,0,0]
	v_mfma_scale_f32_16x16x128_f8f6f4 v[74:77], v[10:17], v[190:197], v[74:77], v237, v237 op_sel_hi:[0,0,0]
	s_waitcnt lgkmcnt(0)
	v_mfma_scale_f32_16x16x128_f8f6f4 v[118:121], v[2:9], v[204:211], v[118:121], v237, v237 op_sel_hi:[0,0,0]
	v_mfma_scale_f32_16x16x128_f8f6f4 v[114:117], v[10:17], v[204:211], v[114:117], v237, v237 op_sel_hi:[0,0,0]
	v_mfma_scale_f32_16x16x128_f8f6f4 v[82:85], v[18:25], v[174:181], v[82:85], v237, v237 op_sel_hi:[0,0,0]
	v_mfma_scale_f32_16x16x128_f8f6f4 v[86:89], v[26:33], v[174:181], v[86:89], v237, v237 op_sel_hi:[0,0,0]
	v_mfma_scale_f32_16x16x128_f8f6f4 v[166:169], v[18:25], v[182:189], v[166:169], v237, v237 op_sel_hi:[0,0,0]
	v_mfma_scale_f32_16x16x128_f8f6f4 v[162:165], v[26:33], v[182:189], v[162:165], v237, v237 op_sel_hi:[0,0,0]
	v_mfma_scale_f32_16x16x128_f8f6f4 v[158:161], v[18:25], v[190:197], v[158:161], v237, v237 op_sel_hi:[0,0,0]
	v_mfma_scale_f32_16x16x128_f8f6f4 v[154:157], v[26:33], v[190:197], v[154:157], v237, v237 op_sel_hi:[0,0,0]
	v_mfma_scale_f32_16x16x128_f8f6f4 v[126:129], v[18:25], v[204:211], v[126:129], v237, v237 op_sel_hi:[0,0,0]
	v_mfma_scale_f32_16x16x128_f8f6f4 v[122:125], v[26:33], v[204:211], v[122:125], v237, v237 op_sel_hi:[0,0,0]
	s_setprio 0
	s_barrier
	s_mov_b32 m0, s12
	ds_read_b128 v[174:177], v104 offset:16384
	ds_read_b128 v[178:181], v104 offset:17408
	ds_read_b128 v[182:185], v104 offset:18432
	ds_read_b128 v[186:189], v104 offset:19456
	ds_read_b128 v[190:193], v104 offset:20480
	ds_read_b128 v[194:197], v104 offset:21504
	ds_read_b128 v[204:207], v104 offset:22528
	ds_read_b128 v[208:211], v104 offset:23552
	buffer_load_dwordx4 v100, s[4:7], s78 offen lds
	s_mov_b32 m0, s20
	s_add_i32 s80, s78, 0xb0000
	buffer_load_dwordx4 v102, s[4:7], s78 offen lds
	s_mov_b32 m0, s21
	s_nop 0
	buffer_load_dwordx4 v100, s[4:7], s80 offen lds
	s_mov_b32 m0, s40
	s_nop 0
	buffer_load_dwordx4 v102, s[4:7], s80 offen lds
	s_waitcnt vmcnt(6)
	s_waitcnt lgkmcnt(0)
	s_barrier
	s_setprio 1
	s_waitcnt lgkmcnt(6)
	v_mfma_scale_f32_16x16x128_f8f6f4 v[46:49], v[2:9], v[174:181], v[46:49], v237, v237 op_sel_hi:[0,0,0]
	v_mfma_scale_f32_16x16x128_f8f6f4 v[42:45], v[10:17], v[174:181], v[42:45], v237, v237 op_sel_hi:[0,0,0]
	s_waitcnt lgkmcnt(4)
	v_mfma_scale_f32_16x16x128_f8f6f4 v[54:57], v[2:9], v[182:189], v[54:57], v237, v237 op_sel_hi:[0,0,0]
	v_mfma_scale_f32_16x16x128_f8f6f4 v[50:53], v[10:17], v[182:189], v[50:53], v237, v237 op_sel_hi:[0,0,0]
	s_waitcnt lgkmcnt(2)
	v_mfma_scale_f32_16x16x128_f8f6f4 v[94:97], v[2:9], v[190:197], v[94:97], v237, v237 op_sel_hi:[0,0,0]
	v_mfma_scale_f32_16x16x128_f8f6f4 v[90:93], v[10:17], v[190:197], v[90:93], v237, v237 op_sel_hi:[0,0,0]
	s_waitcnt lgkmcnt(0)
	v_mfma_scale_f32_16x16x128_f8f6f4 v[134:137], v[2:9], v[204:211], v[134:137], v237, v237 op_sel_hi:[0,0,0]
	v_mfma_scale_f32_16x16x128_f8f6f4 v[130:133], v[10:17], v[204:211], v[130:133], v237, v237 op_sel_hi:[0,0,0]
	v_mfma_scale_f32_16x16x128_f8f6f4 v[62:65], v[18:25], v[174:181], v[62:65], v237, v237 op_sel_hi:[0,0,0]
	v_mfma_scale_f32_16x16x128_f8f6f4 v[58:61], v[26:33], v[174:181], v[58:61], v237, v237 op_sel_hi:[0,0,0]
	v_mfma_scale_f32_16x16x128_f8f6f4 v[110:113], v[18:25], v[182:189], v[110:113], v237, v237 op_sel_hi:[0,0,0]
	v_mfma_scale_f32_16x16x128_f8f6f4 v[106:109], v[26:33], v[182:189], v[106:109], v237, v237 op_sel_hi:[0,0,0]
	v_mfma_scale_f32_16x16x128_f8f6f4 v[150:153], v[18:25], v[190:197], v[150:153], v237, v237 op_sel_hi:[0,0,0]
	v_mfma_scale_f32_16x16x128_f8f6f4 v[146:149], v[26:33], v[190:197], v[146:149], v237, v237 op_sel_hi:[0,0,0]
	v_mfma_scale_f32_16x16x128_f8f6f4 v[142:145], v[18:25], v[204:211], v[142:145], v237, v237 op_sel_hi:[0,0,0]
	v_mfma_scale_f32_16x16x128_f8f6f4 v[138:141], v[26:33], v[204:211], v[138:141], v237, v237 op_sel_hi:[0,0,0]
	s_setprio 0
	s_barrier
	ds_read_b128 v[18:21], v171
	ds_read_b128 v[22:25], v171 offset:1024
	ds_read_b128 v[26:29], v171 offset:2048
	ds_read_b128 v[30:33], v171 offset:3072
	ds_read_b128 v[10:13], v172
	ds_read_b128 v[14:17], v172 offset:1024
	ds_read_b128 v[2:5], v172 offset:2048
	ds_read_b128 v[6:9], v172 offset:3072
	s_mov_b32 m0, s11
	ds_read_b128 v[174:177], v104 offset:32768
	ds_read_b128 v[178:181], v104 offset:33792
	ds_read_b128 v[182:185], v104 offset:34816
	ds_read_b128 v[186:189], v104 offset:35840
	ds_read_b128 v[190:193], v104 offset:36864
	ds_read_b128 v[194:197], v104 offset:37888
	ds_read_b128 v[204:207], v104 offset:38912
	ds_read_b128 v[208:211], v104 offset:39936
	buffer_load_dwordx4 v99, s[64:67], s79 offen lds
	s_mov_b32 m0, s45
	s_nop 0
	buffer_load_dwordx4 v101, s[64:67], s79 offen lds
	s_add_i32 s79, s79, 0xb0000
	s_mov_b32 m0, s47
	s_nop 0
	buffer_load_dwordx4 v99, s[64:67], s79 offen lds
	s_mov_b32 m0, s48
	s_nop 0
	buffer_load_dwordx4 v101, s[64:67], s79 offen lds
	s_waitcnt vmcnt(8)
	s_waitcnt lgkmcnt(0)
	s_barrier
	s_setprio 1
	s_waitcnt lgkmcnt(6)
	v_mfma_scale_f32_16x16x128_f8f6f4 v[34:37], v[18:25], v[174:181], v[34:37], v237, v237 op_sel_hi:[0,0,0]
	v_mfma_scale_f32_16x16x128_f8f6f4 v[38:41], v[26:33], v[174:181], v[38:41], v237, v237 op_sel_hi:[0,0,0]
	s_waitcnt lgkmcnt(4)
	v_mfma_scale_f32_16x16x128_f8f6f4 v[70:73], v[18:25], v[182:189], v[70:73], v237, v237 op_sel_hi:[0,0,0]
	v_mfma_scale_f32_16x16x128_f8f6f4 v[66:69], v[26:33], v[182:189], v[66:69], v237, v237 op_sel_hi:[0,0,0]
	s_waitcnt lgkmcnt(2)
	v_mfma_scale_f32_16x16x128_f8f6f4 v[78:81], v[18:25], v[190:197], v[78:81], v237, v237 op_sel_hi:[0,0,0]
	v_mfma_scale_f32_16x16x128_f8f6f4 v[74:77], v[26:33], v[190:197], v[74:77], v237, v237 op_sel_hi:[0,0,0]
	s_waitcnt lgkmcnt(0)
	v_mfma_scale_f32_16x16x128_f8f6f4 v[118:121], v[18:25], v[204:211], v[118:121], v237, v237 op_sel_hi:[0,0,0]
	v_mfma_scale_f32_16x16x128_f8f6f4 v[114:117], v[26:33], v[204:211], v[114:117], v237, v237 op_sel_hi:[0,0,0]
	v_mfma_scale_f32_16x16x128_f8f6f4 v[82:85], v[10:17], v[174:181], v[82:85], v237, v237 op_sel_hi:[0,0,0]
	v_mfma_scale_f32_16x16x128_f8f6f4 v[86:89], v[2:9], v[174:181], v[86:89], v237, v237 op_sel_hi:[0,0,0]
	v_mfma_scale_f32_16x16x128_f8f6f4 v[166:169], v[10:17], v[182:189], v[166:169], v237, v237 op_sel_hi:[0,0,0]
	v_mfma_scale_f32_16x16x128_f8f6f4 v[162:165], v[2:9], v[182:189], v[162:165], v237, v237 op_sel_hi:[0,0,0]
	v_mfma_scale_f32_16x16x128_f8f6f4 v[158:161], v[10:17], v[190:197], v[158:161], v237, v237 op_sel_hi:[0,0,0]
	v_mfma_scale_f32_16x16x128_f8f6f4 v[154:157], v[2:9], v[190:197], v[154:157], v237, v237 op_sel_hi:[0,0,0]
	v_mfma_scale_f32_16x16x128_f8f6f4 v[126:129], v[10:17], v[204:211], v[126:129], v237, v237 op_sel_hi:[0,0,0]
	v_mfma_scale_f32_16x16x128_f8f6f4 v[122:125], v[2:9], v[204:211], v[122:125], v237, v237 op_sel_hi:[0,0,0]
	s_setprio 0
	s_barrier
	s_mov_b32 m0, s50
	s_or_b32 s79, s78, 0x80
	ds_read_b128 v[174:177], v104 offset:49152
	ds_read_b128 v[178:181], v104 offset:50176
	ds_read_b128 v[182:185], v104 offset:51200
	ds_read_b128 v[186:189], v104 offset:52224
	ds_read_b128 v[190:193], v104 offset:53248
	ds_read_b128 v[194:197], v104 offset:54272
	ds_read_b128 v[204:207], v104 offset:55296
	ds_read_b128 v[208:211], v104 offset:56320
	buffer_load_dwordx4 v100, s[4:7], s79 offen lds
	s_mov_b32 m0, s51
	s_add_i32 s78, s78, 0xb0080
	buffer_load_dwordx4 v102, s[4:7], s79 offen lds
	s_mov_b32 m0, s52
	s_nop 0
	buffer_load_dwordx4 v100, s[4:7], s78 offen lds
	s_mov_b32 m0, s53
	s_nop 0
	buffer_load_dwordx4 v102, s[4:7], s78 offen lds
	s_waitcnt vmcnt(6)
	s_waitcnt lgkmcnt(0)
	s_barrier
	s_setprio 1
	s_waitcnt lgkmcnt(6)
	v_mfma_scale_f32_16x16x128_f8f6f4 v[46:49], v[18:25], v[174:181], v[46:49], v237, v237 op_sel_hi:[0,0,0]
	v_mfma_scale_f32_16x16x128_f8f6f4 v[42:45], v[26:33], v[174:181], v[42:45], v237, v237 op_sel_hi:[0,0,0]
	s_waitcnt lgkmcnt(4)
	v_mfma_scale_f32_16x16x128_f8f6f4 v[54:57], v[18:25], v[182:189], v[54:57], v237, v237 op_sel_hi:[0,0,0]
	v_mfma_scale_f32_16x16x128_f8f6f4 v[50:53], v[26:33], v[182:189], v[50:53], v237, v237 op_sel_hi:[0,0,0]
	s_waitcnt lgkmcnt(2)
	v_mfma_scale_f32_16x16x128_f8f6f4 v[94:97], v[18:25], v[190:197], v[94:97], v237, v237 op_sel_hi:[0,0,0]
	v_mfma_scale_f32_16x16x128_f8f6f4 v[90:93], v[26:33], v[190:197], v[90:93], v237, v237 op_sel_hi:[0,0,0]
	s_waitcnt lgkmcnt(0)
	v_mfma_scale_f32_16x16x128_f8f6f4 v[134:137], v[18:25], v[204:211], v[134:137], v237, v237 op_sel_hi:[0,0,0]
	v_mfma_scale_f32_16x16x128_f8f6f4 v[130:133], v[26:33], v[204:211], v[130:133], v237, v237 op_sel_hi:[0,0,0]
	v_mfma_scale_f32_16x16x128_f8f6f4 v[62:65], v[10:17], v[174:181], v[62:65], v237, v237 op_sel_hi:[0,0,0]
	v_mfma_scale_f32_16x16x128_f8f6f4 v[58:61], v[2:9], v[174:181], v[58:61], v237, v237 op_sel_hi:[0,0,0]
	v_mfma_scale_f32_16x16x128_f8f6f4 v[110:113], v[10:17], v[182:189], v[110:113], v237, v237 op_sel_hi:[0,0,0]
	v_mfma_scale_f32_16x16x128_f8f6f4 v[106:109], v[2:9], v[182:189], v[106:109], v237, v237 op_sel_hi:[0,0,0]
	v_mfma_scale_f32_16x16x128_f8f6f4 v[150:153], v[10:17], v[190:197], v[150:153], v237, v237 op_sel_hi:[0,0,0]
	v_mfma_scale_f32_16x16x128_f8f6f4 v[146:149], v[2:9], v[190:197], v[146:149], v237, v237 op_sel_hi:[0,0,0]
	v_mfma_scale_f32_16x16x128_f8f6f4 v[142:145], v[10:17], v[204:211], v[142:145], v237, v237 op_sel_hi:[0,0,0]
	v_mfma_scale_f32_16x16x128_f8f6f4 v[138:141], v[2:9], v[204:211], v[138:141], v237, v237 op_sel_hi:[0,0,0]
	s_setprio 0
	s_barrier
	s_add_i32 s76, s76, 2
	s_addk_i32 s77, 0x100
	s_cmp_gt_u32 s76, 41
	s_cbranch_scc0 .LBB0_334
	s_branch .Lex_2
.Lfin_2:
	s_add_i32 s81, s80, 0x1580
	s_mov_b32 m0, s54
	ds_read_b128 v[174:177], v104
	ds_read_b128 v[178:181], v104 offset:1024
	ds_read_b128 v[182:185], v104 offset:2048
	ds_read_b128 v[186:189], v104 offset:3072
	ds_read_b128 v[190:193], v104 offset:4096
	ds_read_b128 v[194:197], v104 offset:5120
	ds_read_b128 v[204:207], v104 offset:6144
	ds_read_b128 v[208:211], v104 offset:7168
	buffer_load_dwordx4 v99, s[64:67], s81 offen lds
	s_mov_b32 m0, s56
	s_add_i32 s80, s80, 0xb1580
	buffer_load_dwordx4 v101, s[64:67], s81 offen lds
	s_mov_b32 m0, s55
	s_nop 0
	buffer_load_dwordx4 v99, s[64:67], s80 offen lds
	s_mov_b32 m0, s57
	s_nop 0
	buffer_load_dwordx4 v101, s[64:67], s80 offen lds
	s_waitcnt vmcnt(8)
	s_waitcnt lgkmcnt(0)
	s_barrier
	s_setprio 1
	s_waitcnt lgkmcnt(6)
	v_mfma_scale_f32_16x16x128_f8f6f4 v[34:37], v[2:9], v[174:181], v[34:37], v237, v237 op_sel_hi:[0,0,0]
	v_mfma_scale_f32_16x16x128_f8f6f4 v[38:41], v[10:17], v[174:181], v[38:41], v237, v237 op_sel_hi:[0,0,0]
	s_waitcnt lgkmcnt(4)
	v_mfma_scale_f32_16x16x128_f8f6f4 v[70:73], v[2:9], v[182:189], v[70:73], v237, v237 op_sel_hi:[0,0,0]
	v_mfma_scale_f32_16x16x128_f8f6f4 v[66:69], v[10:17], v[182:189], v[66:69], v237, v237 op_sel_hi:[0,0,0]
	s_waitcnt lgkmcnt(2)
	v_mfma_scale_f32_16x16x128_f8f6f4 v[78:81], v[2:9], v[190:197], v[78:81], v237, v237 op_sel_hi:[0,0,0]
	v_mfma_scale_f32_16x16x128_f8f6f4 v[74:77], v[10:17], v[190:197], v[74:77], v237, v237 op_sel_hi:[0,0,0]
	s_waitcnt lgkmcnt(0)
	v_mfma_scale_f32_16x16x128_f8f6f4 v[118:121], v[2:9], v[204:211], v[118:121], v237, v237 op_sel_hi:[0,0,0]
	v_mfma_scale_f32_16x16x128_f8f6f4 v[114:117], v[10:17], v[204:211], v[114:117], v237, v237 op_sel_hi:[0,0,0]
	v_mfma_scale_f32_16x16x128_f8f6f4 v[82:85], v[18:25], v[174:181], v[82:85], v237, v237 op_sel_hi:[0,0,0]
	v_mfma_scale_f32_16x16x128_f8f6f4 v[86:89], v[26:33], v[174:181], v[86:89], v237, v237 op_sel_hi:[0,0,0]
	v_mfma_scale_f32_16x16x128_f8f6f4 v[166:169], v[18:25], v[182:189], v[166:169], v237, v237 op_sel_hi:[0,0,0]
	v_mfma_scale_f32_16x16x128_f8f6f4 v[162:165], v[26:33], v[182:189], v[162:165], v237, v237 op_sel_hi:[0,0,0]
	v_mfma_scale_f32_16x16x128_f8f6f4 v[158:161], v[18:25], v[190:197], v[158:161], v237, v237 op_sel_hi:[0,0,0]
	v_mfma_scale_f32_16x16x128_f8f6f4 v[154:157], v[26:33], v[190:197], v[154:157], v237, v237 op_sel_hi:[0,0,0]
	v_mfma_scale_f32_16x16x128_f8f6f4 v[126:129], v[18:25], v[204:211], v[126:129], v237, v237 op_sel_hi:[0,0,0]
	v_mfma_scale_f32_16x16x128_f8f6f4 v[122:125], v[26:33], v[204:211], v[122:125], v237, v237 op_sel_hi:[0,0,0]
	s_setprio 0
	s_barrier
	s_mov_b32 m0, s12
	ds_read_b128 v[174:177], v104 offset:16384
	ds_read_b128 v[178:181], v104 offset:17408
	ds_read_b128 v[182:185], v104 offset:18432
	ds_read_b128 v[186:189], v104 offset:19456
	ds_read_b128 v[190:193], v104 offset:20480
	ds_read_b128 v[194:197], v104 offset:21504
	ds_read_b128 v[204:207], v104 offset:22528
	ds_read_b128 v[208:211], v104 offset:23552
	s_mov_b32 m0, s20
	s_add_i32 s80, s78, 0xb0000
	s_mov_b32 m0, s21
	s_nop 0
	s_mov_b32 m0, s40
	s_nop 0
	s_waitcnt vmcnt(0)
	s_waitcnt lgkmcnt(0)
	s_barrier
	s_setprio 1
	s_waitcnt lgkmcnt(6)
	v_mfma_scale_f32_16x16x128_f8f6f4 v[46:49], v[2:9], v[174:181], v[46:49], v237, v237 op_sel_hi:[0,0,0]
	v_mfma_scale_f32_16x16x128_f8f6f4 v[42:45], v[10:17], v[174:181], v[42:45], v237, v237 op_sel_hi:[0,0,0]
	s_waitcnt lgkmcnt(4)
	v_mfma_scale_f32_16x16x128_f8f6f4 v[54:57], v[2:9], v[182:189], v[54:57], v237, v237 op_sel_hi:[0,0,0]
	v_mfma_scale_f32_16x16x128_f8f6f4 v[50:53], v[10:17], v[182:189], v[50:53], v237, v237 op_sel_hi:[0,0,0]
	s_waitcnt lgkmcnt(2)
	v_mfma_scale_f32_16x16x128_f8f6f4 v[94:97], v[2:9], v[190:197], v[94:97], v237, v237 op_sel_hi:[0,0,0]
	v_mfma_scale_f32_16x16x128_f8f6f4 v[90:93], v[10:17], v[190:197], v[90:93], v237, v237 op_sel_hi:[0,0,0]
	s_waitcnt lgkmcnt(0)
	v_mfma_scale_f32_16x16x128_f8f6f4 v[134:137], v[2:9], v[204:211], v[134:137], v237, v237 op_sel_hi:[0,0,0]
	v_mfma_scale_f32_16x16x128_f8f6f4 v[130:133], v[10:17], v[204:211], v[130:133], v237, v237 op_sel_hi:[0,0,0]
	v_mfma_scale_f32_16x16x128_f8f6f4 v[62:65], v[18:25], v[174:181], v[62:65], v237, v237 op_sel_hi:[0,0,0]
	v_mfma_scale_f32_16x16x128_f8f6f4 v[58:61], v[26:33], v[174:181], v[58:61], v237, v237 op_sel_hi:[0,0,0]
	v_mfma_scale_f32_16x16x128_f8f6f4 v[110:113], v[18:25], v[182:189], v[110:113], v237, v237 op_sel_hi:[0,0,0]
	v_mfma_scale_f32_16x16x128_f8f6f4 v[106:109], v[26:33], v[182:189], v[106:109], v237, v237 op_sel_hi:[0,0,0]
	v_mfma_scale_f32_16x16x128_f8f6f4 v[150:153], v[18:25], v[190:197], v[150:153], v237, v237 op_sel_hi:[0,0,0]
	v_mfma_scale_f32_16x16x128_f8f6f4 v[146:149], v[26:33], v[190:197], v[146:149], v237, v237 op_sel_hi:[0,0,0]
	v_mfma_scale_f32_16x16x128_f8f6f4 v[142:145], v[18:25], v[204:211], v[142:145], v237, v237 op_sel_hi:[0,0,0]
	v_mfma_scale_f32_16x16x128_f8f6f4 v[138:141], v[26:33], v[204:211], v[138:141], v237, v237 op_sel_hi:[0,0,0]
	s_setprio 0
	s_barrier
	ds_read_b128 v[18:21], v171
	ds_read_b128 v[22:25], v171 offset:1024
	ds_read_b128 v[26:29], v171 offset:2048
	ds_read_b128 v[30:33], v171 offset:3072
	ds_read_b128 v[10:13], v172
	ds_read_b128 v[14:17], v172 offset:1024
	ds_read_b128 v[2:5], v172 offset:2048
	ds_read_b128 v[6:9], v172 offset:3072
	s_mov_b32 m0, s11
	ds_read_b128 v[174:177], v104 offset:32768
	ds_read_b128 v[178:181], v104 offset:33792
	ds_read_b128 v[182:185], v104 offset:34816
	ds_read_b128 v[186:189], v104 offset:35840
	ds_read_b128 v[190:193], v104 offset:36864
	ds_read_b128 v[194:197], v104 offset:37888
	ds_read_b128 v[204:207], v104 offset:38912
	ds_read_b128 v[208:211], v104 offset:39936
	s_mov_b32 m0, s45
	s_nop 0
	s_add_i32 s79, s79, 0xb0000
	s_mov_b32 m0, s47
	s_nop 0
	s_mov_b32 m0, s48
	s_nop 0
	s_waitcnt vmcnt(8)
	s_waitcnt lgkmcnt(0)
	s_barrier
	s_setprio 1
	s_waitcnt lgkmcnt(6)
	v_mfma_scale_f32_16x16x128_f8f6f4 v[34:37], v[18:25], v[174:181], v[34:37], v237, v237 op_sel_hi:[0,0,0]
	v_mfma_scale_f32_16x16x128_f8f6f4 v[38:41], v[26:33], v[174:181], v[38:41], v237, v237 op_sel_hi:[0,0,0]
	s_waitcnt lgkmcnt(4)
	v_mfma_scale_f32_16x16x128_f8f6f4 v[70:73], v[18:25], v[182:189], v[70:73], v237, v237 op_sel_hi:[0,0,0]
	v_mfma_scale_f32_16x16x128_f8f6f4 v[66:69], v[26:33], v[182:189], v[66:69], v237, v237 op_sel_hi:[0,0,0]
	s_waitcnt lgkmcnt(2)
	v_mfma_scale_f32_16x16x128_f8f6f4 v[78:81], v[18:25], v[190:197], v[78:81], v237, v237 op_sel_hi:[0,0,0]
	v_mfma_scale_f32_16x16x128_f8f6f4 v[74:77], v[26:33], v[190:197], v[74:77], v237, v237 op_sel_hi:[0,0,0]
	s_waitcnt lgkmcnt(0)
	v_mfma_scale_f32_16x16x128_f8f6f4 v[118:121], v[18:25], v[204:211], v[118:121], v237, v237 op_sel_hi:[0,0,0]
	v_mfma_scale_f32_16x16x128_f8f6f4 v[114:117], v[26:33], v[204:211], v[114:117], v237, v237 op_sel_hi:[0,0,0]
	v_mfma_scale_f32_16x16x128_f8f6f4 v[82:85], v[10:17], v[174:181], v[82:85], v237, v237 op_sel_hi:[0,0,0]
	v_mfma_scale_f32_16x16x128_f8f6f4 v[86:89], v[2:9], v[174:181], v[86:89], v237, v237 op_sel_hi:[0,0,0]
	v_mfma_scale_f32_16x16x128_f8f6f4 v[166:169], v[10:17], v[182:189], v[166:169], v237, v237 op_sel_hi:[0,0,0]
	v_mfma_scale_f32_16x16x128_f8f6f4 v[162:165], v[2:9], v[182:189], v[162:165], v237, v237 op_sel_hi:[0,0,0]
	v_mfma_scale_f32_16x16x128_f8f6f4 v[158:161], v[10:17], v[190:197], v[158:161], v237, v237 op_sel_hi:[0,0,0]
	v_mfma_scale_f32_16x16x128_f8f6f4 v[154:157], v[2:9], v[190:197], v[154:157], v237, v237 op_sel_hi:[0,0,0]
	v_mfma_scale_f32_16x16x128_f8f6f4 v[126:129], v[10:17], v[204:211], v[126:129], v237, v237 op_sel_hi:[0,0,0]
	v_mfma_scale_f32_16x16x128_f8f6f4 v[122:125], v[2:9], v[204:211], v[122:125], v237, v237 op_sel_hi:[0,0,0]
	s_setprio 0
	s_barrier
	s_mov_b32 m0, s50
	s_or_b32 s79, s78, 0x80
	ds_read_b128 v[174:177], v104 offset:49152
	ds_read_b128 v[178:181], v104 offset:50176
	ds_read_b128 v[182:185], v104 offset:51200
	ds_read_b128 v[186:189], v104 offset:52224
	ds_read_b128 v[190:193], v104 offset:53248
	ds_read_b128 v[194:197], v104 offset:54272
	ds_read_b128 v[204:207], v104 offset:55296
	ds_read_b128 v[208:211], v104 offset:56320
	s_mov_b32 m0, s51
	s_add_i32 s78, s78, 0xb0080
	s_mov_b32 m0, s52
	s_nop 0
	s_mov_b32 m0, s53
	s_nop 0
	s_waitcnt vmcnt(6)
	s_waitcnt lgkmcnt(0)
	s_barrier
	s_setprio 1
	s_waitcnt lgkmcnt(6)
	v_mfma_scale_f32_16x16x128_f8f6f4 v[46:49], v[18:25], v[174:181], v[46:49], v237, v237 op_sel_hi:[0,0,0]
	v_mfma_scale_f32_16x16x128_f8f6f4 v[42:45], v[26:33], v[174:181], v[42:45], v237, v237 op_sel_hi:[0,0,0]
	s_waitcnt lgkmcnt(4)
	v_mfma_scale_f32_16x16x128_f8f6f4 v[54:57], v[18:25], v[182:189], v[54:57], v237, v237 op_sel_hi:[0,0,0]
	v_mfma_scale_f32_16x16x128_f8f6f4 v[50:53], v[26:33], v[182:189], v[50:53], v237, v237 op_sel_hi:[0,0,0]
	s_waitcnt lgkmcnt(2)
	v_mfma_scale_f32_16x16x128_f8f6f4 v[94:97], v[18:25], v[190:197], v[94:97], v237, v237 op_sel_hi:[0,0,0]
	v_mfma_scale_f32_16x16x128_f8f6f4 v[90:93], v[26:33], v[190:197], v[90:93], v237, v237 op_sel_hi:[0,0,0]
	s_waitcnt lgkmcnt(0)
	v_mfma_scale_f32_16x16x128_f8f6f4 v[134:137], v[18:25], v[204:211], v[134:137], v237, v237 op_sel_hi:[0,0,0]
	v_mfma_scale_f32_16x16x128_f8f6f4 v[130:133], v[26:33], v[204:211], v[130:133], v237, v237 op_sel_hi:[0,0,0]
	v_mfma_scale_f32_16x16x128_f8f6f4 v[62:65], v[10:17], v[174:181], v[62:65], v237, v237 op_sel_hi:[0,0,0]
	v_mfma_scale_f32_16x16x128_f8f6f4 v[58:61], v[2:9], v[174:181], v[58:61], v237, v237 op_sel_hi:[0,0,0]
	v_mfma_scale_f32_16x16x128_f8f6f4 v[110:113], v[10:17], v[182:189], v[110:113], v237, v237 op_sel_hi:[0,0,0]
	v_mfma_scale_f32_16x16x128_f8f6f4 v[106:109], v[2:9], v[182:189], v[106:109], v237, v237 op_sel_hi:[0,0,0]
	v_mfma_scale_f32_16x16x128_f8f6f4 v[150:153], v[10:17], v[190:197], v[150:153], v237, v237 op_sel_hi:[0,0,0]
	v_mfma_scale_f32_16x16x128_f8f6f4 v[146:149], v[2:9], v[190:197], v[146:149], v237, v237 op_sel_hi:[0,0,0]
	v_mfma_scale_f32_16x16x128_f8f6f4 v[142:145], v[10:17], v[204:211], v[142:145], v237, v237 op_sel_hi:[0,0,0]
	v_mfma_scale_f32_16x16x128_f8f6f4 v[138:141], v[2:9], v[204:211], v[138:141], v237, v237 op_sel_hi:[0,0,0]
	s_setprio 0
	s_barrier
	s_add_i32 s76, s76, 2
	s_addk_i32 s77, 0x100
	s_cmp_gt_u32 s76, 41
.Lex_2:
	s_nop 15
	s_nop 15
	s_and_b64 vcc, exec, s[36:37]
	s_cbranch_vccz .LBB0_330
	s_mov_b32 s10, s59
	s_mov_b32 s0, s60
	s_mov_b32 s13, s63
	s_mov_b32 s46, s62
	s_mov_b32 s58, s61
	s_branch .LBB0_330

.LBB0_412:
	ds_read_b128 v[2:5], v137
	ds_read_b128 v[6:9], v137 offset:1024
	ds_read_b128 v[10:13], v137 offset:2048
	ds_read_b128 v[14:17], v137 offset:3072
	ds_read_b128 v[18:21], v170
	ds_read_b128 v[22:25], v170 offset:1024
	ds_read_b128 v[26:29], v170 offset:2048
	ds_read_b128 v[30:33], v170 offset:3072
	s_add_i32 s76, s37, s63
	s_add_i32 s72, s13, s63
	s_add_i32 s73, s76, 0x1600
	s_addk_i32 s72, 0x1600
	s_cmp_eq_u32 s63, 0
	s_cselect_b32 s72, s61, s72
	s_cselect_b32 s73, s60, s73
	s_cbranch_scc0 .Lnx_3
	s_cmp_eq_u64 s[28:29], 0
	s_cbranch_scc1 .Lfin_3
.Lnx_3:
	s_add_i32 s77, s76, 0x1580
	s_mov_b32 m0, s50
	ds_read_b128 v[174:177], v136
	ds_read_b128 v[178:181], v136 offset:1024
	ds_read_b128 v[182:185], v136 offset:2048
	ds_read_b128 v[186:189], v136 offset:3072
	ds_read_b128 v[190:193], v136 offset:4096
	ds_read_b128 v[194:197], v136 offset:5120
	ds_read_b128 v[204:207], v136 offset:6144
	ds_read_b128 v[208:211], v136 offset:7168
	buffer_load_dwordx4 v131, s[64:67], s77 offen lds
	s_mov_b32 m0, s52
	s_add_i32 s76, s76, 0xb1580
	buffer_load_dwordx4 v133, s[64:67], s77 offen lds
	s_mov_b32 m0, s51
	s_nop 0
	buffer_load_dwordx4 v131, s[64:67], s76 offen lds
	s_mov_b32 m0, s53
	s_nop 0
	buffer_load_dwordx4 v133, s[64:67], s76 offen lds
	s_waitcnt vmcnt(8)
	s_waitcnt lgkmcnt(0)
	s_barrier
	s_setprio 1
	s_waitcnt lgkmcnt(6)
	v_mfma_scale_f32_16x16x128_f8f6f4 v[114:117], v[2:9], v[174:181], v[114:117], v237, v237 op_sel_hi:[0,0,0]
	v_mfma_scale_f32_16x16x128_f8f6f4 v[118:121], v[10:17], v[174:181], v[118:121], v237, v237 op_sel_hi:[0,0,0]
	s_waitcnt lgkmcnt(4)
	v_mfma_scale_f32_16x16x128_f8f6f4 v[54:57], v[2:9], v[182:189], v[54:57], v237, v237 op_sel_hi:[0,0,0]
	v_mfma_scale_f32_16x16x128_f8f6f4 v[50:53], v[10:17], v[182:189], v[50:53], v237, v237 op_sel_hi:[0,0,0]
	s_waitcnt lgkmcnt(2)
	v_mfma_scale_f32_16x16x128_f8f6f4 v[46:49], v[2:9], v[190:197], v[46:49], v237, v237 op_sel_hi:[0,0,0]
	v_mfma_scale_f32_16x16x128_f8f6f4 v[42:45], v[10:17], v[190:197], v[42:45], v237, v237 op_sel_hi:[0,0,0]
	s_waitcnt lgkmcnt(0)
	v_mfma_scale_f32_16x16x128_f8f6f4 v[38:41], v[2:9], v[204:211], v[38:41], v237, v237 op_sel_hi:[0,0,0]
	v_mfma_scale_f32_16x16x128_f8f6f4 v[34:37], v[10:17], v[204:211], v[34:37], v237, v237 op_sel_hi:[0,0,0]
	v_mfma_scale_f32_16x16x128_f8f6f4 v[58:61], v[18:25], v[174:181], v[58:61], v237, v237 op_sel_hi:[0,0,0]
	v_mfma_scale_f32_16x16x128_f8f6f4 v[62:65], v[26:33], v[174:181], v[62:65], v237, v237 op_sel_hi:[0,0,0]
	v_mfma_scale_f32_16x16x128_f8f6f4 v[110:113], v[18:25], v[182:189], v[110:113], v237, v237 op_sel_hi:[0,0,0]
	v_mfma_scale_f32_16x16x128_f8f6f4 v[106:109], v[26:33], v[182:189], v[106:109], v237, v237 op_sel_hi:[0,0,0]
	v_mfma_scale_f32_16x16x128_f8f6f4 v[102:105], v[18:25], v[190:197], v[102:105], v237, v237 op_sel_hi:[0,0,0]
	v_mfma_scale_f32_16x16x128_f8f6f4 v[98:101], v[26:33], v[190:197], v[98:101], v237, v237 op_sel_hi:[0,0,0]
	v_mfma_scale_f32_16x16x128_f8f6f4 v[162:165], v[18:25], v[204:211], v[162:165], v237, v237 op_sel_hi:[0,0,0]
	v_mfma_scale_f32_16x16x128_f8f6f4 v[94:97], v[26:33], v[204:211], v[94:97], v237, v237 op_sel_hi:[0,0,0]
	s_setprio 0
	s_barrier
	s_mov_b32 m0, s12
	ds_read_b128 v[174:177], v136 offset:16384
	ds_read_b128 v[178:181], v136 offset:17408
	ds_read_b128 v[182:185], v136 offset:18432
	ds_read_b128 v[186:189], v136 offset:19456
	ds_read_b128 v[190:193], v136 offset:20480
	ds_read_b128 v[194:197], v136 offset:21504
	ds_read_b128 v[204:207], v136 offset:22528
	ds_read_b128 v[208:211], v136 offset:23552
	buffer_load_dwordx4 v132, s[4:7], s72 offen lds
	s_mov_b32 m0, s31
	s_add_i32 s76, s72, 0xb0000
	buffer_load_dwordx4 v134, s[4:7], s72 offen lds
	s_mov_b32 m0, s34
	s_nop 0
	buffer_load_dwordx4 v132, s[4:7], s76 offen lds
	s_mov_b32 m0, s35
	s_nop 0
	buffer_load_dwordx4 v134, s[4:7], s76 offen lds
	s_waitcnt vmcnt(6)
	s_waitcnt lgkmcnt(0)
	s_barrier
	s_setprio 1
	s_waitcnt lgkmcnt(6)
	v_mfma_scale_f32_16x16x128_f8f6f4 v[154:157], v[2:9], v[174:181], v[154:157], v237, v237 op_sel_hi:[0,0,0]
	v_mfma_scale_f32_16x16x128_f8f6f4 v[90:93], v[10:17], v[174:181], v[90:93], v237, v237 op_sel_hi:[0,0,0]
	s_waitcnt lgkmcnt(4)
	v_mfma_scale_f32_16x16x128_f8f6f4 v[86:89], v[2:9], v[182:189], v[86:89], v237, v237 op_sel_hi:[0,0,0]
	v_mfma_scale_f32_16x16x128_f8f6f4 v[82:85], v[10:17], v[182:189], v[82:85], v237, v237 op_sel_hi:[0,0,0]
	s_waitcnt lgkmcnt(2)
	v_mfma_scale_f32_16x16x128_f8f6f4 v[78:81], v[2:9], v[190:197], v[78:81], v237, v237 op_sel_hi:[0,0,0]
	v_mfma_scale_f32_16x16x128_f8f6f4 v[74:77], v[10:17], v[190:197], v[74:77], v237, v237 op_sel_hi:[0,0,0]
	s_waitcnt lgkmcnt(0)
	v_mfma_scale_f32_16x16x128_f8f6f4 v[70:73], v[2:9], v[204:211], v[70:73], v237, v237 op_sel_hi:[0,0,0]
	v_mfma_scale_f32_16x16x128_f8f6f4 v[66:69], v[10:17], v[204:211], v[66:69], v237, v237 op_sel_hi:[0,0,0]
	v_mfma_scale_f32_16x16x128_f8f6f4 v[166:169], v[18:25], v[174:181], v[166:169], v237, v237 op_sel_hi:[0,0,0]
	v_mfma_scale_f32_16x16x128_f8f6f4 v[158:161], v[26:33], v[174:181], v[158:161], v237, v237 op_sel_hi:[0,0,0]
	v_mfma_scale_f32_16x16x128_f8f6f4 v[150:153], v[18:25], v[182:189], v[150:153], v237, v237 op_sel_hi:[0,0,0]
	v_mfma_scale_f32_16x16x128_f8f6f4 v[146:149], v[26:33], v[182:189], v[146:149], v237, v237 op_sel_hi:[0,0,0]
	v_mfma_scale_f32_16x16x128_f8f6f4 v[142:145], v[18:25], v[190:197], v[142:145], v237, v237 op_sel_hi:[0,0,0]
	v_mfma_scale_f32_16x16x128_f8f6f4 v[138:141], v[26:33], v[190:197], v[138:141], v237, v237 op_sel_hi:[0,0,0]
	v_mfma_scale_f32_16x16x128_f8f6f4 v[126:129], v[18:25], v[204:211], v[126:129], v237, v237 op_sel_hi:[0,0,0]
	v_mfma_scale_f32_16x16x128_f8f6f4 v[122:125], v[26:33], v[204:211], v[122:125], v237, v237 op_sel_hi:[0,0,0]
	s_setprio 0
	s_barrier
	ds_read_b128 v[18:21], v171
	ds_read_b128 v[22:25], v171 offset:1024
	ds_read_b128 v[26:29], v171 offset:2048
	ds_read_b128 v[30:33], v171 offset:3072
	ds_read_b128 v[10:13], v172
	ds_read_b128 v[14:17], v172 offset:1024
	ds_read_b128 v[2:5], v172 offset:2048
	ds_read_b128 v[6:9], v172 offset:3072
	s_mov_b32 m0, s11
	ds_read_b128 v[174:177], v136 offset:32768
	ds_read_b128 v[178:181], v136 offset:33792
	ds_read_b128 v[182:185], v136 offset:34816
	ds_read_b128 v[186:189], v136 offset:35840
	ds_read_b128 v[190:193], v136 offset:36864
	ds_read_b128 v[194:197], v136 offset:37888
	ds_read_b128 v[204:207], v136 offset:38912
	ds_read_b128 v[208:211], v136 offset:39936
	buffer_load_dwordx4 v131, s[64:67], s73 offen lds
	s_mov_b32 m0, s36
	s_nop 0
	buffer_load_dwordx4 v133, s[64:67], s73 offen lds
	s_add_i32 s73, s73, 0xb0000
	s_mov_b32 m0, s40
	s_nop 0
	buffer_load_dwordx4 v131, s[64:67], s73 offen lds
	s_mov_b32 m0, s44
	s_nop 0
	buffer_load_dwordx4 v133, s[64:67], s73 offen lds
	s_waitcnt vmcnt(8)
	s_waitcnt lgkmcnt(0)
	s_barrier
	s_setprio 1
	s_waitcnt lgkmcnt(6)
	v_mfma_scale_f32_16x16x128_f8f6f4 v[114:117], v[18:25], v[174:181], v[114:117], v237, v237 op_sel_hi:[0,0,0]
	v_mfma_scale_f32_16x16x128_f8f6f4 v[118:121], v[26:33], v[174:181], v[118:121], v237, v237 op_sel_hi:[0,0,0]
	s_waitcnt lgkmcnt(4)
	v_mfma_scale_f32_16x16x128_f8f6f4 v[54:57], v[18:25], v[182:189], v[54:57], v237, v237 op_sel_hi:[0,0,0]
	v_mfma_scale_f32_16x16x128_f8f6f4 v[50:53], v[26:33], v[182:189], v[50:53], v237, v237 op_sel_hi:[0,0,0]
	s_waitcnt lgkmcnt(2)
	v_mfma_scale_f32_16x16x128_f8f6f4 v[46:49], v[18:25], v[190:197], v[46:49], v237, v237 op_sel_hi:[0,0,0]
	v_mfma_scale_f32_16x16x128_f8f6f4 v[42:45], v[26:33], v[190:197], v[42:45], v237, v237 op_sel_hi:[0,0,0]
	s_waitcnt lgkmcnt(0)
	v_mfma_scale_f32_16x16x128_f8f6f4 v[38:41], v[18:25], v[204:211], v[38:41], v237, v237 op_sel_hi:[0,0,0]
	v_mfma_scale_f32_16x16x128_f8f6f4 v[34:37], v[26:33], v[204:211], v[34:37], v237, v237 op_sel_hi:[0,0,0]
	v_mfma_scale_f32_16x16x128_f8f6f4 v[58:61], v[10:17], v[174:181], v[58:61], v237, v237 op_sel_hi:[0,0,0]
	v_mfma_scale_f32_16x16x128_f8f6f4 v[62:65], v[2:9], v[174:181], v[62:65], v237, v237 op_sel_hi:[0,0,0]
	v_mfma_scale_f32_16x16x128_f8f6f4 v[110:113], v[10:17], v[182:189], v[110:113], v237, v237 op_sel_hi:[0,0,0]
	v_mfma_scale_f32_16x16x128_f8f6f4 v[106:109], v[2:9], v[182:189], v[106:109], v237, v237 op_sel_hi:[0,0,0]
	v_mfma_scale_f32_16x16x128_f8f6f4 v[102:105], v[10:17], v[190:197], v[102:105], v237, v237 op_sel_hi:[0,0,0]
	v_mfma_scale_f32_16x16x128_f8f6f4 v[98:101], v[2:9], v[190:197], v[98:101], v237, v237 op_sel_hi:[0,0,0]
	v_mfma_scale_f32_16x16x128_f8f6f4 v[162:165], v[10:17], v[204:211], v[162:165], v237, v237 op_sel_hi:[0,0,0]
	v_mfma_scale_f32_16x16x128_f8f6f4 v[94:97], v[2:9], v[204:211], v[94:97], v237, v237 op_sel_hi:[0,0,0]
	s_setprio 0
	s_barrier
	s_mov_b32 m0, s46
	s_or_b32 s73, s72, 0x80
	ds_read_b128 v[174:177], v136 offset:49152
	ds_read_b128 v[178:181], v136 offset:50176
	ds_read_b128 v[182:185], v136 offset:51200
	ds_read_b128 v[186:189], v136 offset:52224
	ds_read_b128 v[190:193], v136 offset:53248
	ds_read_b128 v[194:197], v136 offset:54272
	ds_read_b128 v[204:207], v136 offset:55296
	ds_read_b128 v[208:211], v136 offset:56320
	buffer_load_dwordx4 v132, s[4:7], s73 offen lds
	s_mov_b32 m0, s47
	s_add_i32 s72, s72, 0xb0080
	buffer_load_dwordx4 v134, s[4:7], s73 offen lds
	s_mov_b32 m0, s48
	s_nop 0
	buffer_load_dwordx4 v132, s[4:7], s72 offen lds
	s_mov_b32 m0, s49
	s_nop 0
	buffer_load_dwordx4 v134, s[4:7], s72 offen lds
	s_waitcnt vmcnt(6)
	s_waitcnt lgkmcnt(0)
	s_barrier
	s_setprio 1
	s_waitcnt lgkmcnt(6)
	v_mfma_scale_f32_16x16x128_f8f6f4 v[154:157], v[18:25], v[174:181], v[154:157], v237, v237 op_sel_hi:[0,0,0]
	v_mfma_scale_f32_16x16x128_f8f6f4 v[90:93], v[26:33], v[174:181], v[90:93], v237, v237 op_sel_hi:[0,0,0]
	s_waitcnt lgkmcnt(4)
	v_mfma_scale_f32_16x16x128_f8f6f4 v[86:89], v[18:25], v[182:189], v[86:89], v237, v237 op_sel_hi:[0,0,0]
	v_mfma_scale_f32_16x16x128_f8f6f4 v[82:85], v[26:33], v[182:189], v[82:85], v237, v237 op_sel_hi:[0,0,0]
	s_waitcnt lgkmcnt(2)
	v_mfma_scale_f32_16x16x128_f8f6f4 v[78:81], v[18:25], v[190:197], v[78:81], v237, v237 op_sel_hi:[0,0,0]
	v_mfma_scale_f32_16x16x128_f8f6f4 v[74:77], v[26:33], v[190:197], v[74:77], v237, v237 op_sel_hi:[0,0,0]
	s_waitcnt lgkmcnt(0)
	v_mfma_scale_f32_16x16x128_f8f6f4 v[70:73], v[18:25], v[204:211], v[70:73], v237, v237 op_sel_hi:[0,0,0]
	v_mfma_scale_f32_16x16x128_f8f6f4 v[66:69], v[26:33], v[204:211], v[66:69], v237, v237 op_sel_hi:[0,0,0]
	v_mfma_scale_f32_16x16x128_f8f6f4 v[166:169], v[10:17], v[174:181], v[166:169], v237, v237 op_sel_hi:[0,0,0]
	v_mfma_scale_f32_16x16x128_f8f6f4 v[158:161], v[2:9], v[174:181], v[158:161], v237, v237 op_sel_hi:[0,0,0]
	v_mfma_scale_f32_16x16x128_f8f6f4 v[150:153], v[10:17], v[182:189], v[150:153], v237, v237 op_sel_hi:[0,0,0]
	v_mfma_scale_f32_16x16x128_f8f6f4 v[146:149], v[2:9], v[182:189], v[146:149], v237, v237 op_sel_hi:[0,0,0]
	v_mfma_scale_f32_16x16x128_f8f6f4 v[142:145], v[10:17], v[190:197], v[142:145], v237, v237 op_sel_hi:[0,0,0]
	v_mfma_scale_f32_16x16x128_f8f6f4 v[138:141], v[2:9], v[190:197], v[138:141], v237, v237 op_sel_hi:[0,0,0]
	v_mfma_scale_f32_16x16x128_f8f6f4 v[126:129], v[10:17], v[204:211], v[126:129], v237, v237 op_sel_hi:[0,0,0]
	v_mfma_scale_f32_16x16x128_f8f6f4 v[122:125], v[2:9], v[204:211], v[122:125], v237, v237 op_sel_hi:[0,0,0]
	s_setprio 0
	s_barrier
	s_add_i32 s62, s62, 2
	s_addk_i32 s63, 0x100
	s_cmp_gt_u32 s62, 41
	s_cbranch_scc0 .LBB0_412
	s_branch .Lex_3
.Lfin_3:
	s_add_i32 s77, s76, 0x1580
	s_mov_b32 m0, s50
	ds_read_b128 v[174:177], v136
	ds_read_b128 v[178:181], v136 offset:1024
	ds_read_b128 v[182:185], v136 offset:2048
	ds_read_b128 v[186:189], v136 offset:3072
	ds_read_b128 v[190:193], v136 offset:4096
	ds_read_b128 v[194:197], v136 offset:5120
	ds_read_b128 v[204:207], v136 offset:6144
	ds_read_b128 v[208:211], v136 offset:7168
	buffer_load_dwordx4 v131, s[64:67], s77 offen lds
	s_mov_b32 m0, s52
	s_add_i32 s76, s76, 0xb1580
	buffer_load_dwordx4 v133, s[64:67], s77 offen lds
	s_mov_b32 m0, s51
	s_nop 0
	buffer_load_dwordx4 v131, s[64:67], s76 offen lds
	s_mov_b32 m0, s53
	s_nop 0
	buffer_load_dwordx4 v133, s[64:67], s76 offen lds
	s_waitcnt vmcnt(8)
	s_waitcnt lgkmcnt(0)
	s_barrier
	s_setprio 1
	s_waitcnt lgkmcnt(6)
	v_mfma_scale_f32_16x16x128_f8f6f4 v[114:117], v[2:9], v[174:181], v[114:117], v237, v237 op_sel_hi:[0,0,0]
	v_mfma_scale_f32_16x16x128_f8f6f4 v[118:121], v[10:17], v[174:181], v[118:121], v237, v237 op_sel_hi:[0,0,0]
	s_waitcnt lgkmcnt(4)
	v_mfma_scale_f32_16x16x128_f8f6f4 v[54:57], v[2:9], v[182:189], v[54:57], v237, v237 op_sel_hi:[0,0,0]
	v_mfma_scale_f32_16x16x128_f8f6f4 v[50:53], v[10:17], v[182:189], v[50:53], v237, v237 op_sel_hi:[0,0,0]
	s_waitcnt lgkmcnt(2)
	v_mfma_scale_f32_16x16x128_f8f6f4 v[46:49], v[2:9], v[190:197], v[46:49], v237, v237 op_sel_hi:[0,0,0]
	v_mfma_scale_f32_16x16x128_f8f6f4 v[42:45], v[10:17], v[190:197], v[42:45], v237, v237 op_sel_hi:[0,0,0]
	s_waitcnt lgkmcnt(0)
	v_mfma_scale_f32_16x16x128_f8f6f4 v[38:41], v[2:9], v[204:211], v[38:41], v237, v237 op_sel_hi:[0,0,0]
	v_mfma_scale_f32_16x16x128_f8f6f4 v[34:37], v[10:17], v[204:211], v[34:37], v237, v237 op_sel_hi:[0,0,0]
	v_mfma_scale_f32_16x16x128_f8f6f4 v[58:61], v[18:25], v[174:181], v[58:61], v237, v237 op_sel_hi:[0,0,0]
	v_mfma_scale_f32_16x16x128_f8f6f4 v[62:65], v[26:33], v[174:181], v[62:65], v237, v237 op_sel_hi:[0,0,0]
	v_mfma_scale_f32_16x16x128_f8f6f4 v[110:113], v[18:25], v[182:189], v[110:113], v237, v237 op_sel_hi:[0,0,0]
	v_mfma_scale_f32_16x16x128_f8f6f4 v[106:109], v[26:33], v[182:189], v[106:109], v237, v237 op_sel_hi:[0,0,0]
	v_mfma_scale_f32_16x16x128_f8f6f4 v[102:105], v[18:25], v[190:197], v[102:105], v237, v237 op_sel_hi:[0,0,0]
	v_mfma_scale_f32_16x16x128_f8f6f4 v[98:101], v[26:33], v[190:197], v[98:101], v237, v237 op_sel_hi:[0,0,0]
	v_mfma_scale_f32_16x16x128_f8f6f4 v[162:165], v[18:25], v[204:211], v[162:165], v237, v237 op_sel_hi:[0,0,0]
	v_mfma_scale_f32_16x16x128_f8f6f4 v[94:97], v[26:33], v[204:211], v[94:97], v237, v237 op_sel_hi:[0,0,0]
	s_setprio 0
	s_barrier
	s_mov_b32 m0, s12
	ds_read_b128 v[174:177], v136 offset:16384
	ds_read_b128 v[178:181], v136 offset:17408
	ds_read_b128 v[182:185], v136 offset:18432
	ds_read_b128 v[186:189], v136 offset:19456
	ds_read_b128 v[190:193], v136 offset:20480
	ds_read_b128 v[194:197], v136 offset:21504
	ds_read_b128 v[204:207], v136 offset:22528
	ds_read_b128 v[208:211], v136 offset:23552
	s_mov_b32 m0, s31
	s_add_i32 s76, s72, 0xb0000
	s_mov_b32 m0, s34
	s_nop 0
	s_mov_b32 m0, s35
	s_nop 0
	s_waitcnt vmcnt(0)
	s_waitcnt lgkmcnt(0)
	s_barrier
	s_setprio 1
	s_waitcnt lgkmcnt(6)
	v_mfma_scale_f32_16x16x128_f8f6f4 v[154:157], v[2:9], v[174:181], v[154:157], v237, v237 op_sel_hi:[0,0,0]
	v_mfma_scale_f32_16x16x128_f8f6f4 v[90:93], v[10:17], v[174:181], v[90:93], v237, v237 op_sel_hi:[0,0,0]
	s_waitcnt lgkmcnt(4)
	v_mfma_scale_f32_16x16x128_f8f6f4 v[86:89], v[2:9], v[182:189], v[86:89], v237, v237 op_sel_hi:[0,0,0]
	v_mfma_scale_f32_16x16x128_f8f6f4 v[82:85], v[10:17], v[182:189], v[82:85], v237, v237 op_sel_hi:[0,0,0]
	s_waitcnt lgkmcnt(2)
	v_mfma_scale_f32_16x16x128_f8f6f4 v[78:81], v[2:9], v[190:197], v[78:81], v237, v237 op_sel_hi:[0,0,0]
	v_mfma_scale_f32_16x16x128_f8f6f4 v[74:77], v[10:17], v[190:197], v[74:77], v237, v237 op_sel_hi:[0,0,0]
	s_waitcnt lgkmcnt(0)
	v_mfma_scale_f32_16x16x128_f8f6f4 v[70:73], v[2:9], v[204:211], v[70:73], v237, v237 op_sel_hi:[0,0,0]
	v_mfma_scale_f32_16x16x128_f8f6f4 v[66:69], v[10:17], v[204:211], v[66:69], v237, v237 op_sel_hi:[0,0,0]
	v_mfma_scale_f32_16x16x128_f8f6f4 v[166:169], v[18:25], v[174:181], v[166:169], v237, v237 op_sel_hi:[0,0,0]
	v_mfma_scale_f32_16x16x128_f8f6f4 v[158:161], v[26:33], v[174:181], v[158:161], v237, v237 op_sel_hi:[0,0,0]
	v_mfma_scale_f32_16x16x128_f8f6f4 v[150:153], v[18:25], v[182:189], v[150:153], v237, v237 op_sel_hi:[0,0,0]
	v_mfma_scale_f32_16x16x128_f8f6f4 v[146:149], v[26:33], v[182:189], v[146:149], v237, v237 op_sel_hi:[0,0,0]
	v_mfma_scale_f32_16x16x128_f8f6f4 v[142:145], v[18:25], v[190:197], v[142:145], v237, v237 op_sel_hi:[0,0,0]
	v_mfma_scale_f32_16x16x128_f8f6f4 v[138:141], v[26:33], v[190:197], v[138:141], v237, v237 op_sel_hi:[0,0,0]
	v_mfma_scale_f32_16x16x128_f8f6f4 v[126:129], v[18:25], v[204:211], v[126:129], v237, v237 op_sel_hi:[0,0,0]
	v_mfma_scale_f32_16x16x128_f8f6f4 v[122:125], v[26:33], v[204:211], v[122:125], v237, v237 op_sel_hi:[0,0,0]
	s_setprio 0
	s_barrier
	ds_read_b128 v[18:21], v171
	ds_read_b128 v[22:25], v171 offset:1024
	ds_read_b128 v[26:29], v171 offset:2048
	ds_read_b128 v[30:33], v171 offset:3072
	ds_read_b128 v[10:13], v172
	ds_read_b128 v[14:17], v172 offset:1024
	ds_read_b128 v[2:5], v172 offset:2048
	ds_read_b128 v[6:9], v172 offset:3072
	s_mov_b32 m0, s11
	ds_read_b128 v[174:177], v136 offset:32768
	ds_read_b128 v[178:181], v136 offset:33792
	ds_read_b128 v[182:185], v136 offset:34816
	ds_read_b128 v[186:189], v136 offset:35840
	ds_read_b128 v[190:193], v136 offset:36864
	ds_read_b128 v[194:197], v136 offset:37888
	ds_read_b128 v[204:207], v136 offset:38912
	ds_read_b128 v[208:211], v136 offset:39936
	s_mov_b32 m0, s36
	s_nop 0
	s_add_i32 s73, s73, 0xb0000
	s_mov_b32 m0, s40
	s_nop 0
	s_mov_b32 m0, s44
	s_nop 0
	s_waitcnt vmcnt(8)
	s_waitcnt lgkmcnt(0)
	s_barrier
	s_setprio 1
	s_waitcnt lgkmcnt(6)
	v_mfma_scale_f32_16x16x128_f8f6f4 v[114:117], v[18:25], v[174:181], v[114:117], v237, v237 op_sel_hi:[0,0,0]
	v_mfma_scale_f32_16x16x128_f8f6f4 v[118:121], v[26:33], v[174:181], v[118:121], v237, v237 op_sel_hi:[0,0,0]
	s_waitcnt lgkmcnt(4)
	v_mfma_scale_f32_16x16x128_f8f6f4 v[54:57], v[18:25], v[182:189], v[54:57], v237, v237 op_sel_hi:[0,0,0]
	v_mfma_scale_f32_16x16x128_f8f6f4 v[50:53], v[26:33], v[182:189], v[50:53], v237, v237 op_sel_hi:[0,0,0]
	s_waitcnt lgkmcnt(2)
	v_mfma_scale_f32_16x16x128_f8f6f4 v[46:49], v[18:25], v[190:197], v[46:49], v237, v237 op_sel_hi:[0,0,0]
	v_mfma_scale_f32_16x16x128_f8f6f4 v[42:45], v[26:33], v[190:197], v[42:45], v237, v237 op_sel_hi:[0,0,0]
	s_waitcnt lgkmcnt(0)
	v_mfma_scale_f32_16x16x128_f8f6f4 v[38:41], v[18:25], v[204:211], v[38:41], v237, v237 op_sel_hi:[0,0,0]
	v_mfma_scale_f32_16x16x128_f8f6f4 v[34:37], v[26:33], v[204:211], v[34:37], v237, v237 op_sel_hi:[0,0,0]
	v_mfma_scale_f32_16x16x128_f8f6f4 v[58:61], v[10:17], v[174:181], v[58:61], v237, v237 op_sel_hi:[0,0,0]
	v_mfma_scale_f32_16x16x128_f8f6f4 v[62:65], v[2:9], v[174:181], v[62:65], v237, v237 op_sel_hi:[0,0,0]
	v_mfma_scale_f32_16x16x128_f8f6f4 v[110:113], v[10:17], v[182:189], v[110:113], v237, v237 op_sel_hi:[0,0,0]
	v_mfma_scale_f32_16x16x128_f8f6f4 v[106:109], v[2:9], v[182:189], v[106:109], v237, v237 op_sel_hi:[0,0,0]
	v_mfma_scale_f32_16x16x128_f8f6f4 v[102:105], v[10:17], v[190:197], v[102:105], v237, v237 op_sel_hi:[0,0,0]
	v_mfma_scale_f32_16x16x128_f8f6f4 v[98:101], v[2:9], v[190:197], v[98:101], v237, v237 op_sel_hi:[0,0,0]
	v_mfma_scale_f32_16x16x128_f8f6f4 v[162:165], v[10:17], v[204:211], v[162:165], v237, v237 op_sel_hi:[0,0,0]
	v_mfma_scale_f32_16x16x128_f8f6f4 v[94:97], v[2:9], v[204:211], v[94:97], v237, v237 op_sel_hi:[0,0,0]
	s_setprio 0
	s_barrier
	s_mov_b32 m0, s46
	s_or_b32 s73, s72, 0x80
	ds_read_b128 v[174:177], v136 offset:49152
	ds_read_b128 v[178:181], v136 offset:50176
	ds_read_b128 v[182:185], v136 offset:51200
	ds_read_b128 v[186:189], v136 offset:52224
	ds_read_b128 v[190:193], v136 offset:53248
	ds_read_b128 v[194:197], v136 offset:54272
	ds_read_b128 v[204:207], v136 offset:55296
	ds_read_b128 v[208:211], v136 offset:56320
	s_mov_b32 m0, s47
	s_add_i32 s72, s72, 0xb0080
	s_mov_b32 m0, s48
	s_nop 0
	s_mov_b32 m0, s49
	s_nop 0
	s_waitcnt vmcnt(6)
	s_waitcnt lgkmcnt(0)
	s_barrier
	s_setprio 1
	s_waitcnt lgkmcnt(6)
	v_mfma_scale_f32_16x16x128_f8f6f4 v[154:157], v[18:25], v[174:181], v[154:157], v237, v237 op_sel_hi:[0,0,0]
	v_mfma_scale_f32_16x16x128_f8f6f4 v[90:93], v[26:33], v[174:181], v[90:93], v237, v237 op_sel_hi:[0,0,0]
	s_waitcnt lgkmcnt(4)
	v_mfma_scale_f32_16x16x128_f8f6f4 v[86:89], v[18:25], v[182:189], v[86:89], v237, v237 op_sel_hi:[0,0,0]
	v_mfma_scale_f32_16x16x128_f8f6f4 v[82:85], v[26:33], v[182:189], v[82:85], v237, v237 op_sel_hi:[0,0,0]
	s_waitcnt lgkmcnt(2)
	v_mfma_scale_f32_16x16x128_f8f6f4 v[78:81], v[18:25], v[190:197], v[78:81], v237, v237 op_sel_hi:[0,0,0]
	v_mfma_scale_f32_16x16x128_f8f6f4 v[74:77], v[26:33], v[190:197], v[74:77], v237, v237 op_sel_hi:[0,0,0]
	s_waitcnt lgkmcnt(0)
	v_mfma_scale_f32_16x16x128_f8f6f4 v[70:73], v[18:25], v[204:211], v[70:73], v237, v237 op_sel_hi:[0,0,0]
	v_mfma_scale_f32_16x16x128_f8f6f4 v[66:69], v[26:33], v[204:211], v[66:69], v237, v237 op_sel_hi:[0,0,0]
	v_mfma_scale_f32_16x16x128_f8f6f4 v[166:169], v[10:17], v[174:181], v[166:169], v237, v237 op_sel_hi:[0,0,0]
	v_mfma_scale_f32_16x16x128_f8f6f4 v[158:161], v[2:9], v[174:181], v[158:161], v237, v237 op_sel_hi:[0,0,0]
	v_mfma_scale_f32_16x16x128_f8f6f4 v[150:153], v[10:17], v[182:189], v[150:153], v237, v237 op_sel_hi:[0,0,0]
	v_mfma_scale_f32_16x16x128_f8f6f4 v[146:149], v[2:9], v[182:189], v[146:149], v237, v237 op_sel_hi:[0,0,0]
	v_mfma_scale_f32_16x16x128_f8f6f4 v[142:145], v[10:17], v[190:197], v[142:145], v237, v237 op_sel_hi:[0,0,0]
	v_mfma_scale_f32_16x16x128_f8f6f4 v[138:141], v[2:9], v[190:197], v[138:141], v237, v237 op_sel_hi:[0,0,0]
	v_mfma_scale_f32_16x16x128_f8f6f4 v[126:129], v[10:17], v[204:211], v[126:129], v237, v237 op_sel_hi:[0,0,0]
	v_mfma_scale_f32_16x16x128_f8f6f4 v[122:125], v[2:9], v[204:211], v[122:125], v237, v237 op_sel_hi:[0,0,0]
	s_setprio 0
	s_barrier
	s_add_i32 s62, s62, 2
	s_addk_i32 s63, 0x100
	s_cmp_gt_u32 s62, 41
.Lex_3:
	s_nop 15
	s_nop 15
	s_and_b64 vcc, exec, s[28:29]
	s_cbranch_vccz .LBB0_408
	s_mov_b32 s10, s55
	s_mov_b32 s0, s56
	s_mov_b32 s13, s59
	s_mov_b32 s37, s58
	s_mov_b32 s54, s57
	s_branch .LBB0_408

.LBB0_573:
	ds_read_b128 v[142:145], v137
	ds_read_b128 v[146:149], v137 offset:1024
	ds_read_b128 v[150:153], v137 offset:2048
	ds_read_b128 v[154:157], v137 offset:3072
	ds_read_b128 v[158:161], v138
	ds_read_b128 v[162:165], v138 offset:1024
	ds_read_b128 v[166:169], v138 offset:2048
	ds_read_b128 v[170:173], v138 offset:3072
	s_add_i32 s61, s35, s59
	s_add_i32 s60, s28, s59
	s_add_i32 s62, s61, 0x2c00
	s_addk_i32 s60, 0x2c00
	s_cmp_eq_u32 s59, 0
	s_cselect_b32 s60, s57, s60
	s_cselect_b32 s62, s56, s62
	s_cbranch_scc0 .Lnx_4
	s_cmp_eq_u64 s[26:27], 0
	s_cbranch_scc1 .Lfin_4
.Lnx_4:
	s_add_i32 s63, s61, 0x2b80
	s_mov_b32 m0, s46
	ds_read_b128 v[174:177], v136
	ds_read_b128 v[178:181], v136 offset:1024
	ds_read_b128 v[182:185], v136 offset:2048
	ds_read_b128 v[186:189], v136 offset:3072
	ds_read_b128 v[190:193], v136 offset:4096
	ds_read_b128 v[194:197], v136 offset:5120
	ds_read_b128 v[198:201], v136 offset:6144
	ds_read_b128 v[204:207], v136 offset:7168
	buffer_load_dwordx4 v127, s[64:67], s63 offen lds
	s_mov_b32 m0, s48
	s_add_i32 s61, s61, 0x162b80
	buffer_load_dwordx4 v129, s[64:67], s63 offen lds
	s_mov_b32 m0, s47
	s_nop 0
	buffer_load_dwordx4 v127, s[64:67], s61 offen lds
	s_mov_b32 m0, s49
	s_nop 0
	buffer_load_dwordx4 v129, s[64:67], s61 offen lds
	s_waitcnt vmcnt(8)
	s_waitcnt lgkmcnt(0)
	s_barrier
	s_setprio 1
	s_waitcnt lgkmcnt(7)
	v_mfma_f32_16x16x32_bf16 v[122:125], v[142:145], v[174:177], v[122:125]
	v_mfma_f32_16x16x32_bf16 v[118:121], v[150:153], v[174:177], v[118:121]
	s_waitcnt lgkmcnt(5)
	v_mfma_f32_16x16x32_bf16 v[114:117], v[142:145], v[182:185], v[114:117]
	v_mfma_f32_16x16x32_bf16 v[110:113], v[150:153], v[182:185], v[110:113]
	s_waitcnt lgkmcnt(3)
	v_mfma_f32_16x16x32_bf16 v[98:101], v[142:145], v[190:193], v[98:101]
	v_mfma_f32_16x16x32_bf16 v[106:109], v[150:153], v[190:193], v[106:109]
	s_waitcnt lgkmcnt(1)
	v_mfma_f32_16x16x32_bf16 v[102:105], v[142:145], v[198:201], v[102:105]
	v_mfma_f32_16x16x32_bf16 v[2:5], v[150:153], v[198:201], v[2:5]
	v_mfma_f32_16x16x32_bf16 v[30:33], v[158:161], v[174:177], v[30:33]
	v_mfma_f32_16x16x32_bf16 v[34:37], v[166:169], v[174:177], v[34:37]
	v_mfma_f32_16x16x32_bf16 v[10:13], v[158:161], v[182:185], v[10:13]
	v_mfma_f32_16x16x32_bf16 v[14:17], v[166:169], v[182:185], v[14:17]
	v_mfma_f32_16x16x32_bf16 v[18:21], v[158:161], v[190:193], v[18:21]
	v_mfma_f32_16x16x32_bf16 v[22:25], v[166:169], v[190:193], v[22:25]
	v_mfma_f32_16x16x32_bf16 v[94:97], v[158:161], v[198:201], v[94:97]
	v_mfma_f32_16x16x32_bf16 v[6:9], v[166:169], v[198:201], v[6:9]
	v_mfma_f32_16x16x32_bf16 v[122:125], v[146:149], v[178:181], v[122:125]
	v_mfma_f32_16x16x32_bf16 v[118:121], v[154:157], v[178:181], v[118:121]
	v_mfma_f32_16x16x32_bf16 v[114:117], v[146:149], v[186:189], v[114:117]
	v_mfma_f32_16x16x32_bf16 v[110:113], v[154:157], v[186:189], v[110:113]
	v_mfma_f32_16x16x32_bf16 v[98:101], v[146:149], v[194:197], v[98:101]
	v_mfma_f32_16x16x32_bf16 v[106:109], v[154:157], v[194:197], v[106:109]
	s_waitcnt lgkmcnt(0)
	v_mfma_f32_16x16x32_bf16 v[102:105], v[146:149], v[204:207], v[102:105]
	v_mfma_f32_16x16x32_bf16 v[2:5], v[154:157], v[204:207], v[2:5]
	v_mfma_f32_16x16x32_bf16 v[30:33], v[162:165], v[178:181], v[30:33]
	v_mfma_f32_16x16x32_bf16 v[34:37], v[170:173], v[178:181], v[34:37]
	v_mfma_f32_16x16x32_bf16 v[10:13], v[162:165], v[186:189], v[10:13]
	v_mfma_f32_16x16x32_bf16 v[14:17], v[170:173], v[186:189], v[14:17]
	v_mfma_f32_16x16x32_bf16 v[18:21], v[162:165], v[194:197], v[18:21]
	v_mfma_f32_16x16x32_bf16 v[22:25], v[170:173], v[194:197], v[22:25]
	v_mfma_f32_16x16x32_bf16 v[94:97], v[162:165], v[204:207], v[94:97]
	v_mfma_f32_16x16x32_bf16 v[6:9], v[170:173], v[204:207], v[6:9]
	s_setprio 0
	s_barrier
	s_mov_b32 m0, s13
	ds_read_b128 v[174:177], v136 offset:16384
	ds_read_b128 v[178:181], v136 offset:17408
	ds_read_b128 v[182:185], v136 offset:18432
	ds_read_b128 v[186:189], v136 offset:19456
	ds_read_b128 v[190:193], v136 offset:20480
	ds_read_b128 v[194:197], v136 offset:21504
	ds_read_b128 v[198:201], v136 offset:22528
	ds_read_b128 v[204:207], v136 offset:23552
	buffer_load_dwordx4 v128, s[4:7], s60 offen lds
	s_mov_b32 m0, s29
	s_add_i32 s61, s60, 0x160000
	buffer_load_dwordx4 v134, s[4:7], s60 offen lds
	s_mov_b32 m0, s30
	s_nop 0
	buffer_load_dwordx4 v128, s[4:7], s61 offen lds
	s_mov_b32 m0, s31
	s_nop 0
	buffer_load_dwordx4 v134, s[4:7], s61 offen lds
	s_waitcnt vmcnt(6)
	s_waitcnt lgkmcnt(0)
	s_barrier
	s_setprio 1
	s_waitcnt lgkmcnt(7)
	v_mfma_f32_16x16x32_bf16 v[74:77], v[142:145], v[174:177], v[74:77]
	v_mfma_f32_16x16x32_bf16 v[82:85], v[150:153], v[174:177], v[82:85]
	s_waitcnt lgkmcnt(5)
	v_mfma_f32_16x16x32_bf16 v[66:69], v[142:145], v[182:185], v[66:69]
	v_mfma_f32_16x16x32_bf16 v[70:73], v[150:153], v[182:185], v[70:73]
	s_waitcnt lgkmcnt(3)
	v_mfma_f32_16x16x32_bf16 v[90:93], v[142:145], v[190:193], v[90:93]
	v_mfma_f32_16x16x32_bf16 v[50:53], v[150:153], v[190:193], v[50:53]
	s_waitcnt lgkmcnt(1)
	v_mfma_f32_16x16x32_bf16 v[78:81], v[142:145], v[198:201], v[78:81]
	v_mfma_f32_16x16x32_bf16 v[42:45], v[150:153], v[198:201], v[42:45]
	v_mfma_f32_16x16x32_bf16 v[26:29], v[158:161], v[174:177], v[26:29]
	v_mfma_f32_16x16x32_bf16 v[38:41], v[166:169], v[174:177], v[38:41]
	v_mfma_f32_16x16x32_bf16 v[58:61], v[158:161], v[182:185], v[58:61]
	v_mfma_f32_16x16x32_bf16 v[62:65], v[166:169], v[182:185], v[62:65]
	v_mfma_f32_16x16x32_bf16 v[86:89], v[158:161], v[190:193], v[86:89]
	v_mfma_f32_16x16x32_bf16 v[54:57], v[166:169], v[190:193], v[54:57]
	v_mfma_f32_16x16x32_bf16 v[130:133], v[158:161], v[198:201], v[130:133]
	v_mfma_f32_16x16x32_bf16 v[46:49], v[166:169], v[198:201], v[46:49]
	v_mfma_f32_16x16x32_bf16 v[74:77], v[146:149], v[178:181], v[74:77]
	v_mfma_f32_16x16x32_bf16 v[82:85], v[154:157], v[178:181], v[82:85]
	v_mfma_f32_16x16x32_bf16 v[66:69], v[146:149], v[186:189], v[66:69]
	v_mfma_f32_16x16x32_bf16 v[70:73], v[154:157], v[186:189], v[70:73]
	v_mfma_f32_16x16x32_bf16 v[90:93], v[146:149], v[194:197], v[90:93]
	v_mfma_f32_16x16x32_bf16 v[50:53], v[154:157], v[194:197], v[50:53]
	s_waitcnt lgkmcnt(0)
	v_mfma_f32_16x16x32_bf16 v[78:81], v[146:149], v[204:207], v[78:81]
	v_mfma_f32_16x16x32_bf16 v[42:45], v[154:157], v[204:207], v[42:45]
	v_mfma_f32_16x16x32_bf16 v[26:29], v[162:165], v[178:181], v[26:29]
	v_mfma_f32_16x16x32_bf16 v[38:41], v[170:173], v[178:181], v[38:41]
	v_mfma_f32_16x16x32_bf16 v[58:61], v[162:165], v[186:189], v[58:61]
	v_mfma_f32_16x16x32_bf16 v[62:65], v[170:173], v[186:189], v[62:65]
	v_mfma_f32_16x16x32_bf16 v[86:89], v[162:165], v[194:197], v[86:89]
	v_mfma_f32_16x16x32_bf16 v[54:57], v[170:173], v[194:197], v[54:57]
	v_mfma_f32_16x16x32_bf16 v[130:133], v[162:165], v[204:207], v[130:133]
	v_mfma_f32_16x16x32_bf16 v[46:49], v[170:173], v[204:207], v[46:49]
	s_setprio 0
	s_barrier
	ds_read_b128 v[142:145], v139
	ds_read_b128 v[146:149], v139 offset:1024
	ds_read_b128 v[150:153], v139 offset:2048
	ds_read_b128 v[154:157], v139 offset:3072
	ds_read_b128 v[158:161], v140
	ds_read_b128 v[162:165], v140 offset:1024
	ds_read_b128 v[166:169], v140 offset:2048
	ds_read_b128 v[170:173], v140 offset:3072
	s_mov_b32 m0, s12
	ds_read_b128 v[174:177], v136 offset:32768
	ds_read_b128 v[178:181], v136 offset:33792
	ds_read_b128 v[182:185], v136 offset:34816
	ds_read_b128 v[186:189], v136 offset:35840
	ds_read_b128 v[190:193], v136 offset:36864
	ds_read_b128 v[194:197], v136 offset:37888
	ds_read_b128 v[198:201], v136 offset:38912
	ds_read_b128 v[204:207], v136 offset:39936
	buffer_load_dwordx4 v127, s[64:67], s62 offen lds
	s_mov_b32 m0, s34
	s_nop 0
	buffer_load_dwordx4 v129, s[64:67], s62 offen lds
	s_add_i32 s62, s62, 0x160000
	s_mov_b32 m0, s36
	s_nop 0
	buffer_load_dwordx4 v127, s[64:67], s62 offen lds
	s_mov_b32 m0, s37
	s_nop 0
	buffer_load_dwordx4 v129, s[64:67], s62 offen lds
	s_waitcnt vmcnt(8)
	s_waitcnt lgkmcnt(0)
	s_barrier
	s_setprio 1
	s_waitcnt lgkmcnt(7)
	v_mfma_f32_16x16x32_bf16 v[122:125], v[142:145], v[174:177], v[122:125]
	v_mfma_f32_16x16x32_bf16 v[118:121], v[150:153], v[174:177], v[118:121]
	s_waitcnt lgkmcnt(5)
	v_mfma_f32_16x16x32_bf16 v[114:117], v[142:145], v[182:185], v[114:117]
	v_mfma_f32_16x16x32_bf16 v[110:113], v[150:153], v[182:185], v[110:113]
	s_waitcnt lgkmcnt(3)
	v_mfma_f32_16x16x32_bf16 v[98:101], v[142:145], v[190:193], v[98:101]
	v_mfma_f32_16x16x32_bf16 v[106:109], v[150:153], v[190:193], v[106:109]
	s_waitcnt lgkmcnt(1)
	v_mfma_f32_16x16x32_bf16 v[102:105], v[142:145], v[198:201], v[102:105]
	v_mfma_f32_16x16x32_bf16 v[2:5], v[150:153], v[198:201], v[2:5]
	v_mfma_f32_16x16x32_bf16 v[30:33], v[158:161], v[174:177], v[30:33]
	v_mfma_f32_16x16x32_bf16 v[34:37], v[166:169], v[174:177], v[34:37]
	v_mfma_f32_16x16x32_bf16 v[10:13], v[158:161], v[182:185], v[10:13]
	v_mfma_f32_16x16x32_bf16 v[14:17], v[166:169], v[182:185], v[14:17]
	v_mfma_f32_16x16x32_bf16 v[18:21], v[158:161], v[190:193], v[18:21]
	v_mfma_f32_16x16x32_bf16 v[22:25], v[166:169], v[190:193], v[22:25]
	v_mfma_f32_16x16x32_bf16 v[94:97], v[158:161], v[198:201], v[94:97]
	v_mfma_f32_16x16x32_bf16 v[6:9], v[166:169], v[198:201], v[6:9]
	v_mfma_f32_16x16x32_bf16 v[122:125], v[146:149], v[178:181], v[122:125]
	v_mfma_f32_16x16x32_bf16 v[118:121], v[154:157], v[178:181], v[118:121]
	v_mfma_f32_16x16x32_bf16 v[114:117], v[146:149], v[186:189], v[114:117]
	v_mfma_f32_16x16x32_bf16 v[110:113], v[154:157], v[186:189], v[110:113]
	v_mfma_f32_16x16x32_bf16 v[98:101], v[146:149], v[194:197], v[98:101]
	v_mfma_f32_16x16x32_bf16 v[106:109], v[154:157], v[194:197], v[106:109]
	s_waitcnt lgkmcnt(0)
	v_mfma_f32_16x16x32_bf16 v[102:105], v[146:149], v[204:207], v[102:105]
	v_mfma_f32_16x16x32_bf16 v[2:5], v[154:157], v[204:207], v[2:5]
	v_mfma_f32_16x16x32_bf16 v[30:33], v[162:165], v[178:181], v[30:33]
	v_mfma_f32_16x16x32_bf16 v[34:37], v[170:173], v[178:181], v[34:37]
	v_mfma_f32_16x16x32_bf16 v[10:13], v[162:165], v[186:189], v[10:13]
	v_mfma_f32_16x16x32_bf16 v[14:17], v[170:173], v[186:189], v[14:17]
	v_mfma_f32_16x16x32_bf16 v[18:21], v[162:165], v[194:197], v[18:21]
	v_mfma_f32_16x16x32_bf16 v[22:25], v[170:173], v[194:197], v[22:25]
	v_mfma_f32_16x16x32_bf16 v[94:97], v[162:165], v[204:207], v[94:97]
	v_mfma_f32_16x16x32_bf16 v[6:9], v[170:173], v[204:207], v[6:9]
	s_setprio 0
	s_barrier
	s_mov_b32 m0, s42
	s_or_b32 s61, s60, 0x80
	ds_read_b128 v[174:177], v136 offset:49152
	ds_read_b128 v[178:181], v136 offset:50176
	ds_read_b128 v[182:185], v136 offset:51200
	ds_read_b128 v[186:189], v136 offset:52224
	ds_read_b128 v[190:193], v136 offset:53248
	ds_read_b128 v[194:197], v136 offset:54272
	ds_read_b128 v[198:201], v136 offset:55296
	ds_read_b128 v[204:207], v136 offset:56320
	buffer_load_dwordx4 v128, s[4:7], s61 offen lds
	s_mov_b32 m0, s43
	s_add_i32 s60, s60, 0x160080
	buffer_load_dwordx4 v134, s[4:7], s61 offen lds
	s_mov_b32 m0, s44
	s_nop 0
	buffer_load_dwordx4 v128, s[4:7], s60 offen lds
	s_mov_b32 m0, s45
	s_nop 0
	buffer_load_dwordx4 v134, s[4:7], s60 offen lds
	s_waitcnt vmcnt(6)
	s_waitcnt lgkmcnt(0)
	s_barrier
	s_setprio 1
	s_waitcnt lgkmcnt(7)
	v_mfma_f32_16x16x32_bf16 v[74:77], v[142:145], v[174:177], v[74:77]
	v_mfma_f32_16x16x32_bf16 v[82:85], v[150:153], v[174:177], v[82:85]
	s_waitcnt lgkmcnt(5)
	v_mfma_f32_16x16x32_bf16 v[66:69], v[142:145], v[182:185], v[66:69]
	v_mfma_f32_16x16x32_bf16 v[70:73], v[150:153], v[182:185], v[70:73]
	s_waitcnt lgkmcnt(3)
	v_mfma_f32_16x16x32_bf16 v[90:93], v[142:145], v[190:193], v[90:93]
	v_mfma_f32_16x16x32_bf16 v[50:53], v[150:153], v[190:193], v[50:53]
	s_waitcnt lgkmcnt(1)
	v_mfma_f32_16x16x32_bf16 v[78:81], v[142:145], v[198:201], v[78:81]
	v_mfma_f32_16x16x32_bf16 v[42:45], v[150:153], v[198:201], v[42:45]
	v_mfma_f32_16x16x32_bf16 v[26:29], v[158:161], v[174:177], v[26:29]
	v_mfma_f32_16x16x32_bf16 v[38:41], v[166:169], v[174:177], v[38:41]
	v_mfma_f32_16x16x32_bf16 v[58:61], v[158:161], v[182:185], v[58:61]
	v_mfma_f32_16x16x32_bf16 v[62:65], v[166:169], v[182:185], v[62:65]
	v_mfma_f32_16x16x32_bf16 v[86:89], v[158:161], v[190:193], v[86:89]
	v_mfma_f32_16x16x32_bf16 v[54:57], v[166:169], v[190:193], v[54:57]
	v_mfma_f32_16x16x32_bf16 v[130:133], v[158:161], v[198:201], v[130:133]
	v_mfma_f32_16x16x32_bf16 v[46:49], v[166:169], v[198:201], v[46:49]
	v_mfma_f32_16x16x32_bf16 v[74:77], v[146:149], v[178:181], v[74:77]
	v_mfma_f32_16x16x32_bf16 v[82:85], v[154:157], v[178:181], v[82:85]
	v_mfma_f32_16x16x32_bf16 v[66:69], v[146:149], v[186:189], v[66:69]
	v_mfma_f32_16x16x32_bf16 v[70:73], v[154:157], v[186:189], v[70:73]
	v_mfma_f32_16x16x32_bf16 v[90:93], v[146:149], v[194:197], v[90:93]
	v_mfma_f32_16x16x32_bf16 v[50:53], v[154:157], v[194:197], v[50:53]
	s_waitcnt lgkmcnt(0)
	v_mfma_f32_16x16x32_bf16 v[78:81], v[146:149], v[204:207], v[78:81]
	v_mfma_f32_16x16x32_bf16 v[42:45], v[154:157], v[204:207], v[42:45]
	v_mfma_f32_16x16x32_bf16 v[26:29], v[162:165], v[178:181], v[26:29]
	v_mfma_f32_16x16x32_bf16 v[38:41], v[170:173], v[178:181], v[38:41]
	v_mfma_f32_16x16x32_bf16 v[58:61], v[162:165], v[186:189], v[58:61]
	v_mfma_f32_16x16x32_bf16 v[62:65], v[170:173], v[186:189], v[62:65]
	v_mfma_f32_16x16x32_bf16 v[86:89], v[162:165], v[194:197], v[86:89]
	v_mfma_f32_16x16x32_bf16 v[54:57], v[170:173], v[194:197], v[54:57]
	v_mfma_f32_16x16x32_bf16 v[130:133], v[162:165], v[204:207], v[130:133]
	v_mfma_f32_16x16x32_bf16 v[46:49], v[170:173], v[204:207], v[46:49]
	s_setprio 0
	s_barrier
	s_add_i32 s58, s58, 2
	s_addk_i32 s59, 0x100
	s_cmpk_gt_u32 s58, 0x55
	s_cbranch_scc0 .LBB0_573
	s_branch .Lex_4
.Lfin_4:
	s_add_i32 s63, s61, 0x2b80
	s_mov_b32 m0, s46
	ds_read_b128 v[174:177], v136
	ds_read_b128 v[178:181], v136 offset:1024
	ds_read_b128 v[182:185], v136 offset:2048
	ds_read_b128 v[186:189], v136 offset:3072
	ds_read_b128 v[190:193], v136 offset:4096
	ds_read_b128 v[194:197], v136 offset:5120
	ds_read_b128 v[198:201], v136 offset:6144
	ds_read_b128 v[204:207], v136 offset:7168
	buffer_load_dwordx4 v127, s[64:67], s63 offen lds
	s_mov_b32 m0, s48
	s_add_i32 s61, s61, 0x162b80
	buffer_load_dwordx4 v129, s[64:67], s63 offen lds
	s_mov_b32 m0, s47
	s_nop 0
	buffer_load_dwordx4 v127, s[64:67], s61 offen lds
	s_mov_b32 m0, s49
	s_nop 0
	buffer_load_dwordx4 v129, s[64:67], s61 offen lds
	s_waitcnt vmcnt(8)
	s_waitcnt lgkmcnt(0)
	s_barrier
	s_setprio 1
	s_waitcnt lgkmcnt(7)
	v_mfma_f32_16x16x32_bf16 v[122:125], v[142:145], v[174:177], v[122:125]
	v_mfma_f32_16x16x32_bf16 v[118:121], v[150:153], v[174:177], v[118:121]
	s_waitcnt lgkmcnt(5)
	v_mfma_f32_16x16x32_bf16 v[114:117], v[142:145], v[182:185], v[114:117]
	v_mfma_f32_16x16x32_bf16 v[110:113], v[150:153], v[182:185], v[110:113]
	s_waitcnt lgkmcnt(3)
	v_mfma_f32_16x16x32_bf16 v[98:101], v[142:145], v[190:193], v[98:101]
	v_mfma_f32_16x16x32_bf16 v[106:109], v[150:153], v[190:193], v[106:109]
	s_waitcnt lgkmcnt(1)
	v_mfma_f32_16x16x32_bf16 v[102:105], v[142:145], v[198:201], v[102:105]
	v_mfma_f32_16x16x32_bf16 v[2:5], v[150:153], v[198:201], v[2:5]
	v_mfma_f32_16x16x32_bf16 v[30:33], v[158:161], v[174:177], v[30:33]
	v_mfma_f32_16x16x32_bf16 v[34:37], v[166:169], v[174:177], v[34:37]
	v_mfma_f32_16x16x32_bf16 v[10:13], v[158:161], v[182:185], v[10:13]
	v_mfma_f32_16x16x32_bf16 v[14:17], v[166:169], v[182:185], v[14:17]
	v_mfma_f32_16x16x32_bf16 v[18:21], v[158:161], v[190:193], v[18:21]
	v_mfma_f32_16x16x32_bf16 v[22:25], v[166:169], v[190:193], v[22:25]
	v_mfma_f32_16x16x32_bf16 v[94:97], v[158:161], v[198:201], v[94:97]
	v_mfma_f32_16x16x32_bf16 v[6:9], v[166:169], v[198:201], v[6:9]
	v_mfma_f32_16x16x32_bf16 v[122:125], v[146:149], v[178:181], v[122:125]
	v_mfma_f32_16x16x32_bf16 v[118:121], v[154:157], v[178:181], v[118:121]
	v_mfma_f32_16x16x32_bf16 v[114:117], v[146:149], v[186:189], v[114:117]
	v_mfma_f32_16x16x32_bf16 v[110:113], v[154:157], v[186:189], v[110:113]
	v_mfma_f32_16x16x32_bf16 v[98:101], v[146:149], v[194:197], v[98:101]
	v_mfma_f32_16x16x32_bf16 v[106:109], v[154:157], v[194:197], v[106:109]
	s_waitcnt lgkmcnt(0)
	v_mfma_f32_16x16x32_bf16 v[102:105], v[146:149], v[204:207], v[102:105]
	v_mfma_f32_16x16x32_bf16 v[2:5], v[154:157], v[204:207], v[2:5]
	v_mfma_f32_16x16x32_bf16 v[30:33], v[162:165], v[178:181], v[30:33]
	v_mfma_f32_16x16x32_bf16 v[34:37], v[170:173], v[178:181], v[34:37]
	v_mfma_f32_16x16x32_bf16 v[10:13], v[162:165], v[186:189], v[10:13]
	v_mfma_f32_16x16x32_bf16 v[14:17], v[170:173], v[186:189], v[14:17]
	v_mfma_f32_16x16x32_bf16 v[18:21], v[162:165], v[194:197], v[18:21]
	v_mfma_f32_16x16x32_bf16 v[22:25], v[170:173], v[194:197], v[22:25]
	v_mfma_f32_16x16x32_bf16 v[94:97], v[162:165], v[204:207], v[94:97]
	v_mfma_f32_16x16x32_bf16 v[6:9], v[170:173], v[204:207], v[6:9]
	s_setprio 0
	s_barrier
	s_mov_b32 m0, s13
	ds_read_b128 v[174:177], v136 offset:16384
	ds_read_b128 v[178:181], v136 offset:17408
	ds_read_b128 v[182:185], v136 offset:18432
	ds_read_b128 v[186:189], v136 offset:19456
	ds_read_b128 v[190:193], v136 offset:20480
	ds_read_b128 v[194:197], v136 offset:21504
	ds_read_b128 v[198:201], v136 offset:22528
	ds_read_b128 v[204:207], v136 offset:23552
	s_mov_b32 m0, s29
	s_add_i32 s61, s60, 0x160000
	s_mov_b32 m0, s30
	s_nop 0
	s_mov_b32 m0, s31
	s_nop 0
	s_waitcnt vmcnt(0)
	s_waitcnt lgkmcnt(0)
	s_barrier
	s_setprio 1
	s_waitcnt lgkmcnt(7)
	v_mfma_f32_16x16x32_bf16 v[74:77], v[142:145], v[174:177], v[74:77]
	v_mfma_f32_16x16x32_bf16 v[82:85], v[150:153], v[174:177], v[82:85]
	s_waitcnt lgkmcnt(5)
	v_mfma_f32_16x16x32_bf16 v[66:69], v[142:145], v[182:185], v[66:69]
	v_mfma_f32_16x16x32_bf16 v[70:73], v[150:153], v[182:185], v[70:73]
	s_waitcnt lgkmcnt(3)
	v_mfma_f32_16x16x32_bf16 v[90:93], v[142:145], v[190:193], v[90:93]
	v_mfma_f32_16x16x32_bf16 v[50:53], v[150:153], v[190:193], v[50:53]
	s_waitcnt lgkmcnt(1)
	v_mfma_f32_16x16x32_bf16 v[78:81], v[142:145], v[198:201], v[78:81]
	v_mfma_f32_16x16x32_bf16 v[42:45], v[150:153], v[198:201], v[42:45]
	v_mfma_f32_16x16x32_bf16 v[26:29], v[158:161], v[174:177], v[26:29]
	v_mfma_f32_16x16x32_bf16 v[38:41], v[166:169], v[174:177], v[38:41]
	v_mfma_f32_16x16x32_bf16 v[58:61], v[158:161], v[182:185], v[58:61]
	v_mfma_f32_16x16x32_bf16 v[62:65], v[166:169], v[182:185], v[62:65]
	v_mfma_f32_16x16x32_bf16 v[86:89], v[158:161], v[190:193], v[86:89]
	v_mfma_f32_16x16x32_bf16 v[54:57], v[166:169], v[190:193], v[54:57]
	v_mfma_f32_16x16x32_bf16 v[130:133], v[158:161], v[198:201], v[130:133]
	v_mfma_f32_16x16x32_bf16 v[46:49], v[166:169], v[198:201], v[46:49]
	v_mfma_f32_16x16x32_bf16 v[74:77], v[146:149], v[178:181], v[74:77]
	v_mfma_f32_16x16x32_bf16 v[82:85], v[154:157], v[178:181], v[82:85]
	v_mfma_f32_16x16x32_bf16 v[66:69], v[146:149], v[186:189], v[66:69]
	v_mfma_f32_16x16x32_bf16 v[70:73], v[154:157], v[186:189], v[70:73]
	v_mfma_f32_16x16x32_bf16 v[90:93], v[146:149], v[194:197], v[90:93]
	v_mfma_f32_16x16x32_bf16 v[50:53], v[154:157], v[194:197], v[50:53]
	s_waitcnt lgkmcnt(0)
	v_mfma_f32_16x16x32_bf16 v[78:81], v[146:149], v[204:207], v[78:81]
	v_mfma_f32_16x16x32_bf16 v[42:45], v[154:157], v[204:207], v[42:45]
	v_mfma_f32_16x16x32_bf16 v[26:29], v[162:165], v[178:181], v[26:29]
	v_mfma_f32_16x16x32_bf16 v[38:41], v[170:173], v[178:181], v[38:41]
	v_mfma_f32_16x16x32_bf16 v[58:61], v[162:165], v[186:189], v[58:61]
	v_mfma_f32_16x16x32_bf16 v[62:65], v[170:173], v[186:189], v[62:65]
	v_mfma_f32_16x16x32_bf16 v[86:89], v[162:165], v[194:197], v[86:89]
	v_mfma_f32_16x16x32_bf16 v[54:57], v[170:173], v[194:197], v[54:57]
	v_mfma_f32_16x16x32_bf16 v[130:133], v[162:165], v[204:207], v[130:133]
	v_mfma_f32_16x16x32_bf16 v[46:49], v[170:173], v[204:207], v[46:49]
	s_setprio 0
	s_barrier
	ds_read_b128 v[142:145], v139
	ds_read_b128 v[146:149], v139 offset:1024
	ds_read_b128 v[150:153], v139 offset:2048
	ds_read_b128 v[154:157], v139 offset:3072
	ds_read_b128 v[158:161], v140
	ds_read_b128 v[162:165], v140 offset:1024
	ds_read_b128 v[166:169], v140 offset:2048
	ds_read_b128 v[170:173], v140 offset:3072
	s_mov_b32 m0, s12
	ds_read_b128 v[174:177], v136 offset:32768
	ds_read_b128 v[178:181], v136 offset:33792
	ds_read_b128 v[182:185], v136 offset:34816
	ds_read_b128 v[186:189], v136 offset:35840
	ds_read_b128 v[190:193], v136 offset:36864
	ds_read_b128 v[194:197], v136 offset:37888
	ds_read_b128 v[198:201], v136 offset:38912
	ds_read_b128 v[204:207], v136 offset:39936
	s_mov_b32 m0, s34
	s_nop 0
	s_add_i32 s62, s62, 0x160000
	s_mov_b32 m0, s36
	s_nop 0
	s_mov_b32 m0, s37
	s_nop 0
	s_waitcnt vmcnt(8)
	s_waitcnt lgkmcnt(0)
	s_barrier
	s_setprio 1
	s_waitcnt lgkmcnt(7)
	v_mfma_f32_16x16x32_bf16 v[122:125], v[142:145], v[174:177], v[122:125]
	v_mfma_f32_16x16x32_bf16 v[118:121], v[150:153], v[174:177], v[118:121]
	s_waitcnt lgkmcnt(5)
	v_mfma_f32_16x16x32_bf16 v[114:117], v[142:145], v[182:185], v[114:117]
	v_mfma_f32_16x16x32_bf16 v[110:113], v[150:153], v[182:185], v[110:113]
	s_waitcnt lgkmcnt(3)
	v_mfma_f32_16x16x32_bf16 v[98:101], v[142:145], v[190:193], v[98:101]
	v_mfma_f32_16x16x32_bf16 v[106:109], v[150:153], v[190:193], v[106:109]
	s_waitcnt lgkmcnt(1)
	v_mfma_f32_16x16x32_bf16 v[102:105], v[142:145], v[198:201], v[102:105]
	v_mfma_f32_16x16x32_bf16 v[2:5], v[150:153], v[198:201], v[2:5]
	v_mfma_f32_16x16x32_bf16 v[30:33], v[158:161], v[174:177], v[30:33]
	v_mfma_f32_16x16x32_bf16 v[34:37], v[166:169], v[174:177], v[34:37]
	v_mfma_f32_16x16x32_bf16 v[10:13], v[158:161], v[182:185], v[10:13]
	v_mfma_f32_16x16x32_bf16 v[14:17], v[166:169], v[182:185], v[14:17]
	v_mfma_f32_16x16x32_bf16 v[18:21], v[158:161], v[190:193], v[18:21]
	v_mfma_f32_16x16x32_bf16 v[22:25], v[166:169], v[190:193], v[22:25]
	v_mfma_f32_16x16x32_bf16 v[94:97], v[158:161], v[198:201], v[94:97]
	v_mfma_f32_16x16x32_bf16 v[6:9], v[166:169], v[198:201], v[6:9]
	v_mfma_f32_16x16x32_bf16 v[122:125], v[146:149], v[178:181], v[122:125]
	v_mfma_f32_16x16x32_bf16 v[118:121], v[154:157], v[178:181], v[118:121]
	v_mfma_f32_16x16x32_bf16 v[114:117], v[146:149], v[186:189], v[114:117]
	v_mfma_f32_16x16x32_bf16 v[110:113], v[154:157], v[186:189], v[110:113]
	v_mfma_f32_16x16x32_bf16 v[98:101], v[146:149], v[194:197], v[98:101]
	v_mfma_f32_16x16x32_bf16 v[106:109], v[154:157], v[194:197], v[106:109]
	s_waitcnt lgkmcnt(0)
	v_mfma_f32_16x16x32_bf16 v[102:105], v[146:149], v[204:207], v[102:105]
	v_mfma_f32_16x16x32_bf16 v[2:5], v[154:157], v[204:207], v[2:5]
	v_mfma_f32_16x16x32_bf16 v[30:33], v[162:165], v[178:181], v[30:33]
	v_mfma_f32_16x16x32_bf16 v[34:37], v[170:173], v[178:181], v[34:37]
	v_mfma_f32_16x16x32_bf16 v[10:13], v[162:165], v[186:189], v[10:13]
	v_mfma_f32_16x16x32_bf16 v[14:17], v[170:173], v[186:189], v[14:17]
	v_mfma_f32_16x16x32_bf16 v[18:21], v[162:165], v[194:197], v[18:21]
	v_mfma_f32_16x16x32_bf16 v[22:25], v[170:173], v[194:197], v[22:25]
	v_mfma_f32_16x16x32_bf16 v[94:97], v[162:165], v[204:207], v[94:97]
	v_mfma_f32_16x16x32_bf16 v[6:9], v[170:173], v[204:207], v[6:9]
	s_setprio 0
	s_barrier
	s_mov_b32 m0, s42
	s_or_b32 s61, s60, 0x80
	ds_read_b128 v[174:177], v136 offset:49152
	ds_read_b128 v[178:181], v136 offset:50176
	ds_read_b128 v[182:185], v136 offset:51200
	ds_read_b128 v[186:189], v136 offset:52224
	ds_read_b128 v[190:193], v136 offset:53248
	ds_read_b128 v[194:197], v136 offset:54272
	ds_read_b128 v[198:201], v136 offset:55296
	ds_read_b128 v[204:207], v136 offset:56320
	s_mov_b32 m0, s43
	s_add_i32 s60, s60, 0x160080
	s_mov_b32 m0, s44
	s_nop 0
	s_mov_b32 m0, s45
	s_nop 0
	s_waitcnt vmcnt(6)
	s_waitcnt lgkmcnt(0)
	s_barrier
	s_setprio 1
	s_waitcnt lgkmcnt(7)
	v_mfma_f32_16x16x32_bf16 v[74:77], v[142:145], v[174:177], v[74:77]
	v_mfma_f32_16x16x32_bf16 v[82:85], v[150:153], v[174:177], v[82:85]
	s_waitcnt lgkmcnt(5)
	v_mfma_f32_16x16x32_bf16 v[66:69], v[142:145], v[182:185], v[66:69]
	v_mfma_f32_16x16x32_bf16 v[70:73], v[150:153], v[182:185], v[70:73]
	s_waitcnt lgkmcnt(3)
	v_mfma_f32_16x16x32_bf16 v[90:93], v[142:145], v[190:193], v[90:93]
	v_mfma_f32_16x16x32_bf16 v[50:53], v[150:153], v[190:193], v[50:53]
	s_waitcnt lgkmcnt(1)
	v_mfma_f32_16x16x32_bf16 v[78:81], v[142:145], v[198:201], v[78:81]
	v_mfma_f32_16x16x32_bf16 v[42:45], v[150:153], v[198:201], v[42:45]
	v_mfma_f32_16x16x32_bf16 v[26:29], v[158:161], v[174:177], v[26:29]
	v_mfma_f32_16x16x32_bf16 v[38:41], v[166:169], v[174:177], v[38:41]
	v_mfma_f32_16x16x32_bf16 v[58:61], v[158:161], v[182:185], v[58:61]
	v_mfma_f32_16x16x32_bf16 v[62:65], v[166:169], v[182:185], v[62:65]
	v_mfma_f32_16x16x32_bf16 v[86:89], v[158:161], v[190:193], v[86:89]
	v_mfma_f32_16x16x32_bf16 v[54:57], v[166:169], v[190:193], v[54:57]
	v_mfma_f32_16x16x32_bf16 v[130:133], v[158:161], v[198:201], v[130:133]
	v_mfma_f32_16x16x32_bf16 v[46:49], v[166:169], v[198:201], v[46:49]
	v_mfma_f32_16x16x32_bf16 v[74:77], v[146:149], v[178:181], v[74:77]
	v_mfma_f32_16x16x32_bf16 v[82:85], v[154:157], v[178:181], v[82:85]
	v_mfma_f32_16x16x32_bf16 v[66:69], v[146:149], v[186:189], v[66:69]
	v_mfma_f32_16x16x32_bf16 v[70:73], v[154:157], v[186:189], v[70:73]
	v_mfma_f32_16x16x32_bf16 v[90:93], v[146:149], v[194:197], v[90:93]
	v_mfma_f32_16x16x32_bf16 v[50:53], v[154:157], v[194:197], v[50:53]
	s_waitcnt lgkmcnt(0)
	v_mfma_f32_16x16x32_bf16 v[78:81], v[146:149], v[204:207], v[78:81]
	v_mfma_f32_16x16x32_bf16 v[42:45], v[154:157], v[204:207], v[42:45]
	v_mfma_f32_16x16x32_bf16 v[26:29], v[162:165], v[178:181], v[26:29]
	v_mfma_f32_16x16x32_bf16 v[38:41], v[170:173], v[178:181], v[38:41]
	v_mfma_f32_16x16x32_bf16 v[58:61], v[162:165], v[186:189], v[58:61]
	v_mfma_f32_16x16x32_bf16 v[62:65], v[170:173], v[186:189], v[62:65]
	v_mfma_f32_16x16x32_bf16 v[86:89], v[162:165], v[194:197], v[86:89]
	v_mfma_f32_16x16x32_bf16 v[54:57], v[170:173], v[194:197], v[54:57]
	v_mfma_f32_16x16x32_bf16 v[130:133], v[162:165], v[204:207], v[130:133]
	v_mfma_f32_16x16x32_bf16 v[46:49], v[170:173], v[204:207], v[46:49]
	s_setprio 0
	s_barrier
	s_add_i32 s58, s58, 2
	s_addk_i32 s59, 0x100
	s_cmpk_gt_u32 s58, 0x55
.Lex_4:
	s_and_b64 vcc, exec, s[26:27]
	s_cbranch_vccz .LBB0_569
	s_mov_b32 s11, s51
	s_mov_b32 s0, s52
	s_mov_b32 s28, s55
	s_mov_b32 s35, s54
	s_mov_b32 s50, s53
	s_branch .LBB0_569

.LBB0_675:
	ds_read_b128 v[2:5], v169
	ds_read_b128 v[6:9], v169 offset:1024
	ds_read_b128 v[10:13], v169 offset:2048
	ds_read_b128 v[14:17], v169 offset:3072
	ds_read_b128 v[18:21], v170
	ds_read_b128 v[22:25], v170 offset:1024
	ds_read_b128 v[26:29], v170 offset:2048
	ds_read_b128 v[30:33], v170 offset:3072
	s_add_i32 s61, s36, s57
	s_add_i32 s62, s61, 0x100
	s_add_i32 s60, s61, 0x200
	s_add_i32 s59, s54, s57
	s_cmpk_eq_i32 s57, 0x600
	s_cselect_b32 s59, s56, s59
	s_cselect_b32 s60, s55, s60
	s_cbranch_scc0 .Lnx_5
	s_cmp_eq_u64 s[24:25], 0
	s_cbranch_scc1 .Lfin_5
.Lnx_5:
	s_addk_i32 s61, 0x180
	s_mov_b32 m0, s44
	ds_read_b128 v[174:177], v168
	ds_read_b128 v[178:181], v168 offset:1024
	ds_read_b128 v[182:185], v168 offset:2048
	ds_read_b128 v[186:189], v168 offset:3072
	ds_read_b128 v[190:193], v168 offset:4096
	ds_read_b128 v[194:197], v168 offset:5120
	ds_read_b128 v[204:207], v168 offset:6144
	ds_read_b128 v[208:211], v168 offset:7168
	buffer_load_dwordx4 v163, s[64:67], s61 offen lds
	s_mov_b32 m0, s46
	s_nop 0
	buffer_load_dwordx4 v165, s[64:67], s61 offen lds
	s_or_b32 s61, s62, 0x40080
	s_mov_b32 m0, s45
	s_nop 0
	buffer_load_dwordx4 v163, s[64:67], s61 offen lds
	s_mov_b32 m0, s47
	s_nop 0
	buffer_load_dwordx4 v165, s[64:67], s61 offen lds
	s_waitcnt vmcnt(8)
	s_waitcnt lgkmcnt(0)
	s_barrier
	s_setprio 1
	s_waitcnt lgkmcnt(6)
	v_mfma_scale_f32_16x16x128_f8f6f4 v[62:65], v[2:9], v[174:181], v[62:65], v234, v234 op_sel_hi:[0,0,0]
	v_mfma_scale_f32_16x16x128_f8f6f4 v[58:61], v[10:17], v[174:181], v[58:61], v234, v234 op_sel_hi:[0,0,0]
	s_waitcnt lgkmcnt(4)
	v_mfma_scale_f32_16x16x128_f8f6f4 v[78:81], v[2:9], v[182:189], v[78:81], v234, v234 op_sel_hi:[0,0,0]
	v_mfma_scale_f32_16x16x128_f8f6f4 v[74:77], v[10:17], v[182:189], v[74:77], v234, v234 op_sel_hi:[0,0,0]
	s_waitcnt lgkmcnt(2)
	v_mfma_scale_f32_16x16x128_f8f6f4 v[94:97], v[2:9], v[190:197], v[94:97], v234, v234 op_sel_hi:[0,0,0]
	v_mfma_scale_f32_16x16x128_f8f6f4 v[90:93], v[10:17], v[190:197], v[90:93], v234, v234 op_sel_hi:[0,0,0]
	s_waitcnt lgkmcnt(0)
	v_mfma_scale_f32_16x16x128_f8f6f4 v[106:109], v[2:9], v[204:211], v[106:109], v234, v234 op_sel_hi:[0,0,0]
	v_mfma_scale_f32_16x16x128_f8f6f4 v[102:105], v[10:17], v[204:211], v[102:105], v234, v234 op_sel_hi:[0,0,0]
	v_mfma_scale_f32_16x16x128_f8f6f4 v[158:161], v[18:25], v[174:181], v[158:161], v234, v234 op_sel_hi:[0,0,0]
	v_mfma_scale_f32_16x16x128_f8f6f4 v[154:157], v[26:33], v[174:181], v[154:157], v234, v234 op_sel_hi:[0,0,0]
	v_mfma_scale_f32_16x16x128_f8f6f4 v[150:153], v[18:25], v[182:189], v[150:153], v234, v234 op_sel_hi:[0,0,0]
	v_mfma_scale_f32_16x16x128_f8f6f4 v[146:149], v[26:33], v[182:189], v[146:149], v234, v234 op_sel_hi:[0,0,0]
	v_mfma_scale_f32_16x16x128_f8f6f4 v[142:145], v[18:25], v[190:197], v[142:145], v234, v234 op_sel_hi:[0,0,0]
	v_mfma_scale_f32_16x16x128_f8f6f4 v[138:141], v[26:33], v[190:197], v[138:141], v234, v234 op_sel_hi:[0,0,0]
	v_mfma_scale_f32_16x16x128_f8f6f4 v[134:137], v[18:25], v[204:211], v[134:137], v234, v234 op_sel_hi:[0,0,0]
	v_mfma_scale_f32_16x16x128_f8f6f4 v[130:133], v[26:33], v[204:211], v[130:133], v234, v234 op_sel_hi:[0,0,0]
	s_setprio 0
	s_barrier
	s_mov_b32 m0, s11
	ds_read_b128 v[174:177], v168 offset:16384
	ds_read_b128 v[178:181], v168 offset:17408
	ds_read_b128 v[182:185], v168 offset:18432
	ds_read_b128 v[186:189], v168 offset:19456
	ds_read_b128 v[190:193], v168 offset:20480
	ds_read_b128 v[194:197], v168 offset:21504
	ds_read_b128 v[204:207], v168 offset:22528
	ds_read_b128 v[208:211], v168 offset:23552
	buffer_load_dwordx4 v164, s[0:3], s59 offen lds
	s_mov_b32 m0, s30
	s_or_b32 s61, s59, 0x40000
	buffer_load_dwordx4 v166, s[0:3], s59 offen lds
	s_mov_b32 m0, s31
	s_nop 0
	buffer_load_dwordx4 v164, s[0:3], s61 offen lds
	s_mov_b32 m0, s34
	s_nop 0
	buffer_load_dwordx4 v166, s[0:3], s61 offen lds
	s_waitcnt vmcnt(6)
	s_waitcnt lgkmcnt(0)
	s_barrier
	s_setprio 1
	s_waitcnt lgkmcnt(6)
	v_mfma_scale_f32_16x16x128_f8f6f4 v[118:121], v[2:9], v[174:181], v[118:121], v234, v234 op_sel_hi:[0,0,0]
	v_mfma_scale_f32_16x16x128_f8f6f4 v[114:117], v[10:17], v[174:181], v[114:117], v234, v234 op_sel_hi:[0,0,0]
	s_waitcnt lgkmcnt(4)
	v_mfma_scale_f32_16x16x128_f8f6f4 v[126:129], v[2:9], v[182:189], v[126:129], v234, v234 op_sel_hi:[0,0,0]
	v_mfma_scale_f32_16x16x128_f8f6f4 v[122:125], v[10:17], v[182:189], v[122:125], v234, v234 op_sel_hi:[0,0,0]
	s_waitcnt lgkmcnt(2)
	v_mfma_scale_f32_16x16x128_f8f6f4 v[110:113], v[2:9], v[190:197], v[110:113], v234, v234 op_sel_hi:[0,0,0]
	v_mfma_scale_f32_16x16x128_f8f6f4 v[98:101], v[10:17], v[190:197], v[98:101], v234, v234 op_sel_hi:[0,0,0]
	s_waitcnt lgkmcnt(0)
	v_mfma_scale_f32_16x16x128_f8f6f4 v[86:89], v[2:9], v[204:211], v[86:89], v234, v234 op_sel_hi:[0,0,0]
	v_mfma_scale_f32_16x16x128_f8f6f4 v[82:85], v[10:17], v[204:211], v[82:85], v234, v234 op_sel_hi:[0,0,0]
	v_mfma_scale_f32_16x16x128_f8f6f4 v[38:41], v[18:25], v[174:181], v[38:41], v234, v234 op_sel_hi:[0,0,0]
	v_mfma_scale_f32_16x16x128_f8f6f4 v[34:37], v[26:33], v[174:181], v[34:37], v234, v234 op_sel_hi:[0,0,0]
	v_mfma_scale_f32_16x16x128_f8f6f4 v[46:49], v[18:25], v[182:189], v[46:49], v234, v234 op_sel_hi:[0,0,0]
	v_mfma_scale_f32_16x16x128_f8f6f4 v[42:45], v[26:33], v[182:189], v[42:45], v234, v234 op_sel_hi:[0,0,0]
	v_mfma_scale_f32_16x16x128_f8f6f4 v[54:57], v[18:25], v[190:197], v[54:57], v234, v234 op_sel_hi:[0,0,0]
	v_mfma_scale_f32_16x16x128_f8f6f4 v[50:53], v[26:33], v[190:197], v[50:53], v234, v234 op_sel_hi:[0,0,0]
	v_mfma_scale_f32_16x16x128_f8f6f4 v[70:73], v[18:25], v[204:211], v[70:73], v234, v234 op_sel_hi:[0,0,0]
	v_mfma_scale_f32_16x16x128_f8f6f4 v[66:69], v[26:33], v[204:211], v[66:69], v234, v234 op_sel_hi:[0,0,0]
	s_setprio 0
	s_barrier
	ds_read_b128 v[18:21], v171
	ds_read_b128 v[22:25], v171 offset:1024
	ds_read_b128 v[26:29], v171 offset:2048
	ds_read_b128 v[30:33], v171 offset:3072
	ds_read_b128 v[10:13], v172
	ds_read_b128 v[14:17], v172 offset:1024
	ds_read_b128 v[2:5], v172 offset:2048
	ds_read_b128 v[6:9], v172 offset:3072
	s_mov_b32 m0, s10
	ds_read_b128 v[174:177], v168 offset:32768
	ds_read_b128 v[178:181], v168 offset:33792
	ds_read_b128 v[182:185], v168 offset:34816
	ds_read_b128 v[186:189], v168 offset:35840
	ds_read_b128 v[190:193], v168 offset:36864
	ds_read_b128 v[194:197], v168 offset:37888
	ds_read_b128 v[204:207], v168 offset:38912
	ds_read_b128 v[208:211], v168 offset:39936
	buffer_load_dwordx4 v163, s[64:67], s60 offen lds
	s_mov_b32 m0, s35
	s_nop 0
	buffer_load_dwordx4 v165, s[64:67], s60 offen lds
	s_bitset1_b32 s60, 18
	s_mov_b32 m0, s37
	s_nop 0
	buffer_load_dwordx4 v163, s[64:67], s60 offen lds
	s_mov_b32 m0, s38
	s_nop 0
	buffer_load_dwordx4 v165, s[64:67], s60 offen lds
	s_waitcnt vmcnt(8)
	s_waitcnt lgkmcnt(0)
	s_barrier
	s_setprio 1
	s_waitcnt lgkmcnt(6)
	v_mfma_scale_f32_16x16x128_f8f6f4 v[62:65], v[18:25], v[174:181], v[62:65], v234, v234 op_sel_hi:[0,0,0]
	v_mfma_scale_f32_16x16x128_f8f6f4 v[58:61], v[26:33], v[174:181], v[58:61], v234, v234 op_sel_hi:[0,0,0]
	s_waitcnt lgkmcnt(4)
	v_mfma_scale_f32_16x16x128_f8f6f4 v[78:81], v[18:25], v[182:189], v[78:81], v234, v234 op_sel_hi:[0,0,0]
	v_mfma_scale_f32_16x16x128_f8f6f4 v[74:77], v[26:33], v[182:189], v[74:77], v234, v234 op_sel_hi:[0,0,0]
	s_waitcnt lgkmcnt(2)
	v_mfma_scale_f32_16x16x128_f8f6f4 v[94:97], v[18:25], v[190:197], v[94:97], v234, v234 op_sel_hi:[0,0,0]
	v_mfma_scale_f32_16x16x128_f8f6f4 v[90:93], v[26:33], v[190:197], v[90:93], v234, v234 op_sel_hi:[0,0,0]
	s_waitcnt lgkmcnt(0)
	v_mfma_scale_f32_16x16x128_f8f6f4 v[106:109], v[18:25], v[204:211], v[106:109], v234, v234 op_sel_hi:[0,0,0]
	v_mfma_scale_f32_16x16x128_f8f6f4 v[102:105], v[26:33], v[204:211], v[102:105], v234, v234 op_sel_hi:[0,0,0]
	v_mfma_scale_f32_16x16x128_f8f6f4 v[158:161], v[10:17], v[174:181], v[158:161], v234, v234 op_sel_hi:[0,0,0]
	v_mfma_scale_f32_16x16x128_f8f6f4 v[154:157], v[2:9], v[174:181], v[154:157], v234, v234 op_sel_hi:[0,0,0]
	v_mfma_scale_f32_16x16x128_f8f6f4 v[150:153], v[10:17], v[182:189], v[150:153], v234, v234 op_sel_hi:[0,0,0]
	v_mfma_scale_f32_16x16x128_f8f6f4 v[146:149], v[2:9], v[182:189], v[146:149], v234, v234 op_sel_hi:[0,0,0]
	v_mfma_scale_f32_16x16x128_f8f6f4 v[142:145], v[10:17], v[190:197], v[142:145], v234, v234 op_sel_hi:[0,0,0]
	v_mfma_scale_f32_16x16x128_f8f6f4 v[138:141], v[2:9], v[190:197], v[138:141], v234, v234 op_sel_hi:[0,0,0]
	v_mfma_scale_f32_16x16x128_f8f6f4 v[134:137], v[10:17], v[204:211], v[134:137], v234, v234 op_sel_hi:[0,0,0]
	v_mfma_scale_f32_16x16x128_f8f6f4 v[130:133], v[2:9], v[204:211], v[130:133], v234, v234 op_sel_hi:[0,0,0]
	s_setprio 0
	s_barrier
	s_mov_b32 m0, s40
	s_or_b32 s60, s59, 0x80
	ds_read_b128 v[174:177], v168 offset:49152
	ds_read_b128 v[178:181], v168 offset:50176
	ds_read_b128 v[182:185], v168 offset:51200
	ds_read_b128 v[186:189], v168 offset:52224
	ds_read_b128 v[190:193], v168 offset:53248
	ds_read_b128 v[194:197], v168 offset:54272
	ds_read_b128 v[204:207], v168 offset:55296
	ds_read_b128 v[208:211], v168 offset:56320
	buffer_load_dwordx4 v164, s[0:3], s60 offen lds
	s_mov_b32 m0, s41
	s_or_b32 s59, s59, 0x40080
	buffer_load_dwordx4 v166, s[0:3], s60 offen lds
	s_mov_b32 m0, s42
	s_nop 0
	buffer_load_dwordx4 v164, s[0:3], s59 offen lds
	s_mov_b32 m0, s43
	s_nop 0
	buffer_load_dwordx4 v166, s[0:3], s59 offen lds
	s_waitcnt vmcnt(6)
	s_waitcnt lgkmcnt(0)
	s_barrier
	s_setprio 1
	s_waitcnt lgkmcnt(6)
	v_mfma_scale_f32_16x16x128_f8f6f4 v[118:121], v[18:25], v[174:181], v[118:121], v234, v234 op_sel_hi:[0,0,0]
	v_mfma_scale_f32_16x16x128_f8f6f4 v[114:117], v[26:33], v[174:181], v[114:117], v234, v234 op_sel_hi:[0,0,0]
	s_waitcnt lgkmcnt(4)
	v_mfma_scale_f32_16x16x128_f8f6f4 v[126:129], v[18:25], v[182:189], v[126:129], v234, v234 op_sel_hi:[0,0,0]
	v_mfma_scale_f32_16x16x128_f8f6f4 v[122:125], v[26:33], v[182:189], v[122:125], v234, v234 op_sel_hi:[0,0,0]
	s_waitcnt lgkmcnt(2)
	v_mfma_scale_f32_16x16x128_f8f6f4 v[110:113], v[18:25], v[190:197], v[110:113], v234, v234 op_sel_hi:[0,0,0]
	v_mfma_scale_f32_16x16x128_f8f6f4 v[98:101], v[26:33], v[190:197], v[98:101], v234, v234 op_sel_hi:[0,0,0]
	s_waitcnt lgkmcnt(0)
	v_mfma_scale_f32_16x16x128_f8f6f4 v[86:89], v[18:25], v[204:211], v[86:89], v234, v234 op_sel_hi:[0,0,0]
	v_mfma_scale_f32_16x16x128_f8f6f4 v[82:85], v[26:33], v[204:211], v[82:85], v234, v234 op_sel_hi:[0,0,0]
	v_mfma_scale_f32_16x16x128_f8f6f4 v[38:41], v[10:17], v[174:181], v[38:41], v234, v234 op_sel_hi:[0,0,0]
	v_mfma_scale_f32_16x16x128_f8f6f4 v[34:37], v[2:9], v[174:181], v[34:37], v234, v234 op_sel_hi:[0,0,0]
	v_mfma_scale_f32_16x16x128_f8f6f4 v[46:49], v[10:17], v[182:189], v[46:49], v234, v234 op_sel_hi:[0,0,0]
	v_mfma_scale_f32_16x16x128_f8f6f4 v[42:45], v[2:9], v[182:189], v[42:45], v234, v234 op_sel_hi:[0,0,0]
	v_mfma_scale_f32_16x16x128_f8f6f4 v[54:57], v[10:17], v[190:197], v[54:57], v234, v234 op_sel_hi:[0,0,0]
	v_mfma_scale_f32_16x16x128_f8f6f4 v[50:53], v[2:9], v[190:197], v[50:53], v234, v234 op_sel_hi:[0,0,0]
	v_mfma_scale_f32_16x16x128_f8f6f4 v[70:73], v[10:17], v[204:211], v[70:73], v234, v234 op_sel_hi:[0,0,0]
	v_mfma_scale_f32_16x16x128_f8f6f4 v[66:69], v[2:9], v[204:211], v[66:69], v234, v234 op_sel_hi:[0,0,0]
	s_setprio 0
	s_barrier
	s_add_i32 s58, s58, 2
	s_addk_i32 s57, 0x100
	s_cmp_gt_u32 s58, 13
	s_cbranch_scc0 .LBB0_675
	s_branch .Lex_5
.Lfin_5:
	s_addk_i32 s61, 0x180
	s_mov_b32 m0, s44
	ds_read_b128 v[174:177], v168
	ds_read_b128 v[178:181], v168 offset:1024
	ds_read_b128 v[182:185], v168 offset:2048
	ds_read_b128 v[186:189], v168 offset:3072
	ds_read_b128 v[190:193], v168 offset:4096
	ds_read_b128 v[194:197], v168 offset:5120
	ds_read_b128 v[204:207], v168 offset:6144
	ds_read_b128 v[208:211], v168 offset:7168
	buffer_load_dwordx4 v163, s[64:67], s61 offen lds
	s_mov_b32 m0, s46
	s_nop 0
	buffer_load_dwordx4 v165, s[64:67], s61 offen lds
	s_or_b32 s61, s62, 0x40080
	s_mov_b32 m0, s45
	s_nop 0
	buffer_load_dwordx4 v163, s[64:67], s61 offen lds
	s_mov_b32 m0, s47
	s_nop 0
	buffer_load_dwordx4 v165, s[64:67], s61 offen lds
	s_waitcnt vmcnt(8)
	s_waitcnt lgkmcnt(0)
	s_barrier
	s_setprio 1
	s_waitcnt lgkmcnt(6)
	v_mfma_scale_f32_16x16x128_f8f6f4 v[62:65], v[2:9], v[174:181], v[62:65], v234, v234 op_sel_hi:[0,0,0]
	v_mfma_scale_f32_16x16x128_f8f6f4 v[58:61], v[10:17], v[174:181], v[58:61], v234, v234 op_sel_hi:[0,0,0]
	s_waitcnt lgkmcnt(4)
	v_mfma_scale_f32_16x16x128_f8f6f4 v[78:81], v[2:9], v[182:189], v[78:81], v234, v234 op_sel_hi:[0,0,0]
	v_mfma_scale_f32_16x16x128_f8f6f4 v[74:77], v[10:17], v[182:189], v[74:77], v234, v234 op_sel_hi:[0,0,0]
	s_waitcnt lgkmcnt(2)
	v_mfma_scale_f32_16x16x128_f8f6f4 v[94:97], v[2:9], v[190:197], v[94:97], v234, v234 op_sel_hi:[0,0,0]
	v_mfma_scale_f32_16x16x128_f8f6f4 v[90:93], v[10:17], v[190:197], v[90:93], v234, v234 op_sel_hi:[0,0,0]
	s_waitcnt lgkmcnt(0)
	v_mfma_scale_f32_16x16x128_f8f6f4 v[106:109], v[2:9], v[204:211], v[106:109], v234, v234 op_sel_hi:[0,0,0]
	v_mfma_scale_f32_16x16x128_f8f6f4 v[102:105], v[10:17], v[204:211], v[102:105], v234, v234 op_sel_hi:[0,0,0]
	v_mfma_scale_f32_16x16x128_f8f6f4 v[158:161], v[18:25], v[174:181], v[158:161], v234, v234 op_sel_hi:[0,0,0]
	v_mfma_scale_f32_16x16x128_f8f6f4 v[154:157], v[26:33], v[174:181], v[154:157], v234, v234 op_sel_hi:[0,0,0]
	v_mfma_scale_f32_16x16x128_f8f6f4 v[150:153], v[18:25], v[182:189], v[150:153], v234, v234 op_sel_hi:[0,0,0]
	v_mfma_scale_f32_16x16x128_f8f6f4 v[146:149], v[26:33], v[182:189], v[146:149], v234, v234 op_sel_hi:[0,0,0]
	v_mfma_scale_f32_16x16x128_f8f6f4 v[142:145], v[18:25], v[190:197], v[142:145], v234, v234 op_sel_hi:[0,0,0]
	v_mfma_scale_f32_16x16x128_f8f6f4 v[138:141], v[26:33], v[190:197], v[138:141], v234, v234 op_sel_hi:[0,0,0]
	v_mfma_scale_f32_16x16x128_f8f6f4 v[134:137], v[18:25], v[204:211], v[134:137], v234, v234 op_sel_hi:[0,0,0]
	v_mfma_scale_f32_16x16x128_f8f6f4 v[130:133], v[26:33], v[204:211], v[130:133], v234, v234 op_sel_hi:[0,0,0]
	s_setprio 0
	s_barrier
	s_mov_b32 m0, s11
	ds_read_b128 v[174:177], v168 offset:16384
	ds_read_b128 v[178:181], v168 offset:17408
	ds_read_b128 v[182:185], v168 offset:18432
	ds_read_b128 v[186:189], v168 offset:19456
	ds_read_b128 v[190:193], v168 offset:20480
	ds_read_b128 v[194:197], v168 offset:21504
	ds_read_b128 v[204:207], v168 offset:22528
	ds_read_b128 v[208:211], v168 offset:23552
	s_mov_b32 m0, s30
	s_or_b32 s61, s59, 0x40000
	s_mov_b32 m0, s31
	s_nop 0
	s_mov_b32 m0, s34
	s_nop 0
	s_waitcnt vmcnt(0)
	s_waitcnt lgkmcnt(0)
	s_barrier
	s_setprio 1
	s_waitcnt lgkmcnt(6)
	v_mfma_scale_f32_16x16x128_f8f6f4 v[118:121], v[2:9], v[174:181], v[118:121], v234, v234 op_sel_hi:[0,0,0]
	v_mfma_scale_f32_16x16x128_f8f6f4 v[114:117], v[10:17], v[174:181], v[114:117], v234, v234 op_sel_hi:[0,0,0]
	s_waitcnt lgkmcnt(4)
	v_mfma_scale_f32_16x16x128_f8f6f4 v[126:129], v[2:9], v[182:189], v[126:129], v234, v234 op_sel_hi:[0,0,0]
	v_mfma_scale_f32_16x16x128_f8f6f4 v[122:125], v[10:17], v[182:189], v[122:125], v234, v234 op_sel_hi:[0,0,0]
	s_waitcnt lgkmcnt(2)
	v_mfma_scale_f32_16x16x128_f8f6f4 v[110:113], v[2:9], v[190:197], v[110:113], v234, v234 op_sel_hi:[0,0,0]
	v_mfma_scale_f32_16x16x128_f8f6f4 v[98:101], v[10:17], v[190:197], v[98:101], v234, v234 op_sel_hi:[0,0,0]
	s_waitcnt lgkmcnt(0)
	v_mfma_scale_f32_16x16x128_f8f6f4 v[86:89], v[2:9], v[204:211], v[86:89], v234, v234 op_sel_hi:[0,0,0]
	v_mfma_scale_f32_16x16x128_f8f6f4 v[82:85], v[10:17], v[204:211], v[82:85], v234, v234 op_sel_hi:[0,0,0]
	v_mfma_scale_f32_16x16x128_f8f6f4 v[38:41], v[18:25], v[174:181], v[38:41], v234, v234 op_sel_hi:[0,0,0]
	v_mfma_scale_f32_16x16x128_f8f6f4 v[34:37], v[26:33], v[174:181], v[34:37], v234, v234 op_sel_hi:[0,0,0]
	v_mfma_scale_f32_16x16x128_f8f6f4 v[46:49], v[18:25], v[182:189], v[46:49], v234, v234 op_sel_hi:[0,0,0]
	v_mfma_scale_f32_16x16x128_f8f6f4 v[42:45], v[26:33], v[182:189], v[42:45], v234, v234 op_sel_hi:[0,0,0]
	v_mfma_scale_f32_16x16x128_f8f6f4 v[54:57], v[18:25], v[190:197], v[54:57], v234, v234 op_sel_hi:[0,0,0]
	v_mfma_scale_f32_16x16x128_f8f6f4 v[50:53], v[26:33], v[190:197], v[50:53], v234, v234 op_sel_hi:[0,0,0]
	v_mfma_scale_f32_16x16x128_f8f6f4 v[70:73], v[18:25], v[204:211], v[70:73], v234, v234 op_sel_hi:[0,0,0]
	v_mfma_scale_f32_16x16x128_f8f6f4 v[66:69], v[26:33], v[204:211], v[66:69], v234, v234 op_sel_hi:[0,0,0]
	s_setprio 0
	s_barrier
	ds_read_b128 v[18:21], v171
	ds_read_b128 v[22:25], v171 offset:1024
	ds_read_b128 v[26:29], v171 offset:2048
	ds_read_b128 v[30:33], v171 offset:3072
	ds_read_b128 v[10:13], v172
	ds_read_b128 v[14:17], v172 offset:1024
	ds_read_b128 v[2:5], v172 offset:2048
	ds_read_b128 v[6:9], v172 offset:3072
	s_mov_b32 m0, s10
	ds_read_b128 v[174:177], v168 offset:32768
	ds_read_b128 v[178:181], v168 offset:33792
	ds_read_b128 v[182:185], v168 offset:34816
	ds_read_b128 v[186:189], v168 offset:35840
	ds_read_b128 v[190:193], v168 offset:36864
	ds_read_b128 v[194:197], v168 offset:37888
	ds_read_b128 v[204:207], v168 offset:38912
	ds_read_b128 v[208:211], v168 offset:39936
	s_mov_b32 m0, s35
	s_nop 0
	s_bitset1_b32 s60, 18
	s_mov_b32 m0, s37
	s_nop 0
	s_mov_b32 m0, s38
	s_nop 0
	s_waitcnt vmcnt(8)
	s_waitcnt lgkmcnt(0)
	s_barrier
	s_setprio 1
	s_waitcnt lgkmcnt(6)
	v_mfma_scale_f32_16x16x128_f8f6f4 v[62:65], v[18:25], v[174:181], v[62:65], v234, v234 op_sel_hi:[0,0,0]
	v_mfma_scale_f32_16x16x128_f8f6f4 v[58:61], v[26:33], v[174:181], v[58:61], v234, v234 op_sel_hi:[0,0,0]
	s_waitcnt lgkmcnt(4)
	v_mfma_scale_f32_16x16x128_f8f6f4 v[78:81], v[18:25], v[182:189], v[78:81], v234, v234 op_sel_hi:[0,0,0]
	v_mfma_scale_f32_16x16x128_f8f6f4 v[74:77], v[26:33], v[182:189], v[74:77], v234, v234 op_sel_hi:[0,0,0]
	s_waitcnt lgkmcnt(2)
	v_mfma_scale_f32_16x16x128_f8f6f4 v[94:97], v[18:25], v[190:197], v[94:97], v234, v234 op_sel_hi:[0,0,0]
	v_mfma_scale_f32_16x16x128_f8f6f4 v[90:93], v[26:33], v[190:197], v[90:93], v234, v234 op_sel_hi:[0,0,0]
	s_waitcnt lgkmcnt(0)
	v_mfma_scale_f32_16x16x128_f8f6f4 v[106:109], v[18:25], v[204:211], v[106:109], v234, v234 op_sel_hi:[0,0,0]
	v_mfma_scale_f32_16x16x128_f8f6f4 v[102:105], v[26:33], v[204:211], v[102:105], v234, v234 op_sel_hi:[0,0,0]
	v_mfma_scale_f32_16x16x128_f8f6f4 v[158:161], v[10:17], v[174:181], v[158:161], v234, v234 op_sel_hi:[0,0,0]
	v_mfma_scale_f32_16x16x128_f8f6f4 v[154:157], v[2:9], v[174:181], v[154:157], v234, v234 op_sel_hi:[0,0,0]
	v_mfma_scale_f32_16x16x128_f8f6f4 v[150:153], v[10:17], v[182:189], v[150:153], v234, v234 op_sel_hi:[0,0,0]
	v_mfma_scale_f32_16x16x128_f8f6f4 v[146:149], v[2:9], v[182:189], v[146:149], v234, v234 op_sel_hi:[0,0,0]
	v_mfma_scale_f32_16x16x128_f8f6f4 v[142:145], v[10:17], v[190:197], v[142:145], v234, v234 op_sel_hi:[0,0,0]
	v_mfma_scale_f32_16x16x128_f8f6f4 v[138:141], v[2:9], v[190:197], v[138:141], v234, v234 op_sel_hi:[0,0,0]
	v_mfma_scale_f32_16x16x128_f8f6f4 v[134:137], v[10:17], v[204:211], v[134:137], v234, v234 op_sel_hi:[0,0,0]
	v_mfma_scale_f32_16x16x128_f8f6f4 v[130:133], v[2:9], v[204:211], v[130:133], v234, v234 op_sel_hi:[0,0,0]
	s_setprio 0
	s_barrier
	s_mov_b32 m0, s40
	s_or_b32 s60, s59, 0x80
	ds_read_b128 v[174:177], v168 offset:49152
	ds_read_b128 v[178:181], v168 offset:50176
	ds_read_b128 v[182:185], v168 offset:51200
	ds_read_b128 v[186:189], v168 offset:52224
	ds_read_b128 v[190:193], v168 offset:53248
	ds_read_b128 v[194:197], v168 offset:54272
	ds_read_b128 v[204:207], v168 offset:55296
	ds_read_b128 v[208:211], v168 offset:56320
	s_mov_b32 m0, s41
	s_or_b32 s59, s59, 0x40080
	s_mov_b32 m0, s42
	s_nop 0
	s_mov_b32 m0, s43
	s_nop 0
	s_waitcnt vmcnt(6)
	s_waitcnt lgkmcnt(0)
	s_barrier
	s_setprio 1
	s_waitcnt lgkmcnt(6)
	v_mfma_scale_f32_16x16x128_f8f6f4 v[118:121], v[18:25], v[174:181], v[118:121], v234, v234 op_sel_hi:[0,0,0]
	v_mfma_scale_f32_16x16x128_f8f6f4 v[114:117], v[26:33], v[174:181], v[114:117], v234, v234 op_sel_hi:[0,0,0]
	s_waitcnt lgkmcnt(4)
	v_mfma_scale_f32_16x16x128_f8f6f4 v[126:129], v[18:25], v[182:189], v[126:129], v234, v234 op_sel_hi:[0,0,0]
	v_mfma_scale_f32_16x16x128_f8f6f4 v[122:125], v[26:33], v[182:189], v[122:125], v234, v234 op_sel_hi:[0,0,0]
	s_waitcnt lgkmcnt(2)
	v_mfma_scale_f32_16x16x128_f8f6f4 v[110:113], v[18:25], v[190:197], v[110:113], v234, v234 op_sel_hi:[0,0,0]
	v_mfma_scale_f32_16x16x128_f8f6f4 v[98:101], v[26:33], v[190:197], v[98:101], v234, v234 op_sel_hi:[0,0,0]
	s_waitcnt lgkmcnt(0)
	v_mfma_scale_f32_16x16x128_f8f6f4 v[86:89], v[18:25], v[204:211], v[86:89], v234, v234 op_sel_hi:[0,0,0]
	v_mfma_scale_f32_16x16x128_f8f6f4 v[82:85], v[26:33], v[204:211], v[82:85], v234, v234 op_sel_hi:[0,0,0]
	v_mfma_scale_f32_16x16x128_f8f6f4 v[38:41], v[10:17], v[174:181], v[38:41], v234, v234 op_sel_hi:[0,0,0]
	v_mfma_scale_f32_16x16x128_f8f6f4 v[34:37], v[2:9], v[174:181], v[34:37], v234, v234 op_sel_hi:[0,0,0]
	v_mfma_scale_f32_16x16x128_f8f6f4 v[46:49], v[10:17], v[182:189], v[46:49], v234, v234 op_sel_hi:[0,0,0]
	v_mfma_scale_f32_16x16x128_f8f6f4 v[42:45], v[2:9], v[182:189], v[42:45], v234, v234 op_sel_hi:[0,0,0]
	v_mfma_scale_f32_16x16x128_f8f6f4 v[54:57], v[10:17], v[190:197], v[54:57], v234, v234 op_sel_hi:[0,0,0]
	v_mfma_scale_f32_16x16x128_f8f6f4 v[50:53], v[2:9], v[190:197], v[50:53], v234, v234 op_sel_hi:[0,0,0]
	v_mfma_scale_f32_16x16x128_f8f6f4 v[70:73], v[10:17], v[204:211], v[70:73], v234, v234 op_sel_hi:[0,0,0]
	v_mfma_scale_f32_16x16x128_f8f6f4 v[66:69], v[2:9], v[204:211], v[66:69], v234, v234 op_sel_hi:[0,0,0]
	s_setprio 0
	s_barrier
	s_add_i32 s58, s58, 2
	s_addk_i32 s57, 0x100
	s_cmp_gt_u32 s58, 13
.Lex_5:
	s_nop 15
	s_nop 15
	s_and_b64 vcc, exec, s[24:25]
	s_cbranch_vccz .LBB0_671
	s_mov_b32 s9, s49
	s_mov_b32 s20, s50
	s_mov_b32 s26, s53
	s_mov_b32 s36, s52
	s_mov_b32 s48, s51
	s_branch .LBB0_671

.LBB0_845:
	ds_read_b128 v[142:145], v130
	ds_read_b128 v[146:149], v130 offset:1024
	ds_read_b128 v[150:153], v130 offset:2048
	ds_read_b128 v[154:157], v130 offset:3072
	ds_read_b128 v[158:161], v131
	ds_read_b128 v[162:165], v131 offset:1024
	ds_read_b128 v[166:169], v131 offset:2048
	ds_read_b128 v[170:173], v131 offset:3072
	s_add_i32 s60, s53, 0xfff80080
	s_cmp_eq_u32 s58, 28
	s_cselect_b32 s61, vcc_hi, s52
	s_cselect_b32 s60, vcc_lo, s60
	s_cbranch_scc0 .Lnx_6
	s_cmp_eq_u64 s[30:31], 0
	s_cbranch_scc1 .Lfin_6
.Lnx_6:
	s_add_i32 s62, s53, 0xfff80000
	s_mov_b32 m0, s79
	ds_read_b128 v[174:177], v138
	ds_read_b128 v[178:181], v138 offset:1024
	ds_read_b128 v[182:185], v138 offset:2048
	ds_read_b128 v[186:189], v138 offset:3072
	ds_read_b128 v[190:193], v138 offset:4096
	ds_read_b128 v[194:197], v138 offset:5120
	ds_read_b128 v[198:201], v138 offset:6144
	ds_read_b128 v[204:207], v138 offset:7168
	buffer_load_dwordx4 v0, s[64:67], s62 offen lds
	s_mov_b32 m0, s81
	s_nop 0
	buffer_load_dwordx4 v133, s[64:67], s62 offen lds
	s_mov_b32 m0, s80
	s_nop 0
	buffer_load_dwordx4 v0, s[64:67], s53 offen lds
	s_mov_b32 m0, s82
	s_nop 0
	buffer_load_dwordx4 v133, s[64:67], s53 offen lds
	s_waitcnt vmcnt(8)
	s_waitcnt lgkmcnt(0)
	s_barrier
	s_setprio 1
	s_waitcnt lgkmcnt(7)
	v_mfma_f32_16x16x32_bf16 v[126:129], v[142:145], v[174:177], v[126:129]
	v_mfma_f32_16x16x32_bf16 v[118:121], v[150:153], v[174:177], v[118:121]
	s_waitcnt lgkmcnt(5)
	v_mfma_f32_16x16x32_bf16 v[110:113], v[142:145], v[182:185], v[110:113]
	v_mfma_f32_16x16x32_bf16 v[102:105], v[150:153], v[182:185], v[102:105]
	s_waitcnt lgkmcnt(3)
	v_mfma_f32_16x16x32_bf16 v[94:97], v[142:145], v[190:193], v[94:97]
	v_mfma_f32_16x16x32_bf16 v[86:89], v[150:153], v[190:193], v[86:89]
	s_waitcnt lgkmcnt(1)
	v_mfma_f32_16x16x32_bf16 v[62:65], v[142:145], v[198:201], v[62:65]
	v_mfma_f32_16x16x32_bf16 v[54:57], v[150:153], v[198:201], v[54:57]
	v_mfma_f32_16x16x32_bf16 v[122:125], v[158:161], v[174:177], v[122:125]
	v_mfma_f32_16x16x32_bf16 v[114:117], v[166:169], v[174:177], v[114:117]
	v_mfma_f32_16x16x32_bf16 v[106:109], v[158:161], v[182:185], v[106:109]
	v_mfma_f32_16x16x32_bf16 v[98:101], v[166:169], v[182:185], v[98:101]
	v_mfma_f32_16x16x32_bf16 v[90:93], v[158:161], v[190:193], v[90:93]
	v_mfma_f32_16x16x32_bf16 v[82:85], v[166:169], v[190:193], v[82:85]
	v_mfma_f32_16x16x32_bf16 v[58:61], v[158:161], v[198:201], v[58:61]
	v_mfma_f32_16x16x32_bf16 v[50:53], v[166:169], v[198:201], v[50:53]
	v_mfma_f32_16x16x32_bf16 v[126:129], v[146:149], v[178:181], v[126:129]
	v_mfma_f32_16x16x32_bf16 v[118:121], v[154:157], v[178:181], v[118:121]
	v_mfma_f32_16x16x32_bf16 v[110:113], v[146:149], v[186:189], v[110:113]
	v_mfma_f32_16x16x32_bf16 v[102:105], v[154:157], v[186:189], v[102:105]
	v_mfma_f32_16x16x32_bf16 v[94:97], v[146:149], v[194:197], v[94:97]
	v_mfma_f32_16x16x32_bf16 v[86:89], v[154:157], v[194:197], v[86:89]
	s_waitcnt lgkmcnt(0)
	v_mfma_f32_16x16x32_bf16 v[62:65], v[146:149], v[204:207], v[62:65]
	v_mfma_f32_16x16x32_bf16 v[54:57], v[154:157], v[204:207], v[54:57]
	v_mfma_f32_16x16x32_bf16 v[122:125], v[162:165], v[178:181], v[122:125]
	v_mfma_f32_16x16x32_bf16 v[114:117], v[170:173], v[178:181], v[114:117]
	v_mfma_f32_16x16x32_bf16 v[106:109], v[162:165], v[186:189], v[106:109]
	v_mfma_f32_16x16x32_bf16 v[98:101], v[170:173], v[186:189], v[98:101]
	v_mfma_f32_16x16x32_bf16 v[90:93], v[162:165], v[194:197], v[90:93]
	v_mfma_f32_16x16x32_bf16 v[82:85], v[170:173], v[194:197], v[82:85]
	v_mfma_f32_16x16x32_bf16 v[58:61], v[162:165], v[204:207], v[58:61]
	v_mfma_f32_16x16x32_bf16 v[50:53], v[170:173], v[204:207], v[50:53]
	s_setprio 0
	s_barrier
	s_mov_b32 m0, s15
	ds_read_b128 v[174:177], v138 offset:16384
	ds_read_b128 v[178:181], v138 offset:17408
	ds_read_b128 v[182:185], v138 offset:18432
	ds_read_b128 v[186:189], v138 offset:19456
	ds_read_b128 v[190:193], v138 offset:20480
	ds_read_b128 v[194:197], v138 offset:21504
	ds_read_b128 v[198:201], v138 offset:22528
	ds_read_b128 v[204:207], v138 offset:23552
	buffer_load_dwordx4 v132, s[4:7], s61 offen lds
	s_mov_b32 m0, s16
	s_add_i32 s62, s61, 0x80000
	buffer_load_dwordx4 v134, s[4:7], s61 offen lds
	s_mov_b32 m0, s17
	s_nop 0
	buffer_load_dwordx4 v132, s[4:7], s62 offen lds
	s_mov_b32 m0, s20
	s_nop 0
	buffer_load_dwordx4 v134, s[4:7], s62 offen lds
	s_waitcnt vmcnt(6)
	s_waitcnt lgkmcnt(0)
	s_barrier
	s_setprio 1
	s_waitcnt lgkmcnt(7)
	v_mfma_f32_16x16x32_bf16 v[78:81], v[142:145], v[174:177], v[78:81]
	v_mfma_f32_16x16x32_bf16 v[70:73], v[150:153], v[174:177], v[70:73]
	s_waitcnt lgkmcnt(5)
	v_mfma_f32_16x16x32_bf16 v[46:49], v[142:145], v[182:185], v[46:49]
	v_mfma_f32_16x16x32_bf16 v[38:41], v[150:153], v[182:185], v[38:41]
	s_waitcnt lgkmcnt(3)
	v_mfma_f32_16x16x32_bf16 v[30:33], v[142:145], v[190:193], v[30:33]
	v_mfma_f32_16x16x32_bf16 v[22:25], v[150:153], v[190:193], v[22:25]
	s_waitcnt lgkmcnt(1)
	v_mfma_f32_16x16x32_bf16 v[14:17], v[142:145], v[198:201], v[14:17]
	v_mfma_f32_16x16x32_bf16 v[6:9], v[150:153], v[198:201], v[6:9]
	v_mfma_f32_16x16x32_bf16 v[74:77], v[158:161], v[174:177], v[74:77]
	v_mfma_f32_16x16x32_bf16 v[66:69], v[166:169], v[174:177], v[66:69]
	v_mfma_f32_16x16x32_bf16 v[42:45], v[158:161], v[182:185], v[42:45]
	v_mfma_f32_16x16x32_bf16 v[34:37], v[166:169], v[182:185], v[34:37]
	v_mfma_f32_16x16x32_bf16 v[26:29], v[158:161], v[190:193], v[26:29]
	v_mfma_f32_16x16x32_bf16 v[18:21], v[166:169], v[190:193], v[18:21]
	v_mfma_f32_16x16x32_bf16 v[10:13], v[158:161], v[198:201], v[10:13]
	v_mfma_f32_16x16x32_bf16 v[2:5], v[166:169], v[198:201], v[2:5]
	v_mfma_f32_16x16x32_bf16 v[78:81], v[146:149], v[178:181], v[78:81]
	v_mfma_f32_16x16x32_bf16 v[70:73], v[154:157], v[178:181], v[70:73]
	v_mfma_f32_16x16x32_bf16 v[46:49], v[146:149], v[186:189], v[46:49]
	v_mfma_f32_16x16x32_bf16 v[38:41], v[154:157], v[186:189], v[38:41]
	v_mfma_f32_16x16x32_bf16 v[30:33], v[146:149], v[194:197], v[30:33]
	v_mfma_f32_16x16x32_bf16 v[22:25], v[154:157], v[194:197], v[22:25]
	s_waitcnt lgkmcnt(0)
	v_mfma_f32_16x16x32_bf16 v[14:17], v[146:149], v[204:207], v[14:17]
	v_mfma_f32_16x16x32_bf16 v[6:9], v[154:157], v[204:207], v[6:9]
	v_mfma_f32_16x16x32_bf16 v[74:77], v[162:165], v[178:181], v[74:77]
	v_mfma_f32_16x16x32_bf16 v[66:69], v[170:173], v[178:181], v[66:69]
	v_mfma_f32_16x16x32_bf16 v[42:45], v[162:165], v[186:189], v[42:45]
	v_mfma_f32_16x16x32_bf16 v[34:37], v[170:173], v[186:189], v[34:37]
	v_mfma_f32_16x16x32_bf16 v[26:29], v[162:165], v[194:197], v[26:29]
	v_mfma_f32_16x16x32_bf16 v[18:21], v[170:173], v[194:197], v[18:21]
	v_mfma_f32_16x16x32_bf16 v[10:13], v[162:165], v[204:207], v[10:13]
	v_mfma_f32_16x16x32_bf16 v[2:5], v[170:173], v[204:207], v[2:5]
	s_setprio 0
	s_barrier
	ds_read_b128 v[142:145], v139
	ds_read_b128 v[146:149], v139 offset:1024
	ds_read_b128 v[150:153], v139 offset:2048
	ds_read_b128 v[154:157], v139 offset:3072
	ds_read_b128 v[158:161], v140
	ds_read_b128 v[162:165], v140 offset:1024
	ds_read_b128 v[166:169], v140 offset:2048
	ds_read_b128 v[170:173], v140 offset:3072
	s_mov_b32 m0, s14
	ds_read_b128 v[174:177], v138 offset:32768
	ds_read_b128 v[178:181], v138 offset:33792
	ds_read_b128 v[182:185], v138 offset:34816
	ds_read_b128 v[186:189], v138 offset:35840
	ds_read_b128 v[190:193], v138 offset:36864
	ds_read_b128 v[194:197], v138 offset:37888
	ds_read_b128 v[198:201], v138 offset:38912
	ds_read_b128 v[204:207], v138 offset:39936
	buffer_load_dwordx4 v0, s[64:67], s60 offen lds
	s_mov_b32 m0, s21
	s_nop 0
	buffer_load_dwordx4 v133, s[64:67], s60 offen lds
	s_add_i32 s60, s60, 0x80000
	s_mov_b32 m0, s46
	s_nop 0
	buffer_load_dwordx4 v0, s[64:67], s60 offen lds
	s_mov_b32 m0, s47
	s_nop 0
	buffer_load_dwordx4 v133, s[64:67], s60 offen lds
	s_waitcnt vmcnt(8)
	s_waitcnt lgkmcnt(0)
	s_barrier
	s_setprio 1
	s_waitcnt lgkmcnt(7)
	v_mfma_f32_16x16x32_bf16 v[126:129], v[142:145], v[174:177], v[126:129]
	v_mfma_f32_16x16x32_bf16 v[118:121], v[150:153], v[174:177], v[118:121]
	s_waitcnt lgkmcnt(5)
	v_mfma_f32_16x16x32_bf16 v[110:113], v[142:145], v[182:185], v[110:113]
	v_mfma_f32_16x16x32_bf16 v[102:105], v[150:153], v[182:185], v[102:105]
	s_waitcnt lgkmcnt(3)
	v_mfma_f32_16x16x32_bf16 v[94:97], v[142:145], v[190:193], v[94:97]
	v_mfma_f32_16x16x32_bf16 v[86:89], v[150:153], v[190:193], v[86:89]
	s_waitcnt lgkmcnt(1)
	v_mfma_f32_16x16x32_bf16 v[62:65], v[142:145], v[198:201], v[62:65]
	v_mfma_f32_16x16x32_bf16 v[54:57], v[150:153], v[198:201], v[54:57]
	v_mfma_f32_16x16x32_bf16 v[122:125], v[158:161], v[174:177], v[122:125]
	v_mfma_f32_16x16x32_bf16 v[114:117], v[166:169], v[174:177], v[114:117]
	v_mfma_f32_16x16x32_bf16 v[106:109], v[158:161], v[182:185], v[106:109]
	v_mfma_f32_16x16x32_bf16 v[98:101], v[166:169], v[182:185], v[98:101]
	v_mfma_f32_16x16x32_bf16 v[90:93], v[158:161], v[190:193], v[90:93]
	v_mfma_f32_16x16x32_bf16 v[82:85], v[166:169], v[190:193], v[82:85]
	v_mfma_f32_16x16x32_bf16 v[58:61], v[158:161], v[198:201], v[58:61]
	v_mfma_f32_16x16x32_bf16 v[50:53], v[166:169], v[198:201], v[50:53]
	v_mfma_f32_16x16x32_bf16 v[126:129], v[146:149], v[178:181], v[126:129]
	v_mfma_f32_16x16x32_bf16 v[118:121], v[154:157], v[178:181], v[118:121]
	v_mfma_f32_16x16x32_bf16 v[110:113], v[146:149], v[186:189], v[110:113]
	v_mfma_f32_16x16x32_bf16 v[102:105], v[154:157], v[186:189], v[102:105]
	v_mfma_f32_16x16x32_bf16 v[94:97], v[146:149], v[194:197], v[94:97]
	v_mfma_f32_16x16x32_bf16 v[86:89], v[154:157], v[194:197], v[86:89]
	s_waitcnt lgkmcnt(0)
	v_mfma_f32_16x16x32_bf16 v[62:65], v[146:149], v[204:207], v[62:65]
	v_mfma_f32_16x16x32_bf16 v[54:57], v[154:157], v[204:207], v[54:57]
	v_mfma_f32_16x16x32_bf16 v[122:125], v[162:165], v[178:181], v[122:125]
	v_mfma_f32_16x16x32_bf16 v[114:117], v[170:173], v[178:181], v[114:117]
	v_mfma_f32_16x16x32_bf16 v[106:109], v[162:165], v[186:189], v[106:109]
	v_mfma_f32_16x16x32_bf16 v[98:101], v[170:173], v[186:189], v[98:101]
	v_mfma_f32_16x16x32_bf16 v[90:93], v[162:165], v[194:197], v[90:93]
	v_mfma_f32_16x16x32_bf16 v[82:85], v[170:173], v[194:197], v[82:85]
	v_mfma_f32_16x16x32_bf16 v[58:61], v[162:165], v[204:207], v[58:61]
	v_mfma_f32_16x16x32_bf16 v[50:53], v[170:173], v[204:207], v[50:53]
	s_setprio 0
	s_barrier
	s_mov_b32 m0, s55
	s_or_b32 s60, s61, 0x80
	ds_read_b128 v[174:177], v138 offset:49152
	ds_read_b128 v[178:181], v138 offset:50176
	ds_read_b128 v[182:185], v138 offset:51200
	ds_read_b128 v[186:189], v138 offset:52224
	ds_read_b128 v[190:193], v138 offset:53248
	ds_read_b128 v[194:197], v138 offset:54272
	ds_read_b128 v[198:201], v138 offset:55296
	ds_read_b128 v[204:207], v138 offset:56320
	buffer_load_dwordx4 v132, s[4:7], s60 offen lds
	s_mov_b32 m0, s56
	s_add_i32 s61, s61, 0x80080
	buffer_load_dwordx4 v134, s[4:7], s60 offen lds
	s_mov_b32 m0, s63
	s_nop 0
	buffer_load_dwordx4 v132, s[4:7], s61 offen lds
	s_mov_b32 m0, s76
	s_nop 0
	buffer_load_dwordx4 v134, s[4:7], s61 offen lds
	s_waitcnt vmcnt(6)
	s_waitcnt lgkmcnt(0)
	s_barrier
	s_setprio 1
	s_waitcnt lgkmcnt(7)
	v_mfma_f32_16x16x32_bf16 v[78:81], v[142:145], v[174:177], v[78:81]
	v_mfma_f32_16x16x32_bf16 v[70:73], v[150:153], v[174:177], v[70:73]
	s_waitcnt lgkmcnt(5)
	v_mfma_f32_16x16x32_bf16 v[46:49], v[142:145], v[182:185], v[46:49]
	v_mfma_f32_16x16x32_bf16 v[38:41], v[150:153], v[182:185], v[38:41]
	s_waitcnt lgkmcnt(3)
	v_mfma_f32_16x16x32_bf16 v[30:33], v[142:145], v[190:193], v[30:33]
	v_mfma_f32_16x16x32_bf16 v[22:25], v[150:153], v[190:193], v[22:25]
	s_waitcnt lgkmcnt(1)
	v_mfma_f32_16x16x32_bf16 v[14:17], v[142:145], v[198:201], v[14:17]
	v_mfma_f32_16x16x32_bf16 v[6:9], v[150:153], v[198:201], v[6:9]
	v_mfma_f32_16x16x32_bf16 v[74:77], v[158:161], v[174:177], v[74:77]
	v_mfma_f32_16x16x32_bf16 v[66:69], v[166:169], v[174:177], v[66:69]
	v_mfma_f32_16x16x32_bf16 v[42:45], v[158:161], v[182:185], v[42:45]
	v_mfma_f32_16x16x32_bf16 v[34:37], v[166:169], v[182:185], v[34:37]
	v_mfma_f32_16x16x32_bf16 v[26:29], v[158:161], v[190:193], v[26:29]
	v_mfma_f32_16x16x32_bf16 v[18:21], v[166:169], v[190:193], v[18:21]
	v_mfma_f32_16x16x32_bf16 v[10:13], v[158:161], v[198:201], v[10:13]
	v_mfma_f32_16x16x32_bf16 v[2:5], v[166:169], v[198:201], v[2:5]
	v_mfma_f32_16x16x32_bf16 v[78:81], v[146:149], v[178:181], v[78:81]
	v_mfma_f32_16x16x32_bf16 v[70:73], v[154:157], v[178:181], v[70:73]
	v_mfma_f32_16x16x32_bf16 v[46:49], v[146:149], v[186:189], v[46:49]
	v_mfma_f32_16x16x32_bf16 v[38:41], v[154:157], v[186:189], v[38:41]
	v_mfma_f32_16x16x32_bf16 v[30:33], v[146:149], v[194:197], v[30:33]
	v_mfma_f32_16x16x32_bf16 v[22:25], v[154:157], v[194:197], v[22:25]
	s_waitcnt lgkmcnt(0)
	v_mfma_f32_16x16x32_bf16 v[14:17], v[146:149], v[204:207], v[14:17]
	v_mfma_f32_16x16x32_bf16 v[6:9], v[154:157], v[204:207], v[6:9]
	v_mfma_f32_16x16x32_bf16 v[74:77], v[162:165], v[178:181], v[74:77]
	v_mfma_f32_16x16x32_bf16 v[66:69], v[170:173], v[178:181], v[66:69]
	v_mfma_f32_16x16x32_bf16 v[42:45], v[162:165], v[186:189], v[42:45]
	v_mfma_f32_16x16x32_bf16 v[34:37], v[170:173], v[186:189], v[34:37]
	v_mfma_f32_16x16x32_bf16 v[26:29], v[162:165], v[194:197], v[26:29]
	v_mfma_f32_16x16x32_bf16 v[18:21], v[170:173], v[194:197], v[18:21]
	v_mfma_f32_16x16x32_bf16 v[10:13], v[162:165], v[204:207], v[10:13]
	v_mfma_f32_16x16x32_bf16 v[2:5], v[170:173], v[204:207], v[2:5]
	s_setprio 0
	s_barrier
	s_add_i32 s58, s58, 2
	s_addk_i32 s52, 0x100
	s_addk_i32 s53, 0x100
	s_cmp_gt_u32 s58, 29
	s_cbranch_scc0 .LBB0_845
	s_branch .Lex_6
.Lfin_6:
	s_add_i32 s62, s53, 0xfff80000
	s_mov_b32 m0, s79
	ds_read_b128 v[174:177], v138
	ds_read_b128 v[178:181], v138 offset:1024
	ds_read_b128 v[182:185], v138 offset:2048
	ds_read_b128 v[186:189], v138 offset:3072
	ds_read_b128 v[190:193], v138 offset:4096
	ds_read_b128 v[194:197], v138 offset:5120
	ds_read_b128 v[198:201], v138 offset:6144
	ds_read_b128 v[204:207], v138 offset:7168
	buffer_load_dwordx4 v0, s[64:67], s62 offen lds
	s_mov_b32 m0, s81
	s_nop 0
	buffer_load_dwordx4 v133, s[64:67], s62 offen lds
	s_mov_b32 m0, s80
	s_nop 0
	buffer_load_dwordx4 v0, s[64:67], s53 offen lds
	s_mov_b32 m0, s82
	s_nop 0
	buffer_load_dwordx4 v133, s[64:67], s53 offen lds
	s_waitcnt vmcnt(8)
	s_waitcnt lgkmcnt(0)
	s_barrier
	s_setprio 1
	s_waitcnt lgkmcnt(7)
	v_mfma_f32_16x16x32_bf16 v[126:129], v[142:145], v[174:177], v[126:129]
	v_mfma_f32_16x16x32_bf16 v[118:121], v[150:153], v[174:177], v[118:121]
	s_waitcnt lgkmcnt(5)
	v_mfma_f32_16x16x32_bf16 v[110:113], v[142:145], v[182:185], v[110:113]
	v_mfma_f32_16x16x32_bf16 v[102:105], v[150:153], v[182:185], v[102:105]
	s_waitcnt lgkmcnt(3)
	v_mfma_f32_16x16x32_bf16 v[94:97], v[142:145], v[190:193], v[94:97]
	v_mfma_f32_16x16x32_bf16 v[86:89], v[150:153], v[190:193], v[86:89]
	s_waitcnt lgkmcnt(1)
	v_mfma_f32_16x16x32_bf16 v[62:65], v[142:145], v[198:201], v[62:65]
	v_mfma_f32_16x16x32_bf16 v[54:57], v[150:153], v[198:201], v[54:57]
	v_mfma_f32_16x16x32_bf16 v[122:125], v[158:161], v[174:177], v[122:125]
	v_mfma_f32_16x16x32_bf16 v[114:117], v[166:169], v[174:177], v[114:117]
	v_mfma_f32_16x16x32_bf16 v[106:109], v[158:161], v[182:185], v[106:109]
	v_mfma_f32_16x16x32_bf16 v[98:101], v[166:169], v[182:185], v[98:101]
	v_mfma_f32_16x16x32_bf16 v[90:93], v[158:161], v[190:193], v[90:93]
	v_mfma_f32_16x16x32_bf16 v[82:85], v[166:169], v[190:193], v[82:85]
	v_mfma_f32_16x16x32_bf16 v[58:61], v[158:161], v[198:201], v[58:61]
	v_mfma_f32_16x16x32_bf16 v[50:53], v[166:169], v[198:201], v[50:53]
	v_mfma_f32_16x16x32_bf16 v[126:129], v[146:149], v[178:181], v[126:129]
	v_mfma_f32_16x16x32_bf16 v[118:121], v[154:157], v[178:181], v[118:121]
	v_mfma_f32_16x16x32_bf16 v[110:113], v[146:149], v[186:189], v[110:113]
	v_mfma_f32_16x16x32_bf16 v[102:105], v[154:157], v[186:189], v[102:105]
	v_mfma_f32_16x16x32_bf16 v[94:97], v[146:149], v[194:197], v[94:97]
	v_mfma_f32_16x16x32_bf16 v[86:89], v[154:157], v[194:197], v[86:89]
	s_waitcnt lgkmcnt(0)
	v_mfma_f32_16x16x32_bf16 v[62:65], v[146:149], v[204:207], v[62:65]
	v_mfma_f32_16x16x32_bf16 v[54:57], v[154:157], v[204:207], v[54:57]
	v_mfma_f32_16x16x32_bf16 v[122:125], v[162:165], v[178:181], v[122:125]
	v_mfma_f32_16x16x32_bf16 v[114:117], v[170:173], v[178:181], v[114:117]
	v_mfma_f32_16x16x32_bf16 v[106:109], v[162:165], v[186:189], v[106:109]
	v_mfma_f32_16x16x32_bf16 v[98:101], v[170:173], v[186:189], v[98:101]
	v_mfma_f32_16x16x32_bf16 v[90:93], v[162:165], v[194:197], v[90:93]
	v_mfma_f32_16x16x32_bf16 v[82:85], v[170:173], v[194:197], v[82:85]
	v_mfma_f32_16x16x32_bf16 v[58:61], v[162:165], v[204:207], v[58:61]
	v_mfma_f32_16x16x32_bf16 v[50:53], v[170:173], v[204:207], v[50:53]
	s_setprio 0
	s_barrier
	s_mov_b32 m0, s15
	ds_read_b128 v[174:177], v138 offset:16384
	ds_read_b128 v[178:181], v138 offset:17408
	ds_read_b128 v[182:185], v138 offset:18432
	ds_read_b128 v[186:189], v138 offset:19456
	ds_read_b128 v[190:193], v138 offset:20480
	ds_read_b128 v[194:197], v138 offset:21504
	ds_read_b128 v[198:201], v138 offset:22528
	ds_read_b128 v[204:207], v138 offset:23552
	s_mov_b32 m0, s16
	s_add_i32 s62, s61, 0x80000
	s_mov_b32 m0, s17
	s_nop 0
	s_mov_b32 m0, s20
	s_nop 0
	s_waitcnt vmcnt(0)
	s_waitcnt lgkmcnt(0)
	s_barrier
	s_setprio 1
	s_waitcnt lgkmcnt(7)
	v_mfma_f32_16x16x32_bf16 v[78:81], v[142:145], v[174:177], v[78:81]
	v_mfma_f32_16x16x32_bf16 v[70:73], v[150:153], v[174:177], v[70:73]
	s_waitcnt lgkmcnt(5)
	v_mfma_f32_16x16x32_bf16 v[46:49], v[142:145], v[182:185], v[46:49]
	v_mfma_f32_16x16x32_bf16 v[38:41], v[150:153], v[182:185], v[38:41]
	s_waitcnt lgkmcnt(3)
	v_mfma_f32_16x16x32_bf16 v[30:33], v[142:145], v[190:193], v[30:33]
	v_mfma_f32_16x16x32_bf16 v[22:25], v[150:153], v[190:193], v[22:25]
	s_waitcnt lgkmcnt(1)
	v_mfma_f32_16x16x32_bf16 v[14:17], v[142:145], v[198:201], v[14:17]
	v_mfma_f32_16x16x32_bf16 v[6:9], v[150:153], v[198:201], v[6:9]
	v_mfma_f32_16x16x32_bf16 v[74:77], v[158:161], v[174:177], v[74:77]
	v_mfma_f32_16x16x32_bf16 v[66:69], v[166:169], v[174:177], v[66:69]
	v_mfma_f32_16x16x32_bf16 v[42:45], v[158:161], v[182:185], v[42:45]
	v_mfma_f32_16x16x32_bf16 v[34:37], v[166:169], v[182:185], v[34:37]
	v_mfma_f32_16x16x32_bf16 v[26:29], v[158:161], v[190:193], v[26:29]
	v_mfma_f32_16x16x32_bf16 v[18:21], v[166:169], v[190:193], v[18:21]
	v_mfma_f32_16x16x32_bf16 v[10:13], v[158:161], v[198:201], v[10:13]
	v_mfma_f32_16x16x32_bf16 v[2:5], v[166:169], v[198:201], v[2:5]
	v_mfma_f32_16x16x32_bf16 v[78:81], v[146:149], v[178:181], v[78:81]
	v_mfma_f32_16x16x32_bf16 v[70:73], v[154:157], v[178:181], v[70:73]
	v_mfma_f32_16x16x32_bf16 v[46:49], v[146:149], v[186:189], v[46:49]
	v_mfma_f32_16x16x32_bf16 v[38:41], v[154:157], v[186:189], v[38:41]
	v_mfma_f32_16x16x32_bf16 v[30:33], v[146:149], v[194:197], v[30:33]
	v_mfma_f32_16x16x32_bf16 v[22:25], v[154:157], v[194:197], v[22:25]
	s_waitcnt lgkmcnt(0)
	v_mfma_f32_16x16x32_bf16 v[14:17], v[146:149], v[204:207], v[14:17]
	v_mfma_f32_16x16x32_bf16 v[6:9], v[154:157], v[204:207], v[6:9]
	v_mfma_f32_16x16x32_bf16 v[74:77], v[162:165], v[178:181], v[74:77]
	v_mfma_f32_16x16x32_bf16 v[66:69], v[170:173], v[178:181], v[66:69]
	v_mfma_f32_16x16x32_bf16 v[42:45], v[162:165], v[186:189], v[42:45]
	v_mfma_f32_16x16x32_bf16 v[34:37], v[170:173], v[186:189], v[34:37]
	v_mfma_f32_16x16x32_bf16 v[26:29], v[162:165], v[194:197], v[26:29]
	v_mfma_f32_16x16x32_bf16 v[18:21], v[170:173], v[194:197], v[18:21]
	v_mfma_f32_16x16x32_bf16 v[10:13], v[162:165], v[204:207], v[10:13]
	v_mfma_f32_16x16x32_bf16 v[2:5], v[170:173], v[204:207], v[2:5]
	s_setprio 0
	s_barrier
	ds_read_b128 v[142:145], v139
	ds_read_b128 v[146:149], v139 offset:1024
	ds_read_b128 v[150:153], v139 offset:2048
	ds_read_b128 v[154:157], v139 offset:3072
	ds_read_b128 v[158:161], v140
	ds_read_b128 v[162:165], v140 offset:1024
	ds_read_b128 v[166:169], v140 offset:2048
	ds_read_b128 v[170:173], v140 offset:3072
	s_mov_b32 m0, s14
	ds_read_b128 v[174:177], v138 offset:32768
	ds_read_b128 v[178:181], v138 offset:33792
	ds_read_b128 v[182:185], v138 offset:34816
	ds_read_b128 v[186:189], v138 offset:35840
	ds_read_b128 v[190:193], v138 offset:36864
	ds_read_b128 v[194:197], v138 offset:37888
	ds_read_b128 v[198:201], v138 offset:38912
	ds_read_b128 v[204:207], v138 offset:39936
	s_mov_b32 m0, s21
	s_nop 0
	s_add_i32 s60, s60, 0x80000
	s_mov_b32 m0, s46
	s_nop 0
	s_mov_b32 m0, s47
	s_nop 0
	s_waitcnt vmcnt(8)
	s_waitcnt lgkmcnt(0)
	s_barrier
	s_setprio 1
	s_waitcnt lgkmcnt(7)
	v_mfma_f32_16x16x32_bf16 v[126:129], v[142:145], v[174:177], v[126:129]
	v_mfma_f32_16x16x32_bf16 v[118:121], v[150:153], v[174:177], v[118:121]
	s_waitcnt lgkmcnt(5)
	v_mfma_f32_16x16x32_bf16 v[110:113], v[142:145], v[182:185], v[110:113]
	v_mfma_f32_16x16x32_bf16 v[102:105], v[150:153], v[182:185], v[102:105]
	s_waitcnt lgkmcnt(3)
	v_mfma_f32_16x16x32_bf16 v[94:97], v[142:145], v[190:193], v[94:97]
	v_mfma_f32_16x16x32_bf16 v[86:89], v[150:153], v[190:193], v[86:89]
	s_waitcnt lgkmcnt(1)
	v_mfma_f32_16x16x32_bf16 v[62:65], v[142:145], v[198:201], v[62:65]
	v_mfma_f32_16x16x32_bf16 v[54:57], v[150:153], v[198:201], v[54:57]
	v_mfma_f32_16x16x32_bf16 v[122:125], v[158:161], v[174:177], v[122:125]
	v_mfma_f32_16x16x32_bf16 v[114:117], v[166:169], v[174:177], v[114:117]
	v_mfma_f32_16x16x32_bf16 v[106:109], v[158:161], v[182:185], v[106:109]
	v_mfma_f32_16x16x32_bf16 v[98:101], v[166:169], v[182:185], v[98:101]
	v_mfma_f32_16x16x32_bf16 v[90:93], v[158:161], v[190:193], v[90:93]
	v_mfma_f32_16x16x32_bf16 v[82:85], v[166:169], v[190:193], v[82:85]
	v_mfma_f32_16x16x32_bf16 v[58:61], v[158:161], v[198:201], v[58:61]
	v_mfma_f32_16x16x32_bf16 v[50:53], v[166:169], v[198:201], v[50:53]
	v_mfma_f32_16x16x32_bf16 v[126:129], v[146:149], v[178:181], v[126:129]
	v_mfma_f32_16x16x32_bf16 v[118:121], v[154:157], v[178:181], v[118:121]
	v_mfma_f32_16x16x32_bf16 v[110:113], v[146:149], v[186:189], v[110:113]
	v_mfma_f32_16x16x32_bf16 v[102:105], v[154:157], v[186:189], v[102:105]
	v_mfma_f32_16x16x32_bf16 v[94:97], v[146:149], v[194:197], v[94:97]
	v_mfma_f32_16x16x32_bf16 v[86:89], v[154:157], v[194:197], v[86:89]
	s_waitcnt lgkmcnt(0)
	v_mfma_f32_16x16x32_bf16 v[62:65], v[146:149], v[204:207], v[62:65]
	v_mfma_f32_16x16x32_bf16 v[54:57], v[154:157], v[204:207], v[54:57]
	v_mfma_f32_16x16x32_bf16 v[122:125], v[162:165], v[178:181], v[122:125]
	v_mfma_f32_16x16x32_bf16 v[114:117], v[170:173], v[178:181], v[114:117]
	v_mfma_f32_16x16x32_bf16 v[106:109], v[162:165], v[186:189], v[106:109]
	v_mfma_f32_16x16x32_bf16 v[98:101], v[170:173], v[186:189], v[98:101]
	v_mfma_f32_16x16x32_bf16 v[90:93], v[162:165], v[194:197], v[90:93]
	v_mfma_f32_16x16x32_bf16 v[82:85], v[170:173], v[194:197], v[82:85]
	v_mfma_f32_16x16x32_bf16 v[58:61], v[162:165], v[204:207], v[58:61]
	v_mfma_f32_16x16x32_bf16 v[50:53], v[170:173], v[204:207], v[50:53]
	s_setprio 0
	s_barrier
	s_mov_b32 m0, s55
	s_or_b32 s60, s61, 0x80
	ds_read_b128 v[174:177], v138 offset:49152
	ds_read_b128 v[178:181], v138 offset:50176
	ds_read_b128 v[182:185], v138 offset:51200
	ds_read_b128 v[186:189], v138 offset:52224
	ds_read_b128 v[190:193], v138 offset:53248
	ds_read_b128 v[194:197], v138 offset:54272
	ds_read_b128 v[198:201], v138 offset:55296
	ds_read_b128 v[204:207], v138 offset:56320
	s_mov_b32 m0, s56
	s_add_i32 s61, s61, 0x80080
	s_mov_b32 m0, s63
	s_nop 0
	s_mov_b32 m0, s76
	s_nop 0
	s_waitcnt vmcnt(6)
	s_waitcnt lgkmcnt(0)
	s_barrier
	s_setprio 1
	s_waitcnt lgkmcnt(7)
	v_mfma_f32_16x16x32_bf16 v[78:81], v[142:145], v[174:177], v[78:81]
	v_mfma_f32_16x16x32_bf16 v[70:73], v[150:153], v[174:177], v[70:73]
	s_waitcnt lgkmcnt(5)
	v_mfma_f32_16x16x32_bf16 v[46:49], v[142:145], v[182:185], v[46:49]
	v_mfma_f32_16x16x32_bf16 v[38:41], v[150:153], v[182:185], v[38:41]
	s_waitcnt lgkmcnt(3)
	v_mfma_f32_16x16x32_bf16 v[30:33], v[142:145], v[190:193], v[30:33]
	v_mfma_f32_16x16x32_bf16 v[22:25], v[150:153], v[190:193], v[22:25]
	s_waitcnt lgkmcnt(1)
	v_mfma_f32_16x16x32_bf16 v[14:17], v[142:145], v[198:201], v[14:17]
	v_mfma_f32_16x16x32_bf16 v[6:9], v[150:153], v[198:201], v[6:9]
	v_mfma_f32_16x16x32_bf16 v[74:77], v[158:161], v[174:177], v[74:77]
	v_mfma_f32_16x16x32_bf16 v[66:69], v[166:169], v[174:177], v[66:69]
	v_mfma_f32_16x16x32_bf16 v[42:45], v[158:161], v[182:185], v[42:45]
	v_mfma_f32_16x16x32_bf16 v[34:37], v[166:169], v[182:185], v[34:37]
	v_mfma_f32_16x16x32_bf16 v[26:29], v[158:161], v[190:193], v[26:29]
	v_mfma_f32_16x16x32_bf16 v[18:21], v[166:169], v[190:193], v[18:21]
	v_mfma_f32_16x16x32_bf16 v[10:13], v[158:161], v[198:201], v[10:13]
	v_mfma_f32_16x16x32_bf16 v[2:5], v[166:169], v[198:201], v[2:5]
	v_mfma_f32_16x16x32_bf16 v[78:81], v[146:149], v[178:181], v[78:81]
	v_mfma_f32_16x16x32_bf16 v[70:73], v[154:157], v[178:181], v[70:73]
	v_mfma_f32_16x16x32_bf16 v[46:49], v[146:149], v[186:189], v[46:49]
	v_mfma_f32_16x16x32_bf16 v[38:41], v[154:157], v[186:189], v[38:41]
	v_mfma_f32_16x16x32_bf16 v[30:33], v[146:149], v[194:197], v[30:33]
	v_mfma_f32_16x16x32_bf16 v[22:25], v[154:157], v[194:197], v[22:25]
	s_waitcnt lgkmcnt(0)
	v_mfma_f32_16x16x32_bf16 v[14:17], v[146:149], v[204:207], v[14:17]
	v_mfma_f32_16x16x32_bf16 v[6:9], v[154:157], v[204:207], v[6:9]
	v_mfma_f32_16x16x32_bf16 v[74:77], v[162:165], v[178:181], v[74:77]
	v_mfma_f32_16x16x32_bf16 v[66:69], v[170:173], v[178:181], v[66:69]
	v_mfma_f32_16x16x32_bf16 v[42:45], v[162:165], v[186:189], v[42:45]
	v_mfma_f32_16x16x32_bf16 v[34:37], v[170:173], v[186:189], v[34:37]
	v_mfma_f32_16x16x32_bf16 v[26:29], v[162:165], v[194:197], v[26:29]
	v_mfma_f32_16x16x32_bf16 v[18:21], v[170:173], v[194:197], v[18:21]
	v_mfma_f32_16x16x32_bf16 v[10:13], v[162:165], v[204:207], v[10:13]
	v_mfma_f32_16x16x32_bf16 v[2:5], v[170:173], v[204:207], v[2:5]
	s_setprio 0
	s_barrier
	s_add_i32 s58, s58, 2
	s_addk_i32 s52, 0x100
	s_addk_i32 s53, 0x100
	s_cmp_gt_u32 s58, 29
.Lex_6:
	s_and_b64 vcc, exec, s[28:29]
	s_cbranch_vccz .LBB0_848
	s_barrier

.LBB0_872:
	ds_read_b128 v[2:5], v169
	ds_read_b128 v[6:9], v169 offset:1024
	ds_read_b128 v[10:13], v169 offset:2048
	ds_read_b128 v[14:17], v169 offset:3072
	ds_read_b128 v[18:21], v170
	ds_read_b128 v[22:25], v170 offset:1024
	ds_read_b128 v[26:29], v170 offset:2048
	ds_read_b128 v[30:33], v170 offset:3072
	s_add_i32 s52, s19, 0xfffc0080
	s_cmp_eq_u32 s49, 12
	s_cselect_b32 s51, vcc_lo, s18
	s_cselect_b32 s52, s15, s52
	s_cbranch_scc0 .Lnx_7
	s_cmp_eq_u64 s[28:29], 0
	s_cbranch_scc1 .Lfin_7
.Lnx_7:
	s_add_i32 s53, s19, 0xfffc0000
	s_mov_b32 m0, s30
	ds_read_b128 v[174:177], v168
	ds_read_b128 v[178:181], v168 offset:1024
	ds_read_b128 v[182:185], v168 offset:2048
	ds_read_b128 v[186:189], v168 offset:3072
	ds_read_b128 v[190:193], v168 offset:4096
	ds_read_b128 v[194:197], v168 offset:5120
	ds_read_b128 v[204:207], v168 offset:6144
	ds_read_b128 v[208:211], v168 offset:7168
	buffer_load_dwordx4 v0, s[64:67], s53 offen lds
	s_mov_b32 m0, s16
	s_nop 0
	buffer_load_dwordx4 v163, s[64:67], s53 offen lds
	s_mov_b32 m0, s17
	s_nop 0
	buffer_load_dwordx4 v0, s[64:67], s19 offen lds
	s_mov_b32 m0, s21
	s_nop 0
	buffer_load_dwordx4 v163, s[64:67], s19 offen lds
	s_waitcnt vmcnt(8)
	s_waitcnt lgkmcnt(0)
	s_barrier
	s_setprio 1
	s_waitcnt lgkmcnt(6)
	v_mfma_scale_f32_16x16x128_f8f6f4 v[138:141], v[2:9], v[174:181], v[138:141], v234, v234 op_sel_hi:[0,0,0]
	v_mfma_scale_f32_16x16x128_f8f6f4 v[146:149], v[10:17], v[174:181], v[146:149], v234, v234 op_sel_hi:[0,0,0]
	s_waitcnt lgkmcnt(4)
	v_mfma_scale_f32_16x16x128_f8f6f4 v[134:137], v[2:9], v[182:189], v[134:137], v234, v234 op_sel_hi:[0,0,0]
	v_mfma_scale_f32_16x16x128_f8f6f4 v[130:133], v[10:17], v[182:189], v[130:133], v234, v234 op_sel_hi:[0,0,0]
	s_waitcnt lgkmcnt(2)
	v_mfma_scale_f32_16x16x128_f8f6f4 v[110:113], v[2:9], v[190:197], v[110:113], v234, v234 op_sel_hi:[0,0,0]
	v_mfma_scale_f32_16x16x128_f8f6f4 v[102:105], v[10:17], v[190:197], v[102:105], v234, v234 op_sel_hi:[0,0,0]
	s_waitcnt lgkmcnt(0)
	v_mfma_scale_f32_16x16x128_f8f6f4 v[78:81], v[2:9], v[204:211], v[78:81], v234, v234 op_sel_hi:[0,0,0]
	v_mfma_scale_f32_16x16x128_f8f6f4 v[70:73], v[10:17], v[204:211], v[70:73], v234, v234 op_sel_hi:[0,0,0]
	v_mfma_scale_f32_16x16x128_f8f6f4 v[154:157], v[18:25], v[174:181], v[154:157], v234, v234 op_sel_hi:[0,0,0]
	v_mfma_scale_f32_16x16x128_f8f6f4 v[158:161], v[26:33], v[174:181], v[158:161], v234, v234 op_sel_hi:[0,0,0]
	v_mfma_scale_f32_16x16x128_f8f6f4 v[150:153], v[18:25], v[182:189], v[150:153], v234, v234 op_sel_hi:[0,0,0]
	v_mfma_scale_f32_16x16x128_f8f6f4 v[142:145], v[26:33], v[182:189], v[142:145], v234, v234 op_sel_hi:[0,0,0]
	v_mfma_scale_f32_16x16x128_f8f6f4 v[126:129], v[18:25], v[190:197], v[126:129], v234, v234 op_sel_hi:[0,0,0]
	v_mfma_scale_f32_16x16x128_f8f6f4 v[118:121], v[26:33], v[190:197], v[118:121], v234, v234 op_sel_hi:[0,0,0]
	v_mfma_scale_f32_16x16x128_f8f6f4 v[94:97], v[18:25], v[204:211], v[94:97], v234, v234 op_sel_hi:[0,0,0]
	v_mfma_scale_f32_16x16x128_f8f6f4 v[86:89], v[26:33], v[204:211], v[86:89], v234, v234 op_sel_hi:[0,0,0]
	s_setprio 0
	s_barrier
	s_mov_b32 m0, s31
	ds_read_b128 v[174:177], v168 offset:16384
	ds_read_b128 v[178:181], v168 offset:17408
	ds_read_b128 v[182:185], v168 offset:18432
	ds_read_b128 v[186:189], v168 offset:19456
	ds_read_b128 v[190:193], v168 offset:20480
	ds_read_b128 v[194:197], v168 offset:21504
	ds_read_b128 v[204:207], v168 offset:22528
	ds_read_b128 v[208:211], v168 offset:23552
	buffer_load_dwordx4 v162, s[4:7], s51 offen lds
	s_mov_b32 m0, s73
	s_add_i32 s53, s51, 0x40000
	buffer_load_dwordx4 v164, s[4:7], s51 offen lds
	s_mov_b32 m0, s76
	s_nop 0
	buffer_load_dwordx4 v162, s[4:7], s53 offen lds
	s_mov_b32 m0, s77
	s_nop 0
	buffer_load_dwordx4 v164, s[4:7], s53 offen lds
	s_waitcnt vmcnt(6)
	s_waitcnt lgkmcnt(0)
	s_barrier
	s_setprio 1
	s_waitcnt lgkmcnt(6)
	v_mfma_scale_f32_16x16x128_f8f6f4 v[106:109], v[2:9], v[174:181], v[106:109], v234, v234 op_sel_hi:[0,0,0]
	v_mfma_scale_f32_16x16x128_f8f6f4 v[98:101], v[10:17], v[174:181], v[98:101], v234, v234 op_sel_hi:[0,0,0]
	s_waitcnt lgkmcnt(4)
	v_mfma_scale_f32_16x16x128_f8f6f4 v[74:77], v[2:9], v[182:189], v[74:77], v234, v234 op_sel_hi:[0,0,0]
	v_mfma_scale_f32_16x16x128_f8f6f4 v[66:69], v[10:17], v[182:189], v[66:69], v234, v234 op_sel_hi:[0,0,0]
	s_waitcnt lgkmcnt(2)
	v_mfma_scale_f32_16x16x128_f8f6f4 v[62:65], v[2:9], v[190:197], v[62:65], v234, v234 op_sel_hi:[0,0,0]
	v_mfma_scale_f32_16x16x128_f8f6f4 v[54:57], v[10:17], v[190:197], v[54:57], v234, v234 op_sel_hi:[0,0,0]
	s_waitcnt lgkmcnt(0)
	v_mfma_scale_f32_16x16x128_f8f6f4 v[46:49], v[2:9], v[204:211], v[46:49], v234, v234 op_sel_hi:[0,0,0]
	v_mfma_scale_f32_16x16x128_f8f6f4 v[42:45], v[10:17], v[204:211], v[42:45], v234, v234 op_sel_hi:[0,0,0]
	v_mfma_scale_f32_16x16x128_f8f6f4 v[122:125], v[18:25], v[174:181], v[122:125], v234, v234 op_sel_hi:[0,0,0]
	v_mfma_scale_f32_16x16x128_f8f6f4 v[114:117], v[26:33], v[174:181], v[114:117], v234, v234 op_sel_hi:[0,0,0]
	v_mfma_scale_f32_16x16x128_f8f6f4 v[90:93], v[18:25], v[182:189], v[90:93], v234, v234 op_sel_hi:[0,0,0]
	v_mfma_scale_f32_16x16x128_f8f6f4 v[82:85], v[26:33], v[182:189], v[82:85], v234, v234 op_sel_hi:[0,0,0]
	v_mfma_scale_f32_16x16x128_f8f6f4 v[58:61], v[18:25], v[190:197], v[58:61], v234, v234 op_sel_hi:[0,0,0]
	v_mfma_scale_f32_16x16x128_f8f6f4 v[50:53], v[26:33], v[190:197], v[50:53], v234, v234 op_sel_hi:[0,0,0]
	v_mfma_scale_f32_16x16x128_f8f6f4 v[38:41], v[18:25], v[204:211], v[38:41], v234, v234 op_sel_hi:[0,0,0]
	v_mfma_scale_f32_16x16x128_f8f6f4 v[34:37], v[26:33], v[204:211], v[34:37], v234, v234 op_sel_hi:[0,0,0]
	s_setprio 0
	s_barrier
	ds_read_b128 v[18:21], v171
	ds_read_b128 v[22:25], v171 offset:1024
	ds_read_b128 v[26:29], v171 offset:2048
	ds_read_b128 v[30:33], v171 offset:3072
	ds_read_b128 v[10:13], v172
	ds_read_b128 v[14:17], v172 offset:1024
	ds_read_b128 v[2:5], v172 offset:2048
	ds_read_b128 v[6:9], v172 offset:3072
	s_mov_b32 m0, s20
	ds_read_b128 v[174:177], v168 offset:32768
	ds_read_b128 v[178:181], v168 offset:33792
	ds_read_b128 v[182:185], v168 offset:34816
	ds_read_b128 v[186:189], v168 offset:35840
	ds_read_b128 v[190:193], v168 offset:36864
	ds_read_b128 v[194:197], v168 offset:37888
	ds_read_b128 v[204:207], v168 offset:38912
	ds_read_b128 v[208:211], v168 offset:39936
	buffer_load_dwordx4 v0, s[64:67], s52 offen lds
	s_mov_b32 m0, s78
	s_nop 0
	buffer_load_dwordx4 v163, s[64:67], s52 offen lds
	s_add_i32 s52, s52, 0x40000
	s_mov_b32 m0, s79
	s_nop 0
	buffer_load_dwordx4 v0, s[64:67], s52 offen lds
	s_mov_b32 m0, s80
	s_nop 0
	buffer_load_dwordx4 v163, s[64:67], s52 offen lds
	s_waitcnt vmcnt(8)
	s_waitcnt lgkmcnt(0)
	s_barrier
	s_setprio 1
	s_waitcnt lgkmcnt(6)
	v_mfma_scale_f32_16x16x128_f8f6f4 v[138:141], v[18:25], v[174:181], v[138:141], v234, v234 op_sel_hi:[0,0,0]
	v_mfma_scale_f32_16x16x128_f8f6f4 v[146:149], v[26:33], v[174:181], v[146:149], v234, v234 op_sel_hi:[0,0,0]
	s_waitcnt lgkmcnt(4)
	v_mfma_scale_f32_16x16x128_f8f6f4 v[134:137], v[18:25], v[182:189], v[134:137], v234, v234 op_sel_hi:[0,0,0]
	v_mfma_scale_f32_16x16x128_f8f6f4 v[130:133], v[26:33], v[182:189], v[130:133], v234, v234 op_sel_hi:[0,0,0]
	s_waitcnt lgkmcnt(2)
	v_mfma_scale_f32_16x16x128_f8f6f4 v[110:113], v[18:25], v[190:197], v[110:113], v234, v234 op_sel_hi:[0,0,0]
	v_mfma_scale_f32_16x16x128_f8f6f4 v[102:105], v[26:33], v[190:197], v[102:105], v234, v234 op_sel_hi:[0,0,0]
	s_waitcnt lgkmcnt(0)
	v_mfma_scale_f32_16x16x128_f8f6f4 v[78:81], v[18:25], v[204:211], v[78:81], v234, v234 op_sel_hi:[0,0,0]
	v_mfma_scale_f32_16x16x128_f8f6f4 v[70:73], v[26:33], v[204:211], v[70:73], v234, v234 op_sel_hi:[0,0,0]
	v_mfma_scale_f32_16x16x128_f8f6f4 v[154:157], v[10:17], v[174:181], v[154:157], v234, v234 op_sel_hi:[0,0,0]
	v_mfma_scale_f32_16x16x128_f8f6f4 v[158:161], v[2:9], v[174:181], v[158:161], v234, v234 op_sel_hi:[0,0,0]
	v_mfma_scale_f32_16x16x128_f8f6f4 v[150:153], v[10:17], v[182:189], v[150:153], v234, v234 op_sel_hi:[0,0,0]
	v_mfma_scale_f32_16x16x128_f8f6f4 v[142:145], v[2:9], v[182:189], v[142:145], v234, v234 op_sel_hi:[0,0,0]
	v_mfma_scale_f32_16x16x128_f8f6f4 v[126:129], v[10:17], v[190:197], v[126:129], v234, v234 op_sel_hi:[0,0,0]
	v_mfma_scale_f32_16x16x128_f8f6f4 v[118:121], v[2:9], v[190:197], v[118:121], v234, v234 op_sel_hi:[0,0,0]
	v_mfma_scale_f32_16x16x128_f8f6f4 v[94:97], v[10:17], v[204:211], v[94:97], v234, v234 op_sel_hi:[0,0,0]
	v_mfma_scale_f32_16x16x128_f8f6f4 v[86:89], v[2:9], v[204:211], v[86:89], v234, v234 op_sel_hi:[0,0,0]
	s_setprio 0
	s_barrier
	s_mov_b32 m0, s81
	s_or_b32 s52, s51, 0x80
	ds_read_b128 v[174:177], v168 offset:49152
	ds_read_b128 v[178:181], v168 offset:50176
	ds_read_b128 v[182:185], v168 offset:51200
	ds_read_b128 v[186:189], v168 offset:52224
	ds_read_b128 v[190:193], v168 offset:53248
	ds_read_b128 v[194:197], v168 offset:54272
	ds_read_b128 v[204:207], v168 offset:55296
	ds_read_b128 v[208:211], v168 offset:56320
	buffer_load_dwordx4 v162, s[4:7], s52 offen lds
	s_mov_b32 m0, s82
	s_add_i32 s51, s51, 0x40080
	buffer_load_dwordx4 v164, s[4:7], s52 offen lds
	s_mov_b32 m0, s83
	s_nop 0
	buffer_load_dwordx4 v162, s[4:7], s51 offen lds
	s_mov_b32 m0, s84
	s_nop 0
	buffer_load_dwordx4 v164, s[4:7], s51 offen lds
	s_waitcnt vmcnt(6)
	s_waitcnt lgkmcnt(0)
	s_barrier
	s_setprio 1
	s_waitcnt lgkmcnt(6)
	v_mfma_scale_f32_16x16x128_f8f6f4 v[106:109], v[18:25], v[174:181], v[106:109], v234, v234 op_sel_hi:[0,0,0]
	v_mfma_scale_f32_16x16x128_f8f6f4 v[98:101], v[26:33], v[174:181], v[98:101], v234, v234 op_sel_hi:[0,0,0]
	s_waitcnt lgkmcnt(4)
	v_mfma_scale_f32_16x16x128_f8f6f4 v[74:77], v[18:25], v[182:189], v[74:77], v234, v234 op_sel_hi:[0,0,0]
	v_mfma_scale_f32_16x16x128_f8f6f4 v[66:69], v[26:33], v[182:189], v[66:69], v234, v234 op_sel_hi:[0,0,0]
	s_waitcnt lgkmcnt(2)
	v_mfma_scale_f32_16x16x128_f8f6f4 v[62:65], v[18:25], v[190:197], v[62:65], v234, v234 op_sel_hi:[0,0,0]
	v_mfma_scale_f32_16x16x128_f8f6f4 v[54:57], v[26:33], v[190:197], v[54:57], v234, v234 op_sel_hi:[0,0,0]
	s_waitcnt lgkmcnt(0)
	v_mfma_scale_f32_16x16x128_f8f6f4 v[46:49], v[18:25], v[204:211], v[46:49], v234, v234 op_sel_hi:[0,0,0]
	v_mfma_scale_f32_16x16x128_f8f6f4 v[42:45], v[26:33], v[204:211], v[42:45], v234, v234 op_sel_hi:[0,0,0]
	v_mfma_scale_f32_16x16x128_f8f6f4 v[122:125], v[10:17], v[174:181], v[122:125], v234, v234 op_sel_hi:[0,0,0]
	v_mfma_scale_f32_16x16x128_f8f6f4 v[114:117], v[2:9], v[174:181], v[114:117], v234, v234 op_sel_hi:[0,0,0]
	v_mfma_scale_f32_16x16x128_f8f6f4 v[90:93], v[10:17], v[182:189], v[90:93], v234, v234 op_sel_hi:[0,0,0]
	v_mfma_scale_f32_16x16x128_f8f6f4 v[82:85], v[2:9], v[182:189], v[82:85], v234, v234 op_sel_hi:[0,0,0]
	v_mfma_scale_f32_16x16x128_f8f6f4 v[58:61], v[10:17], v[190:197], v[58:61], v234, v234 op_sel_hi:[0,0,0]
	v_mfma_scale_f32_16x16x128_f8f6f4 v[50:53], v[2:9], v[190:197], v[50:53], v234, v234 op_sel_hi:[0,0,0]
	v_mfma_scale_f32_16x16x128_f8f6f4 v[38:41], v[10:17], v[204:211], v[38:41], v234, v234 op_sel_hi:[0,0,0]
	v_mfma_scale_f32_16x16x128_f8f6f4 v[34:37], v[2:9], v[204:211], v[34:37], v234, v234 op_sel_hi:[0,0,0]
	s_setprio 0
	s_barrier
	s_add_i32 s49, s49, 2
	s_addk_i32 s18, 0x100
	s_addk_i32 s19, 0x100
	s_cmp_gt_u32 s49, 13
	s_cbranch_scc0 .LBB0_872
	s_branch .Lex_7
.Lfin_7:
	s_add_i32 s53, s19, 0xfffc0000
	s_mov_b32 m0, s30
	ds_read_b128 v[174:177], v168
	ds_read_b128 v[178:181], v168 offset:1024
	ds_read_b128 v[182:185], v168 offset:2048
	ds_read_b128 v[186:189], v168 offset:3072
	ds_read_b128 v[190:193], v168 offset:4096
	ds_read_b128 v[194:197], v168 offset:5120
	ds_read_b128 v[204:207], v168 offset:6144
	ds_read_b128 v[208:211], v168 offset:7168
	buffer_load_dwordx4 v0, s[64:67], s53 offen lds
	s_mov_b32 m0, s16
	s_nop 0
	buffer_load_dwordx4 v163, s[64:67], s53 offen lds
	s_mov_b32 m0, s17
	s_nop 0
	buffer_load_dwordx4 v0, s[64:67], s19 offen lds
	s_mov_b32 m0, s21
	s_nop 0
	buffer_load_dwordx4 v163, s[64:67], s19 offen lds
	s_waitcnt vmcnt(8)
	s_waitcnt lgkmcnt(0)
	s_barrier
	s_setprio 1
	s_waitcnt lgkmcnt(6)
	v_mfma_scale_f32_16x16x128_f8f6f4 v[138:141], v[2:9], v[174:181], v[138:141], v234, v234 op_sel_hi:[0,0,0]
	v_mfma_scale_f32_16x16x128_f8f6f4 v[146:149], v[10:17], v[174:181], v[146:149], v234, v234 op_sel_hi:[0,0,0]
	s_waitcnt lgkmcnt(4)
	v_mfma_scale_f32_16x16x128_f8f6f4 v[134:137], v[2:9], v[182:189], v[134:137], v234, v234 op_sel_hi:[0,0,0]
	v_mfma_scale_f32_16x16x128_f8f6f4 v[130:133], v[10:17], v[182:189], v[130:133], v234, v234 op_sel_hi:[0,0,0]
	s_waitcnt lgkmcnt(2)
	v_mfma_scale_f32_16x16x128_f8f6f4 v[110:113], v[2:9], v[190:197], v[110:113], v234, v234 op_sel_hi:[0,0,0]
	v_mfma_scale_f32_16x16x128_f8f6f4 v[102:105], v[10:17], v[190:197], v[102:105], v234, v234 op_sel_hi:[0,0,0]
	s_waitcnt lgkmcnt(0)
	v_mfma_scale_f32_16x16x128_f8f6f4 v[78:81], v[2:9], v[204:211], v[78:81], v234, v234 op_sel_hi:[0,0,0]
	v_mfma_scale_f32_16x16x128_f8f6f4 v[70:73], v[10:17], v[204:211], v[70:73], v234, v234 op_sel_hi:[0,0,0]
	v_mfma_scale_f32_16x16x128_f8f6f4 v[154:157], v[18:25], v[174:181], v[154:157], v234, v234 op_sel_hi:[0,0,0]
	v_mfma_scale_f32_16x16x128_f8f6f4 v[158:161], v[26:33], v[174:181], v[158:161], v234, v234 op_sel_hi:[0,0,0]
	v_mfma_scale_f32_16x16x128_f8f6f4 v[150:153], v[18:25], v[182:189], v[150:153], v234, v234 op_sel_hi:[0,0,0]
	v_mfma_scale_f32_16x16x128_f8f6f4 v[142:145], v[26:33], v[182:189], v[142:145], v234, v234 op_sel_hi:[0,0,0]
	v_mfma_scale_f32_16x16x128_f8f6f4 v[126:129], v[18:25], v[190:197], v[126:129], v234, v234 op_sel_hi:[0,0,0]
	v_mfma_scale_f32_16x16x128_f8f6f4 v[118:121], v[26:33], v[190:197], v[118:121], v234, v234 op_sel_hi:[0,0,0]
	v_mfma_scale_f32_16x16x128_f8f6f4 v[94:97], v[18:25], v[204:211], v[94:97], v234, v234 op_sel_hi:[0,0,0]
	v_mfma_scale_f32_16x16x128_f8f6f4 v[86:89], v[26:33], v[204:211], v[86:89], v234, v234 op_sel_hi:[0,0,0]
	s_setprio 0
	s_barrier
	s_mov_b32 m0, s31
	ds_read_b128 v[174:177], v168 offset:16384
	ds_read_b128 v[178:181], v168 offset:17408
	ds_read_b128 v[182:185], v168 offset:18432
	ds_read_b128 v[186:189], v168 offset:19456
	ds_read_b128 v[190:193], v168 offset:20480
	ds_read_b128 v[194:197], v168 offset:21504
	ds_read_b128 v[204:207], v168 offset:22528
	ds_read_b128 v[208:211], v168 offset:23552
	s_mov_b32 m0, s73
	s_add_i32 s53, s51, 0x40000
	s_mov_b32 m0, s76
	s_nop 0
	s_mov_b32 m0, s77
	s_nop 0
	s_waitcnt vmcnt(0)
	s_waitcnt lgkmcnt(0)
	s_barrier
	s_setprio 1
	s_waitcnt lgkmcnt(6)
	v_mfma_scale_f32_16x16x128_f8f6f4 v[106:109], v[2:9], v[174:181], v[106:109], v234, v234 op_sel_hi:[0,0,0]
	v_mfma_scale_f32_16x16x128_f8f6f4 v[98:101], v[10:17], v[174:181], v[98:101], v234, v234 op_sel_hi:[0,0,0]
	s_waitcnt lgkmcnt(4)
	v_mfma_scale_f32_16x16x128_f8f6f4 v[74:77], v[2:9], v[182:189], v[74:77], v234, v234 op_sel_hi:[0,0,0]
	v_mfma_scale_f32_16x16x128_f8f6f4 v[66:69], v[10:17], v[182:189], v[66:69], v234, v234 op_sel_hi:[0,0,0]
	s_waitcnt lgkmcnt(2)
	v_mfma_scale_f32_16x16x128_f8f6f4 v[62:65], v[2:9], v[190:197], v[62:65], v234, v234 op_sel_hi:[0,0,0]
	v_mfma_scale_f32_16x16x128_f8f6f4 v[54:57], v[10:17], v[190:197], v[54:57], v234, v234 op_sel_hi:[0,0,0]
	s_waitcnt lgkmcnt(0)
	v_mfma_scale_f32_16x16x128_f8f6f4 v[46:49], v[2:9], v[204:211], v[46:49], v234, v234 op_sel_hi:[0,0,0]
	v_mfma_scale_f32_16x16x128_f8f6f4 v[42:45], v[10:17], v[204:211], v[42:45], v234, v234 op_sel_hi:[0,0,0]
	v_mfma_scale_f32_16x16x128_f8f6f4 v[122:125], v[18:25], v[174:181], v[122:125], v234, v234 op_sel_hi:[0,0,0]
	v_mfma_scale_f32_16x16x128_f8f6f4 v[114:117], v[26:33], v[174:181], v[114:117], v234, v234 op_sel_hi:[0,0,0]
	v_mfma_scale_f32_16x16x128_f8f6f4 v[90:93], v[18:25], v[182:189], v[90:93], v234, v234 op_sel_hi:[0,0,0]
	v_mfma_scale_f32_16x16x128_f8f6f4 v[82:85], v[26:33], v[182:189], v[82:85], v234, v234 op_sel_hi:[0,0,0]
	v_mfma_scale_f32_16x16x128_f8f6f4 v[58:61], v[18:25], v[190:197], v[58:61], v234, v234 op_sel_hi:[0,0,0]
	v_mfma_scale_f32_16x16x128_f8f6f4 v[50:53], v[26:33], v[190:197], v[50:53], v234, v234 op_sel_hi:[0,0,0]
	v_mfma_scale_f32_16x16x128_f8f6f4 v[38:41], v[18:25], v[204:211], v[38:41], v234, v234 op_sel_hi:[0,0,0]
	v_mfma_scale_f32_16x16x128_f8f6f4 v[34:37], v[26:33], v[204:211], v[34:37], v234, v234 op_sel_hi:[0,0,0]
	s_setprio 0
	s_barrier
	ds_read_b128 v[18:21], v171
	ds_read_b128 v[22:25], v171 offset:1024
	ds_read_b128 v[26:29], v171 offset:2048
	ds_read_b128 v[30:33], v171 offset:3072
	ds_read_b128 v[10:13], v172
	ds_read_b128 v[14:17], v172 offset:1024
	ds_read_b128 v[2:5], v172 offset:2048
	ds_read_b128 v[6:9], v172 offset:3072
	s_mov_b32 m0, s20
	ds_read_b128 v[174:177], v168 offset:32768
	ds_read_b128 v[178:181], v168 offset:33792
	ds_read_b128 v[182:185], v168 offset:34816
	ds_read_b128 v[186:189], v168 offset:35840
	ds_read_b128 v[190:193], v168 offset:36864
	ds_read_b128 v[194:197], v168 offset:37888
	ds_read_b128 v[204:207], v168 offset:38912
	ds_read_b128 v[208:211], v168 offset:39936
	s_mov_b32 m0, s78
	s_nop 0
	s_add_i32 s52, s52, 0x40000
	s_mov_b32 m0, s79
	s_nop 0
	s_mov_b32 m0, s80
	s_nop 0
	s_waitcnt vmcnt(8)
	s_waitcnt lgkmcnt(0)
	s_barrier
	s_setprio 1
	s_waitcnt lgkmcnt(6)
	v_mfma_scale_f32_16x16x128_f8f6f4 v[138:141], v[18:25], v[174:181], v[138:141], v234, v234 op_sel_hi:[0,0,0]
	v_mfma_scale_f32_16x16x128_f8f6f4 v[146:149], v[26:33], v[174:181], v[146:149], v234, v234 op_sel_hi:[0,0,0]
	s_waitcnt lgkmcnt(4)
	v_mfma_scale_f32_16x16x128_f8f6f4 v[134:137], v[18:25], v[182:189], v[134:137], v234, v234 op_sel_hi:[0,0,0]
	v_mfma_scale_f32_16x16x128_f8f6f4 v[130:133], v[26:33], v[182:189], v[130:133], v234, v234 op_sel_hi:[0,0,0]
	s_waitcnt lgkmcnt(2)
	v_mfma_scale_f32_16x16x128_f8f6f4 v[110:113], v[18:25], v[190:197], v[110:113], v234, v234 op_sel_hi:[0,0,0]
	v_mfma_scale_f32_16x16x128_f8f6f4 v[102:105], v[26:33], v[190:197], v[102:105], v234, v234 op_sel_hi:[0,0,0]
	s_waitcnt lgkmcnt(0)
	v_mfma_scale_f32_16x16x128_f8f6f4 v[78:81], v[18:25], v[204:211], v[78:81], v234, v234 op_sel_hi:[0,0,0]
	v_mfma_scale_f32_16x16x128_f8f6f4 v[70:73], v[26:33], v[204:211], v[70:73], v234, v234 op_sel_hi:[0,0,0]
	v_mfma_scale_f32_16x16x128_f8f6f4 v[154:157], v[10:17], v[174:181], v[154:157], v234, v234 op_sel_hi:[0,0,0]
	v_mfma_scale_f32_16x16x128_f8f6f4 v[158:161], v[2:9], v[174:181], v[158:161], v234, v234 op_sel_hi:[0,0,0]
	v_mfma_scale_f32_16x16x128_f8f6f4 v[150:153], v[10:17], v[182:189], v[150:153], v234, v234 op_sel_hi:[0,0,0]
	v_mfma_scale_f32_16x16x128_f8f6f4 v[142:145], v[2:9], v[182:189], v[142:145], v234, v234 op_sel_hi:[0,0,0]
	v_mfma_scale_f32_16x16x128_f8f6f4 v[126:129], v[10:17], v[190:197], v[126:129], v234, v234 op_sel_hi:[0,0,0]
	v_mfma_scale_f32_16x16x128_f8f6f4 v[118:121], v[2:9], v[190:197], v[118:121], v234, v234 op_sel_hi:[0,0,0]
	v_mfma_scale_f32_16x16x128_f8f6f4 v[94:97], v[10:17], v[204:211], v[94:97], v234, v234 op_sel_hi:[0,0,0]
	v_mfma_scale_f32_16x16x128_f8f6f4 v[86:89], v[2:9], v[204:211], v[86:89], v234, v234 op_sel_hi:[0,0,0]
	s_setprio 0
	s_barrier
	s_mov_b32 m0, s81
	s_or_b32 s52, s51, 0x80
	ds_read_b128 v[174:177], v168 offset:49152
	ds_read_b128 v[178:181], v168 offset:50176
	ds_read_b128 v[182:185], v168 offset:51200
	ds_read_b128 v[186:189], v168 offset:52224
	ds_read_b128 v[190:193], v168 offset:53248
	ds_read_b128 v[194:197], v168 offset:54272
	ds_read_b128 v[204:207], v168 offset:55296
	ds_read_b128 v[208:211], v168 offset:56320
	s_mov_b32 m0, s82
	s_add_i32 s51, s51, 0x40080
	s_mov_b32 m0, s83
	s_nop 0
	s_mov_b32 m0, s84
	s_nop 0
	s_waitcnt vmcnt(6)
	s_waitcnt lgkmcnt(0)
	s_barrier
	s_setprio 1
	s_waitcnt lgkmcnt(6)
	v_mfma_scale_f32_16x16x128_f8f6f4 v[106:109], v[18:25], v[174:181], v[106:109], v234, v234 op_sel_hi:[0,0,0]
	v_mfma_scale_f32_16x16x128_f8f6f4 v[98:101], v[26:33], v[174:181], v[98:101], v234, v234 op_sel_hi:[0,0,0]
	s_waitcnt lgkmcnt(4)
	v_mfma_scale_f32_16x16x128_f8f6f4 v[74:77], v[18:25], v[182:189], v[74:77], v234, v234 op_sel_hi:[0,0,0]
	v_mfma_scale_f32_16x16x128_f8f6f4 v[66:69], v[26:33], v[182:189], v[66:69], v234, v234 op_sel_hi:[0,0,0]
	s_waitcnt lgkmcnt(2)
	v_mfma_scale_f32_16x16x128_f8f6f4 v[62:65], v[18:25], v[190:197], v[62:65], v234, v234 op_sel_hi:[0,0,0]
	v_mfma_scale_f32_16x16x128_f8f6f4 v[54:57], v[26:33], v[190:197], v[54:57], v234, v234 op_sel_hi:[0,0,0]
	s_waitcnt lgkmcnt(0)
	v_mfma_scale_f32_16x16x128_f8f6f4 v[46:49], v[18:25], v[204:211], v[46:49], v234, v234 op_sel_hi:[0,0,0]
	v_mfma_scale_f32_16x16x128_f8f6f4 v[42:45], v[26:33], v[204:211], v[42:45], v234, v234 op_sel_hi:[0,0,0]
	v_mfma_scale_f32_16x16x128_f8f6f4 v[122:125], v[10:17], v[174:181], v[122:125], v234, v234 op_sel_hi:[0,0,0]
	v_mfma_scale_f32_16x16x128_f8f6f4 v[114:117], v[2:9], v[174:181], v[114:117], v234, v234 op_sel_hi:[0,0,0]
	v_mfma_scale_f32_16x16x128_f8f6f4 v[90:93], v[10:17], v[182:189], v[90:93], v234, v234 op_sel_hi:[0,0,0]
	v_mfma_scale_f32_16x16x128_f8f6f4 v[82:85], v[2:9], v[182:189], v[82:85], v234, v234 op_sel_hi:[0,0,0]
	v_mfma_scale_f32_16x16x128_f8f6f4 v[58:61], v[10:17], v[190:197], v[58:61], v234, v234 op_sel_hi:[0,0,0]
	v_mfma_scale_f32_16x16x128_f8f6f4 v[50:53], v[2:9], v[190:197], v[50:53], v234, v234 op_sel_hi:[0,0,0]
	v_mfma_scale_f32_16x16x128_f8f6f4 v[38:41], v[10:17], v[204:211], v[38:41], v234, v234 op_sel_hi:[0,0,0]
	v_mfma_scale_f32_16x16x128_f8f6f4 v[34:37], v[2:9], v[204:211], v[34:37], v234, v234 op_sel_hi:[0,0,0]
	s_setprio 0
	s_barrier
	s_add_i32 s49, s49, 2
	s_addk_i32 s18, 0x100
	s_addk_i32 s19, 0x100
	s_cmp_gt_u32 s49, 13
.Lex_7:
	s_nop 15
	s_nop 15
	s_and_b64 vcc, exec, s[26:27]
	s_cbranch_vccz .LBB0_875
	s_barrier

.LBB0_1797:
	ds_read_b128 v[142:145], v137
	ds_read_b128 v[146:149], v137 offset:1024
	ds_read_b128 v[150:153], v137 offset:2048
	ds_read_b128 v[154:157], v137 offset:3072
	ds_read_b128 v[158:161], v138
	ds_read_b128 v[162:165], v138 offset:1024
	ds_read_b128 v[166:169], v138 offset:2048
	ds_read_b128 v[170:173], v138 offset:3072
	s_add_i32 s73, s41, s62
	s_add_i32 s76, s73, 0x100
	s_add_i32 s77, s73, 0x200
	s_add_i32 s72, s59, s62
	s_cmpk_eq_i32 s62, 0xe00
	s_cselect_b32 s72, s61, s72
	s_cselect_b32 s77, s60, s77
	s_cbranch_scc0 .Lnx_8
	s_cmp_eq_u64 s[22:23], 0
	s_cbranch_scc1 .Lfin_8
.Lnx_8:
	s_addk_i32 s73, 0x180
	s_mov_b32 m0, s49
	ds_read_b128 v[174:177], v136
	ds_read_b128 v[178:181], v136 offset:1024
	ds_read_b128 v[182:185], v136 offset:2048
	ds_read_b128 v[186:189], v136 offset:3072
	ds_read_b128 v[190:193], v136 offset:4096
	ds_read_b128 v[194:197], v136 offset:5120
	ds_read_b128 v[198:201], v136 offset:6144
	ds_read_b128 v[204:207], v136 offset:7168
	buffer_load_dwordx4 v131, s[64:67], s73 offen lds
	s_mov_b32 m0, s51
	s_nop 0
	buffer_load_dwordx4 v133, s[64:67], s73 offen lds
	s_or_b32 s73, s76, 0x80080
	s_mov_b32 m0, s50
	s_nop 0
	buffer_load_dwordx4 v131, s[64:67], s73 offen lds
	s_mov_b32 m0, s52
	s_nop 0
	buffer_load_dwordx4 v133, s[64:67], s73 offen lds
	s_waitcnt vmcnt(8)
	s_waitcnt lgkmcnt(0)
	s_barrier
	s_setprio 1
	s_waitcnt lgkmcnt(7)
	v_mfma_f32_16x16x32_bf16 v[122:125], v[142:145], v[174:177], v[122:125]
	v_mfma_f32_16x16x32_bf16 v[126:129], v[150:153], v[174:177], v[126:129]
	s_waitcnt lgkmcnt(5)
	v_mfma_f32_16x16x32_bf16 v[114:117], v[142:145], v[182:185], v[114:117]
	v_mfma_f32_16x16x32_bf16 v[118:121], v[150:153], v[182:185], v[118:121]
	s_waitcnt lgkmcnt(3)
	v_mfma_f32_16x16x32_bf16 v[110:113], v[142:145], v[190:193], v[110:113]
	v_mfma_f32_16x16x32_bf16 v[106:109], v[150:153], v[190:193], v[106:109]
	s_waitcnt lgkmcnt(1)
	v_mfma_f32_16x16x32_bf16 v[98:101], v[142:145], v[198:201], v[98:101]
	v_mfma_f32_16x16x32_bf16 v[102:105], v[150:153], v[198:201], v[102:105]
	v_mfma_f32_16x16x32_bf16 v[58:61], v[158:161], v[174:177], v[58:61]
	v_mfma_f32_16x16x32_bf16 v[62:65], v[166:169], v[174:177], v[62:65]
	v_mfma_f32_16x16x32_bf16 v[50:53], v[158:161], v[182:185], v[50:53]
	v_mfma_f32_16x16x32_bf16 v[54:57], v[166:169], v[182:185], v[54:57]
	v_mfma_f32_16x16x32_bf16 v[42:45], v[158:161], v[190:193], v[42:45]
	v_mfma_f32_16x16x32_bf16 v[46:49], v[166:169], v[190:193], v[46:49]
	v_mfma_f32_16x16x32_bf16 v[34:37], v[158:161], v[198:201], v[34:37]
	v_mfma_f32_16x16x32_bf16 v[38:41], v[166:169], v[198:201], v[38:41]
	v_mfma_f32_16x16x32_bf16 v[122:125], v[146:149], v[178:181], v[122:125]
	v_mfma_f32_16x16x32_bf16 v[126:129], v[154:157], v[178:181], v[126:129]
	v_mfma_f32_16x16x32_bf16 v[114:117], v[146:149], v[186:189], v[114:117]
	v_mfma_f32_16x16x32_bf16 v[118:121], v[154:157], v[186:189], v[118:121]
	v_mfma_f32_16x16x32_bf16 v[110:113], v[146:149], v[194:197], v[110:113]
	v_mfma_f32_16x16x32_bf16 v[106:109], v[154:157], v[194:197], v[106:109]
	s_waitcnt lgkmcnt(0)
	v_mfma_f32_16x16x32_bf16 v[98:101], v[146:149], v[204:207], v[98:101]
	v_mfma_f32_16x16x32_bf16 v[102:105], v[154:157], v[204:207], v[102:105]
	v_mfma_f32_16x16x32_bf16 v[58:61], v[162:165], v[178:181], v[58:61]
	v_mfma_f32_16x16x32_bf16 v[62:65], v[170:173], v[178:181], v[62:65]
	v_mfma_f32_16x16x32_bf16 v[50:53], v[162:165], v[186:189], v[50:53]
	v_mfma_f32_16x16x32_bf16 v[54:57], v[170:173], v[186:189], v[54:57]
	v_mfma_f32_16x16x32_bf16 v[42:45], v[162:165], v[194:197], v[42:45]
	v_mfma_f32_16x16x32_bf16 v[46:49], v[170:173], v[194:197], v[46:49]
	v_mfma_f32_16x16x32_bf16 v[34:37], v[162:165], v[204:207], v[34:37]
	v_mfma_f32_16x16x32_bf16 v[38:41], v[170:173], v[204:207], v[38:41]
	s_setprio 0
	s_barrier
	s_mov_b32 m0, s35
	ds_read_b128 v[174:177], v136 offset:16384
	ds_read_b128 v[178:181], v136 offset:17408
	ds_read_b128 v[182:185], v136 offset:18432
	ds_read_b128 v[186:189], v136 offset:19456
	ds_read_b128 v[190:193], v136 offset:20480
	ds_read_b128 v[194:197], v136 offset:21504
	ds_read_b128 v[198:201], v136 offset:22528
	ds_read_b128 v[204:207], v136 offset:23552
	buffer_load_dwordx4 v132, s[0:3], s72 offen lds
	s_mov_b32 m0, s37
	s_or_b32 s73, s72, 0x80000
	buffer_load_dwordx4 v134, s[0:3], s72 offen lds
	s_mov_b32 m0, s38
	s_nop 0
	buffer_load_dwordx4 v132, s[0:3], s73 offen lds
	s_mov_b32 m0, s39
	s_nop 0
	buffer_load_dwordx4 v134, s[0:3], s73 offen lds
	s_waitcnt vmcnt(6)
	s_waitcnt lgkmcnt(0)
	s_barrier
	s_setprio 1
	s_waitcnt lgkmcnt(7)
	v_mfma_f32_16x16x32_bf16 v[90:93], v[142:145], v[174:177], v[90:93]
	v_mfma_f32_16x16x32_bf16 v[94:97], v[150:153], v[174:177], v[94:97]
	s_waitcnt lgkmcnt(5)
	v_mfma_f32_16x16x32_bf16 v[82:85], v[142:145], v[182:185], v[82:85]
	v_mfma_f32_16x16x32_bf16 v[86:89], v[150:153], v[182:185], v[86:89]
	s_waitcnt lgkmcnt(3)
	v_mfma_f32_16x16x32_bf16 v[74:77], v[142:145], v[190:193], v[74:77]
	v_mfma_f32_16x16x32_bf16 v[78:81], v[150:153], v[190:193], v[78:81]
	s_waitcnt lgkmcnt(1)
	v_mfma_f32_16x16x32_bf16 v[66:69], v[142:145], v[198:201], v[66:69]
	v_mfma_f32_16x16x32_bf16 v[70:73], v[150:153], v[198:201], v[70:73]
	v_mfma_f32_16x16x32_bf16 v[26:29], v[158:161], v[174:177], v[26:29]
	v_mfma_f32_16x16x32_bf16 v[30:33], v[166:169], v[174:177], v[30:33]
	v_mfma_f32_16x16x32_bf16 v[18:21], v[158:161], v[182:185], v[18:21]
	v_mfma_f32_16x16x32_bf16 v[22:25], v[166:169], v[182:185], v[22:25]
	v_mfma_f32_16x16x32_bf16 v[10:13], v[158:161], v[190:193], v[10:13]
	v_mfma_f32_16x16x32_bf16 v[14:17], v[166:169], v[190:193], v[14:17]
	v_mfma_f32_16x16x32_bf16 v[2:5], v[158:161], v[198:201], v[2:5]
	v_mfma_f32_16x16x32_bf16 v[6:9], v[166:169], v[198:201], v[6:9]
	v_mfma_f32_16x16x32_bf16 v[90:93], v[146:149], v[178:181], v[90:93]
	v_mfma_f32_16x16x32_bf16 v[94:97], v[154:157], v[178:181], v[94:97]
	v_mfma_f32_16x16x32_bf16 v[82:85], v[146:149], v[186:189], v[82:85]
	v_mfma_f32_16x16x32_bf16 v[86:89], v[154:157], v[186:189], v[86:89]
	v_mfma_f32_16x16x32_bf16 v[74:77], v[146:149], v[194:197], v[74:77]
	v_mfma_f32_16x16x32_bf16 v[78:81], v[154:157], v[194:197], v[78:81]
	s_waitcnt lgkmcnt(0)
	v_mfma_f32_16x16x32_bf16 v[66:69], v[146:149], v[204:207], v[66:69]
	v_mfma_f32_16x16x32_bf16 v[70:73], v[154:157], v[204:207], v[70:73]
	v_mfma_f32_16x16x32_bf16 v[26:29], v[162:165], v[178:181], v[26:29]
	v_mfma_f32_16x16x32_bf16 v[30:33], v[170:173], v[178:181], v[30:33]
	v_mfma_f32_16x16x32_bf16 v[18:21], v[162:165], v[186:189], v[18:21]
	v_mfma_f32_16x16x32_bf16 v[22:25], v[170:173], v[186:189], v[22:25]
	v_mfma_f32_16x16x32_bf16 v[10:13], v[162:165], v[194:197], v[10:13]
	v_mfma_f32_16x16x32_bf16 v[14:17], v[170:173], v[194:197], v[14:17]
	v_mfma_f32_16x16x32_bf16 v[2:5], v[162:165], v[204:207], v[2:5]
	v_mfma_f32_16x16x32_bf16 v[6:9], v[170:173], v[204:207], v[6:9]
	s_setprio 0
	s_barrier
	ds_read_b128 v[142:145], v139
	ds_read_b128 v[146:149], v139 offset:1024
	ds_read_b128 v[150:153], v139 offset:2048
	ds_read_b128 v[154:157], v139 offset:3072
	ds_read_b128 v[158:161], v140
	ds_read_b128 v[162:165], v140 offset:1024
	ds_read_b128 v[166:169], v140 offset:2048
	ds_read_b128 v[170:173], v140 offset:3072
	s_mov_b32 m0, s34
	ds_read_b128 v[174:177], v136 offset:32768
	ds_read_b128 v[178:181], v136 offset:33792
	ds_read_b128 v[182:185], v136 offset:34816
	ds_read_b128 v[186:189], v136 offset:35840
	ds_read_b128 v[190:193], v136 offset:36864
	ds_read_b128 v[194:197], v136 offset:37888
	ds_read_b128 v[198:201], v136 offset:38912
	ds_read_b128 v[204:207], v136 offset:39936
	buffer_load_dwordx4 v131, s[64:67], s77 offen lds
	s_mov_b32 m0, s40
	s_nop 0
	buffer_load_dwordx4 v133, s[64:67], s77 offen lds
	s_bitset1_b32 s77, 19
	s_mov_b32 m0, s42
	s_nop 0
	buffer_load_dwordx4 v131, s[64:67], s77 offen lds
	s_mov_b32 m0, s43
	s_nop 0
	buffer_load_dwordx4 v133, s[64:67], s77 offen lds
	s_waitcnt vmcnt(8)
	s_waitcnt lgkmcnt(0)
	s_barrier
	s_setprio 1
	s_waitcnt lgkmcnt(7)
	v_mfma_f32_16x16x32_bf16 v[122:125], v[142:145], v[174:177], v[122:125]
	v_mfma_f32_16x16x32_bf16 v[126:129], v[150:153], v[174:177], v[126:129]
	s_waitcnt lgkmcnt(5)
	v_mfma_f32_16x16x32_bf16 v[114:117], v[142:145], v[182:185], v[114:117]
	v_mfma_f32_16x16x32_bf16 v[118:121], v[150:153], v[182:185], v[118:121]
	s_waitcnt lgkmcnt(3)
	v_mfma_f32_16x16x32_bf16 v[110:113], v[142:145], v[190:193], v[110:113]
	v_mfma_f32_16x16x32_bf16 v[106:109], v[150:153], v[190:193], v[106:109]
	s_waitcnt lgkmcnt(1)
	v_mfma_f32_16x16x32_bf16 v[98:101], v[142:145], v[198:201], v[98:101]
	v_mfma_f32_16x16x32_bf16 v[102:105], v[150:153], v[198:201], v[102:105]
	v_mfma_f32_16x16x32_bf16 v[58:61], v[158:161], v[174:177], v[58:61]
	v_mfma_f32_16x16x32_bf16 v[62:65], v[166:169], v[174:177], v[62:65]
	v_mfma_f32_16x16x32_bf16 v[50:53], v[158:161], v[182:185], v[50:53]
	v_mfma_f32_16x16x32_bf16 v[54:57], v[166:169], v[182:185], v[54:57]
	v_mfma_f32_16x16x32_bf16 v[42:45], v[158:161], v[190:193], v[42:45]
	v_mfma_f32_16x16x32_bf16 v[46:49], v[166:169], v[190:193], v[46:49]
	v_mfma_f32_16x16x32_bf16 v[34:37], v[158:161], v[198:201], v[34:37]
	v_mfma_f32_16x16x32_bf16 v[38:41], v[166:169], v[198:201], v[38:41]
	v_mfma_f32_16x16x32_bf16 v[122:125], v[146:149], v[178:181], v[122:125]
	v_mfma_f32_16x16x32_bf16 v[126:129], v[154:157], v[178:181], v[126:129]
	v_mfma_f32_16x16x32_bf16 v[114:117], v[146:149], v[186:189], v[114:117]
	v_mfma_f32_16x16x32_bf16 v[118:121], v[154:157], v[186:189], v[118:121]
	v_mfma_f32_16x16x32_bf16 v[110:113], v[146:149], v[194:197], v[110:113]
	v_mfma_f32_16x16x32_bf16 v[106:109], v[154:157], v[194:197], v[106:109]
	s_waitcnt lgkmcnt(0)
	v_mfma_f32_16x16x32_bf16 v[98:101], v[146:149], v[204:207], v[98:101]
	v_mfma_f32_16x16x32_bf16 v[102:105], v[154:157], v[204:207], v[102:105]
	v_mfma_f32_16x16x32_bf16 v[58:61], v[162:165], v[178:181], v[58:61]
	v_mfma_f32_16x16x32_bf16 v[62:65], v[170:173], v[178:181], v[62:65]
	v_mfma_f32_16x16x32_bf16 v[50:53], v[162:165], v[186:189], v[50:53]
	v_mfma_f32_16x16x32_bf16 v[54:57], v[170:173], v[186:189], v[54:57]
	v_mfma_f32_16x16x32_bf16 v[42:45], v[162:165], v[194:197], v[42:45]
	v_mfma_f32_16x16x32_bf16 v[46:49], v[170:173], v[194:197], v[46:49]
	v_mfma_f32_16x16x32_bf16 v[34:37], v[162:165], v[204:207], v[34:37]
	v_mfma_f32_16x16x32_bf16 v[38:41], v[170:173], v[204:207], v[38:41]
	s_setprio 0
	s_barrier
	s_mov_b32 m0, s45
	s_or_b32 s73, s72, 0x80
	ds_read_b128 v[174:177], v136 offset:49152
	ds_read_b128 v[178:181], v136 offset:50176
	ds_read_b128 v[182:185], v136 offset:51200
	ds_read_b128 v[186:189], v136 offset:52224
	ds_read_b128 v[190:193], v136 offset:53248
	ds_read_b128 v[194:197], v136 offset:54272
	ds_read_b128 v[198:201], v136 offset:55296
	ds_read_b128 v[204:207], v136 offset:56320
	buffer_load_dwordx4 v132, s[0:3], s73 offen lds
	s_mov_b32 m0, s46
	s_or_b32 s72, s72, 0x80080
	buffer_load_dwordx4 v134, s[0:3], s73 offen lds
	s_mov_b32 m0, s47
	s_nop 0
	buffer_load_dwordx4 v132, s[0:3], s72 offen lds
	s_mov_b32 m0, s48
	s_nop 0
	buffer_load_dwordx4 v134, s[0:3], s72 offen lds
	s_waitcnt vmcnt(6)
	s_waitcnt lgkmcnt(0)
	s_barrier
	s_setprio 1
	s_waitcnt lgkmcnt(7)
	v_mfma_f32_16x16x32_bf16 v[90:93], v[142:145], v[174:177], v[90:93]
	v_mfma_f32_16x16x32_bf16 v[94:97], v[150:153], v[174:177], v[94:97]
	s_waitcnt lgkmcnt(5)
	v_mfma_f32_16x16x32_bf16 v[82:85], v[142:145], v[182:185], v[82:85]
	v_mfma_f32_16x16x32_bf16 v[86:89], v[150:153], v[182:185], v[86:89]
	s_waitcnt lgkmcnt(3)
	v_mfma_f32_16x16x32_bf16 v[74:77], v[142:145], v[190:193], v[74:77]
	v_mfma_f32_16x16x32_bf16 v[78:81], v[150:153], v[190:193], v[78:81]
	s_waitcnt lgkmcnt(1)
	v_mfma_f32_16x16x32_bf16 v[66:69], v[142:145], v[198:201], v[66:69]
	v_mfma_f32_16x16x32_bf16 v[70:73], v[150:153], v[198:201], v[70:73]
	v_mfma_f32_16x16x32_bf16 v[26:29], v[158:161], v[174:177], v[26:29]
	v_mfma_f32_16x16x32_bf16 v[30:33], v[166:169], v[174:177], v[30:33]
	v_mfma_f32_16x16x32_bf16 v[18:21], v[158:161], v[182:185], v[18:21]
	v_mfma_f32_16x16x32_bf16 v[22:25], v[166:169], v[182:185], v[22:25]
	v_mfma_f32_16x16x32_bf16 v[10:13], v[158:161], v[190:193], v[10:13]
	v_mfma_f32_16x16x32_bf16 v[14:17], v[166:169], v[190:193], v[14:17]
	v_mfma_f32_16x16x32_bf16 v[2:5], v[158:161], v[198:201], v[2:5]
	v_mfma_f32_16x16x32_bf16 v[6:9], v[166:169], v[198:201], v[6:9]
	v_mfma_f32_16x16x32_bf16 v[90:93], v[146:149], v[178:181], v[90:93]
	v_mfma_f32_16x16x32_bf16 v[94:97], v[154:157], v[178:181], v[94:97]
	v_mfma_f32_16x16x32_bf16 v[82:85], v[146:149], v[186:189], v[82:85]
	v_mfma_f32_16x16x32_bf16 v[86:89], v[154:157], v[186:189], v[86:89]
	v_mfma_f32_16x16x32_bf16 v[74:77], v[146:149], v[194:197], v[74:77]
	v_mfma_f32_16x16x32_bf16 v[78:81], v[154:157], v[194:197], v[78:81]
	s_waitcnt lgkmcnt(0)
	v_mfma_f32_16x16x32_bf16 v[66:69], v[146:149], v[204:207], v[66:69]
	v_mfma_f32_16x16x32_bf16 v[70:73], v[154:157], v[204:207], v[70:73]
	v_mfma_f32_16x16x32_bf16 v[26:29], v[162:165], v[178:181], v[26:29]
	v_mfma_f32_16x16x32_bf16 v[30:33], v[170:173], v[178:181], v[30:33]
	v_mfma_f32_16x16x32_bf16 v[18:21], v[162:165], v[186:189], v[18:21]
	v_mfma_f32_16x16x32_bf16 v[22:25], v[170:173], v[186:189], v[22:25]
	v_mfma_f32_16x16x32_bf16 v[10:13], v[162:165], v[194:197], v[10:13]
	v_mfma_f32_16x16x32_bf16 v[14:17], v[170:173], v[194:197], v[14:17]
	v_mfma_f32_16x16x32_bf16 v[2:5], v[162:165], v[204:207], v[2:5]
	v_mfma_f32_16x16x32_bf16 v[6:9], v[170:173], v[204:207], v[6:9]
	s_setprio 0
	s_barrier
	s_add_i32 s63, s63, 2
	s_addk_i32 s62, 0x100
	s_cmp_gt_u32 s63, 29
	s_cbranch_scc0 .LBB0_1797
	s_branch .Lex_8
.Lfin_8:
	s_addk_i32 s73, 0x180
	s_mov_b32 m0, s49
	ds_read_b128 v[174:177], v136
	ds_read_b128 v[178:181], v136 offset:1024
	ds_read_b128 v[182:185], v136 offset:2048
	ds_read_b128 v[186:189], v136 offset:3072
	ds_read_b128 v[190:193], v136 offset:4096
	ds_read_b128 v[194:197], v136 offset:5120
	ds_read_b128 v[198:201], v136 offset:6144
	ds_read_b128 v[204:207], v136 offset:7168
	buffer_load_dwordx4 v131, s[64:67], s73 offen lds
	s_mov_b32 m0, s51
	s_nop 0
	buffer_load_dwordx4 v133, s[64:67], s73 offen lds
	s_or_b32 s73, s76, 0x80080
	s_mov_b32 m0, s50
	s_nop 0
	buffer_load_dwordx4 v131, s[64:67], s73 offen lds
	s_mov_b32 m0, s52
	s_nop 0
	buffer_load_dwordx4 v133, s[64:67], s73 offen lds
	s_waitcnt vmcnt(8)
	s_waitcnt lgkmcnt(0)
	s_barrier
	s_setprio 1
	s_waitcnt lgkmcnt(7)
	v_mfma_f32_16x16x32_bf16 v[122:125], v[142:145], v[174:177], v[122:125]
	v_mfma_f32_16x16x32_bf16 v[126:129], v[150:153], v[174:177], v[126:129]
	s_waitcnt lgkmcnt(5)
	v_mfma_f32_16x16x32_bf16 v[114:117], v[142:145], v[182:185], v[114:117]
	v_mfma_f32_16x16x32_bf16 v[118:121], v[150:153], v[182:185], v[118:121]
	s_waitcnt lgkmcnt(3)
	v_mfma_f32_16x16x32_bf16 v[110:113], v[142:145], v[190:193], v[110:113]
	v_mfma_f32_16x16x32_bf16 v[106:109], v[150:153], v[190:193], v[106:109]
	s_waitcnt lgkmcnt(1)
	v_mfma_f32_16x16x32_bf16 v[98:101], v[142:145], v[198:201], v[98:101]
	v_mfma_f32_16x16x32_bf16 v[102:105], v[150:153], v[198:201], v[102:105]
	v_mfma_f32_16x16x32_bf16 v[58:61], v[158:161], v[174:177], v[58:61]
	v_mfma_f32_16x16x32_bf16 v[62:65], v[166:169], v[174:177], v[62:65]
	v_mfma_f32_16x16x32_bf16 v[50:53], v[158:161], v[182:185], v[50:53]
	v_mfma_f32_16x16x32_bf16 v[54:57], v[166:169], v[182:185], v[54:57]
	v_mfma_f32_16x16x32_bf16 v[42:45], v[158:161], v[190:193], v[42:45]
	v_mfma_f32_16x16x32_bf16 v[46:49], v[166:169], v[190:193], v[46:49]
	v_mfma_f32_16x16x32_bf16 v[34:37], v[158:161], v[198:201], v[34:37]
	v_mfma_f32_16x16x32_bf16 v[38:41], v[166:169], v[198:201], v[38:41]
	v_mfma_f32_16x16x32_bf16 v[122:125], v[146:149], v[178:181], v[122:125]
	v_mfma_f32_16x16x32_bf16 v[126:129], v[154:157], v[178:181], v[126:129]
	v_mfma_f32_16x16x32_bf16 v[114:117], v[146:149], v[186:189], v[114:117]
	v_mfma_f32_16x16x32_bf16 v[118:121], v[154:157], v[186:189], v[118:121]
	v_mfma_f32_16x16x32_bf16 v[110:113], v[146:149], v[194:197], v[110:113]
	v_mfma_f32_16x16x32_bf16 v[106:109], v[154:157], v[194:197], v[106:109]
	s_waitcnt lgkmcnt(0)
	v_mfma_f32_16x16x32_bf16 v[98:101], v[146:149], v[204:207], v[98:101]
	v_mfma_f32_16x16x32_bf16 v[102:105], v[154:157], v[204:207], v[102:105]
	v_mfma_f32_16x16x32_bf16 v[58:61], v[162:165], v[178:181], v[58:61]
	v_mfma_f32_16x16x32_bf16 v[62:65], v[170:173], v[178:181], v[62:65]
	v_mfma_f32_16x16x32_bf16 v[50:53], v[162:165], v[186:189], v[50:53]
	v_mfma_f32_16x16x32_bf16 v[54:57], v[170:173], v[186:189], v[54:57]
	v_mfma_f32_16x16x32_bf16 v[42:45], v[162:165], v[194:197], v[42:45]
	v_mfma_f32_16x16x32_bf16 v[46:49], v[170:173], v[194:197], v[46:49]
	v_mfma_f32_16x16x32_bf16 v[34:37], v[162:165], v[204:207], v[34:37]
	v_mfma_f32_16x16x32_bf16 v[38:41], v[170:173], v[204:207], v[38:41]
	s_setprio 0
	s_barrier
	s_mov_b32 m0, s35
	ds_read_b128 v[174:177], v136 offset:16384
	ds_read_b128 v[178:181], v136 offset:17408
	ds_read_b128 v[182:185], v136 offset:18432
	ds_read_b128 v[186:189], v136 offset:19456
	ds_read_b128 v[190:193], v136 offset:20480
	ds_read_b128 v[194:197], v136 offset:21504
	ds_read_b128 v[198:201], v136 offset:22528
	ds_read_b128 v[204:207], v136 offset:23552
	s_mov_b32 m0, s37
	s_or_b32 s73, s72, 0x80000
	s_mov_b32 m0, s38
	s_nop 0
	s_mov_b32 m0, s39
	s_nop 0
	s_waitcnt vmcnt(0)
	s_waitcnt lgkmcnt(0)
	s_barrier
	s_setprio 1
	s_waitcnt lgkmcnt(7)
	v_mfma_f32_16x16x32_bf16 v[90:93], v[142:145], v[174:177], v[90:93]
	v_mfma_f32_16x16x32_bf16 v[94:97], v[150:153], v[174:177], v[94:97]
	s_waitcnt lgkmcnt(5)
	v_mfma_f32_16x16x32_bf16 v[82:85], v[142:145], v[182:185], v[82:85]
	v_mfma_f32_16x16x32_bf16 v[86:89], v[150:153], v[182:185], v[86:89]
	s_waitcnt lgkmcnt(3)
	v_mfma_f32_16x16x32_bf16 v[74:77], v[142:145], v[190:193], v[74:77]
	v_mfma_f32_16x16x32_bf16 v[78:81], v[150:153], v[190:193], v[78:81]
	s_waitcnt lgkmcnt(1)
	v_mfma_f32_16x16x32_bf16 v[66:69], v[142:145], v[198:201], v[66:69]
	v_mfma_f32_16x16x32_bf16 v[70:73], v[150:153], v[198:201], v[70:73]
	v_mfma_f32_16x16x32_bf16 v[26:29], v[158:161], v[174:177], v[26:29]
	v_mfma_f32_16x16x32_bf16 v[30:33], v[166:169], v[174:177], v[30:33]
	v_mfma_f32_16x16x32_bf16 v[18:21], v[158:161], v[182:185], v[18:21]
	v_mfma_f32_16x16x32_bf16 v[22:25], v[166:169], v[182:185], v[22:25]
	v_mfma_f32_16x16x32_bf16 v[10:13], v[158:161], v[190:193], v[10:13]
	v_mfma_f32_16x16x32_bf16 v[14:17], v[166:169], v[190:193], v[14:17]
	v_mfma_f32_16x16x32_bf16 v[2:5], v[158:161], v[198:201], v[2:5]
	v_mfma_f32_16x16x32_bf16 v[6:9], v[166:169], v[198:201], v[6:9]
	v_mfma_f32_16x16x32_bf16 v[90:93], v[146:149], v[178:181], v[90:93]
	v_mfma_f32_16x16x32_bf16 v[94:97], v[154:157], v[178:181], v[94:97]
	v_mfma_f32_16x16x32_bf16 v[82:85], v[146:149], v[186:189], v[82:85]
	v_mfma_f32_16x16x32_bf16 v[86:89], v[154:157], v[186:189], v[86:89]
	v_mfma_f32_16x16x32_bf16 v[74:77], v[146:149], v[194:197], v[74:77]
	v_mfma_f32_16x16x32_bf16 v[78:81], v[154:157], v[194:197], v[78:81]
	s_waitcnt lgkmcnt(0)
	v_mfma_f32_16x16x32_bf16 v[66:69], v[146:149], v[204:207], v[66:69]
	v_mfma_f32_16x16x32_bf16 v[70:73], v[154:157], v[204:207], v[70:73]
	v_mfma_f32_16x16x32_bf16 v[26:29], v[162:165], v[178:181], v[26:29]
	v_mfma_f32_16x16x32_bf16 v[30:33], v[170:173], v[178:181], v[30:33]
	v_mfma_f32_16x16x32_bf16 v[18:21], v[162:165], v[186:189], v[18:21]
	v_mfma_f32_16x16x32_bf16 v[22:25], v[170:173], v[186:189], v[22:25]
	v_mfma_f32_16x16x32_bf16 v[10:13], v[162:165], v[194:197], v[10:13]
	v_mfma_f32_16x16x32_bf16 v[14:17], v[170:173], v[194:197], v[14:17]
	v_mfma_f32_16x16x32_bf16 v[2:5], v[162:165], v[204:207], v[2:5]
	v_mfma_f32_16x16x32_bf16 v[6:9], v[170:173], v[204:207], v[6:9]
	s_setprio 0
	s_barrier
	ds_read_b128 v[142:145], v139
	ds_read_b128 v[146:149], v139 offset:1024
	ds_read_b128 v[150:153], v139 offset:2048
	ds_read_b128 v[154:157], v139 offset:3072
	ds_read_b128 v[158:161], v140
	ds_read_b128 v[162:165], v140 offset:1024
	ds_read_b128 v[166:169], v140 offset:2048
	ds_read_b128 v[170:173], v140 offset:3072
	s_mov_b32 m0, s34
	ds_read_b128 v[174:177], v136 offset:32768
	ds_read_b128 v[178:181], v136 offset:33792
	ds_read_b128 v[182:185], v136 offset:34816
	ds_read_b128 v[186:189], v136 offset:35840
	ds_read_b128 v[190:193], v136 offset:36864
	ds_read_b128 v[194:197], v136 offset:37888
	ds_read_b128 v[198:201], v136 offset:38912
	ds_read_b128 v[204:207], v136 offset:39936
	s_mov_b32 m0, s40
	s_nop 0
	s_bitset1_b32 s77, 19
	s_mov_b32 m0, s42
	s_nop 0
	s_mov_b32 m0, s43
	s_nop 0
	s_waitcnt vmcnt(8)
	s_waitcnt lgkmcnt(0)
	s_barrier
	s_setprio 1
	s_waitcnt lgkmcnt(7)
	v_mfma_f32_16x16x32_bf16 v[122:125], v[142:145], v[174:177], v[122:125]
	v_mfma_f32_16x16x32_bf16 v[126:129], v[150:153], v[174:177], v[126:129]
	s_waitcnt lgkmcnt(5)
	v_mfma_f32_16x16x32_bf16 v[114:117], v[142:145], v[182:185], v[114:117]
	v_mfma_f32_16x16x32_bf16 v[118:121], v[150:153], v[182:185], v[118:121]
	s_waitcnt lgkmcnt(3)
	v_mfma_f32_16x16x32_bf16 v[110:113], v[142:145], v[190:193], v[110:113]
	v_mfma_f32_16x16x32_bf16 v[106:109], v[150:153], v[190:193], v[106:109]
	s_waitcnt lgkmcnt(1)
	v_mfma_f32_16x16x32_bf16 v[98:101], v[142:145], v[198:201], v[98:101]
	v_mfma_f32_16x16x32_bf16 v[102:105], v[150:153], v[198:201], v[102:105]
	v_mfma_f32_16x16x32_bf16 v[58:61], v[158:161], v[174:177], v[58:61]
	v_mfma_f32_16x16x32_bf16 v[62:65], v[166:169], v[174:177], v[62:65]
	v_mfma_f32_16x16x32_bf16 v[50:53], v[158:161], v[182:185], v[50:53]
	v_mfma_f32_16x16x32_bf16 v[54:57], v[166:169], v[182:185], v[54:57]
	v_mfma_f32_16x16x32_bf16 v[42:45], v[158:161], v[190:193], v[42:45]
	v_mfma_f32_16x16x32_bf16 v[46:49], v[166:169], v[190:193], v[46:49]
	v_mfma_f32_16x16x32_bf16 v[34:37], v[158:161], v[198:201], v[34:37]
	v_mfma_f32_16x16x32_bf16 v[38:41], v[166:169], v[198:201], v[38:41]
	v_mfma_f32_16x16x32_bf16 v[122:125], v[146:149], v[178:181], v[122:125]
	v_mfma_f32_16x16x32_bf16 v[126:129], v[154:157], v[178:181], v[126:129]
	v_mfma_f32_16x16x32_bf16 v[114:117], v[146:149], v[186:189], v[114:117]
	v_mfma_f32_16x16x32_bf16 v[118:121], v[154:157], v[186:189], v[118:121]
	v_mfma_f32_16x16x32_bf16 v[110:113], v[146:149], v[194:197], v[110:113]
	v_mfma_f32_16x16x32_bf16 v[106:109], v[154:157], v[194:197], v[106:109]
	s_waitcnt lgkmcnt(0)
	v_mfma_f32_16x16x32_bf16 v[98:101], v[146:149], v[204:207], v[98:101]
	v_mfma_f32_16x16x32_bf16 v[102:105], v[154:157], v[204:207], v[102:105]
	v_mfma_f32_16x16x32_bf16 v[58:61], v[162:165], v[178:181], v[58:61]
	v_mfma_f32_16x16x32_bf16 v[62:65], v[170:173], v[178:181], v[62:65]
	v_mfma_f32_16x16x32_bf16 v[50:53], v[162:165], v[186:189], v[50:53]
	v_mfma_f32_16x16x32_bf16 v[54:57], v[170:173], v[186:189], v[54:57]
	v_mfma_f32_16x16x32_bf16 v[42:45], v[162:165], v[194:197], v[42:45]
	v_mfma_f32_16x16x32_bf16 v[46:49], v[170:173], v[194:197], v[46:49]
	v_mfma_f32_16x16x32_bf16 v[34:37], v[162:165], v[204:207], v[34:37]
	v_mfma_f32_16x16x32_bf16 v[38:41], v[170:173], v[204:207], v[38:41]
	s_setprio 0
	s_barrier
	s_mov_b32 m0, s45
	s_or_b32 s73, s72, 0x80
	ds_read_b128 v[174:177], v136 offset:49152
	ds_read_b128 v[178:181], v136 offset:50176
	ds_read_b128 v[182:185], v136 offset:51200
	ds_read_b128 v[186:189], v136 offset:52224
	ds_read_b128 v[190:193], v136 offset:53248
	ds_read_b128 v[194:197], v136 offset:54272
	ds_read_b128 v[198:201], v136 offset:55296
	ds_read_b128 v[204:207], v136 offset:56320
	s_mov_b32 m0, s46
	s_or_b32 s72, s72, 0x80080
	s_mov_b32 m0, s47
	s_nop 0
	s_mov_b32 m0, s48
	s_nop 0
	s_waitcnt vmcnt(6)
	s_waitcnt lgkmcnt(0)
	s_barrier
	s_setprio 1
	s_waitcnt lgkmcnt(7)
	v_mfma_f32_16x16x32_bf16 v[90:93], v[142:145], v[174:177], v[90:93]
	v_mfma_f32_16x16x32_bf16 v[94:97], v[150:153], v[174:177], v[94:97]
	s_waitcnt lgkmcnt(5)
	v_mfma_f32_16x16x32_bf16 v[82:85], v[142:145], v[182:185], v[82:85]
	v_mfma_f32_16x16x32_bf16 v[86:89], v[150:153], v[182:185], v[86:89]
	s_waitcnt lgkmcnt(3)
	v_mfma_f32_16x16x32_bf16 v[74:77], v[142:145], v[190:193], v[74:77]
	v_mfma_f32_16x16x32_bf16 v[78:81], v[150:153], v[190:193], v[78:81]
	s_waitcnt lgkmcnt(1)
	v_mfma_f32_16x16x32_bf16 v[66:69], v[142:145], v[198:201], v[66:69]
	v_mfma_f32_16x16x32_bf16 v[70:73], v[150:153], v[198:201], v[70:73]
	v_mfma_f32_16x16x32_bf16 v[26:29], v[158:161], v[174:177], v[26:29]
	v_mfma_f32_16x16x32_bf16 v[30:33], v[166:169], v[174:177], v[30:33]
	v_mfma_f32_16x16x32_bf16 v[18:21], v[158:161], v[182:185], v[18:21]
	v_mfma_f32_16x16x32_bf16 v[22:25], v[166:169], v[182:185], v[22:25]
	v_mfma_f32_16x16x32_bf16 v[10:13], v[158:161], v[190:193], v[10:13]
	v_mfma_f32_16x16x32_bf16 v[14:17], v[166:169], v[190:193], v[14:17]
	v_mfma_f32_16x16x32_bf16 v[2:5], v[158:161], v[198:201], v[2:5]
	v_mfma_f32_16x16x32_bf16 v[6:9], v[166:169], v[198:201], v[6:9]
	v_mfma_f32_16x16x32_bf16 v[90:93], v[146:149], v[178:181], v[90:93]
	v_mfma_f32_16x16x32_bf16 v[94:97], v[154:157], v[178:181], v[94:97]
	v_mfma_f32_16x16x32_bf16 v[82:85], v[146:149], v[186:189], v[82:85]
	v_mfma_f32_16x16x32_bf16 v[86:89], v[154:157], v[186:189], v[86:89]
	v_mfma_f32_16x16x32_bf16 v[74:77], v[146:149], v[194:197], v[74:77]
	v_mfma_f32_16x16x32_bf16 v[78:81], v[154:157], v[194:197], v[78:81]
	s_waitcnt lgkmcnt(0)
	v_mfma_f32_16x16x32_bf16 v[66:69], v[146:149], v[204:207], v[66:69]
	v_mfma_f32_16x16x32_bf16 v[70:73], v[154:157], v[204:207], v[70:73]
	v_mfma_f32_16x16x32_bf16 v[26:29], v[162:165], v[178:181], v[26:29]
	v_mfma_f32_16x16x32_bf16 v[30:33], v[170:173], v[178:181], v[30:33]
	v_mfma_f32_16x16x32_bf16 v[18:21], v[162:165], v[186:189], v[18:21]
	v_mfma_f32_16x16x32_bf16 v[22:25], v[170:173], v[186:189], v[22:25]
	v_mfma_f32_16x16x32_bf16 v[10:13], v[162:165], v[194:197], v[10:13]
	v_mfma_f32_16x16x32_bf16 v[14:17], v[170:173], v[194:197], v[14:17]
	v_mfma_f32_16x16x32_bf16 v[2:5], v[162:165], v[204:207], v[2:5]
	v_mfma_f32_16x16x32_bf16 v[6:9], v[170:173], v[204:207], v[6:9]
	s_setprio 0
	s_barrier
	s_add_i32 s63, s63, 2
	s_addk_i32 s62, 0x100
	s_cmp_gt_u32 s63, 29
.Lex_8:
	s_and_b64 vcc, exec, s[22:23]
	s_cbranch_vccz .LBB0_1793
	s_mov_b32 s31, s54
	s_mov_b32 s18, s55
	s_mov_b32 s36, s58
	s_mov_b32 s41, s57
	s_mov_b32 s53, s56
	s_branch .LBB0_1793

.LBB0_1843:
	ds_read_b128 v[2:5], v137
	ds_read_b128 v[6:9], v137 offset:1024
	ds_read_b128 v[10:13], v137 offset:2048
	ds_read_b128 v[14:17], v137 offset:3072
	ds_read_b128 v[18:21], v170
	ds_read_b128 v[22:25], v170 offset:1024
	ds_read_b128 v[26:29], v170 offset:2048
	ds_read_b128 v[30:33], v170 offset:3072
	s_add_i32 s63, s39, s60
	s_add_i32 s61, s34, s60
	s_add_i32 s62, s63, 0x800
	s_addk_i32 s61, 0x800
	s_cmp_eq_u32 s60, 0
	s_cselect_b32 s61, s58, s61
	s_cselect_b32 s62, s57, s62
	s_cbranch_scc0 .Lnx_9
	s_cmp_eq_u64 s[20:21], 0
	s_cbranch_scc1 .Lfin_9
.Lnx_9:
	s_add_i32 s72, s63, 0x780
	s_mov_b32 m0, s47
	ds_read_b128 v[174:177], v136
	ds_read_b128 v[178:181], v136 offset:1024
	ds_read_b128 v[182:185], v136 offset:2048
	ds_read_b128 v[186:189], v136 offset:3072
	ds_read_b128 v[190:193], v136 offset:4096
	ds_read_b128 v[194:197], v136 offset:5120
	ds_read_b128 v[204:207], v136 offset:6144
	ds_read_b128 v[208:211], v136 offset:7168
	buffer_load_dwordx4 v131, s[64:67], s72 offen lds
	s_mov_b32 m0, s49
	s_add_i32 s63, s63, 0x40780
	buffer_load_dwordx4 v133, s[64:67], s72 offen lds
	s_mov_b32 m0, s48
	s_nop 0
	buffer_load_dwordx4 v131, s[64:67], s63 offen lds
	s_mov_b32 m0, s50
	s_nop 0
	buffer_load_dwordx4 v133, s[64:67], s63 offen lds
	s_waitcnt vmcnt(8)
	s_waitcnt lgkmcnt(0)
	s_barrier
	s_setprio 1
	s_waitcnt lgkmcnt(6)
	v_mfma_scale_f32_16x16x128_f8f6f4 v[62:65], v[2:9], v[174:181], v[62:65], v237, v237 op_sel_hi:[0,0,0]
	v_mfma_scale_f32_16x16x128_f8f6f4 v[118:121], v[10:17], v[174:181], v[118:121], v237, v237 op_sel_hi:[0,0,0]
	s_waitcnt lgkmcnt(4)
	v_mfma_scale_f32_16x16x128_f8f6f4 v[54:57], v[2:9], v[182:189], v[54:57], v237, v237 op_sel_hi:[0,0,0]
	v_mfma_scale_f32_16x16x128_f8f6f4 v[50:53], v[10:17], v[182:189], v[50:53], v237, v237 op_sel_hi:[0,0,0]
	s_waitcnt lgkmcnt(2)
	v_mfma_scale_f32_16x16x128_f8f6f4 v[46:49], v[2:9], v[190:197], v[46:49], v237, v237 op_sel_hi:[0,0,0]
	v_mfma_scale_f32_16x16x128_f8f6f4 v[42:45], v[10:17], v[190:197], v[42:45], v237, v237 op_sel_hi:[0,0,0]
	s_waitcnt lgkmcnt(0)
	v_mfma_scale_f32_16x16x128_f8f6f4 v[98:101], v[2:9], v[204:211], v[98:101], v237, v237 op_sel_hi:[0,0,0]
	v_mfma_scale_f32_16x16x128_f8f6f4 v[34:37], v[10:17], v[204:211], v[34:37], v237, v237 op_sel_hi:[0,0,0]
	v_mfma_scale_f32_16x16x128_f8f6f4 v[58:61], v[18:25], v[174:181], v[58:61], v237, v237 op_sel_hi:[0,0,0]
	v_mfma_scale_f32_16x16x128_f8f6f4 v[114:117], v[26:33], v[174:181], v[114:117], v237, v237 op_sel_hi:[0,0,0]
	v_mfma_scale_f32_16x16x128_f8f6f4 v[110:113], v[18:25], v[182:189], v[110:113], v237, v237 op_sel_hi:[0,0,0]
	v_mfma_scale_f32_16x16x128_f8f6f4 v[106:109], v[26:33], v[182:189], v[106:109], v237, v237 op_sel_hi:[0,0,0]
	v_mfma_scale_f32_16x16x128_f8f6f4 v[166:169], v[18:25], v[190:197], v[166:169], v237, v237 op_sel_hi:[0,0,0]
	v_mfma_scale_f32_16x16x128_f8f6f4 v[102:105], v[26:33], v[190:197], v[102:105], v237, v237 op_sel_hi:[0,0,0]
	v_mfma_scale_f32_16x16x128_f8f6f4 v[158:161], v[18:25], v[204:211], v[158:161], v237, v237 op_sel_hi:[0,0,0]
	v_mfma_scale_f32_16x16x128_f8f6f4 v[38:41], v[26:33], v[204:211], v[38:41], v237, v237 op_sel_hi:[0,0,0]
	s_setprio 0
	s_barrier
	s_mov_b32 m0, s31
	ds_read_b128 v[174:177], v136 offset:16384
	ds_read_b128 v[178:181], v136 offset:17408
	ds_read_b128 v[182:185], v136 offset:18432
	ds_read_b128 v[186:189], v136 offset:19456
	ds_read_b128 v[190:193], v136 offset:20480
	ds_read_b128 v[194:197], v136 offset:21504
	ds_read_b128 v[204:207], v136 offset:22528
	ds_read_b128 v[208:211], v136 offset:23552
	buffer_load_dwordx4 v132, s[4:7], s61 offen lds
	s_mov_b32 m0, s35
	s_add_i32 s63, s61, 0x40000
	buffer_load_dwordx4 v134, s[4:7], s61 offen lds
	s_mov_b32 m0, s36
	s_nop 0
	buffer_load_dwordx4 v132, s[4:7], s63 offen lds
	s_mov_b32 m0, s37
	s_nop 0
	buffer_load_dwordx4 v134, s[4:7], s63 offen lds
	s_waitcnt vmcnt(6)
	s_waitcnt lgkmcnt(0)
	s_barrier
	s_setprio 1
	s_waitcnt lgkmcnt(6)
	v_mfma_scale_f32_16x16x128_f8f6f4 v[90:93], v[2:9], v[174:181], v[90:93], v237, v237 op_sel_hi:[0,0,0]
	v_mfma_scale_f32_16x16x128_f8f6f4 v[94:97], v[10:17], v[174:181], v[94:97], v237, v237 op_sel_hi:[0,0,0]
	s_waitcnt lgkmcnt(4)
	v_mfma_scale_f32_16x16x128_f8f6f4 v[82:85], v[2:9], v[182:189], v[82:85], v237, v237 op_sel_hi:[0,0,0]
	v_mfma_scale_f32_16x16x128_f8f6f4 v[86:89], v[10:17], v[182:189], v[86:89], v237, v237 op_sel_hi:[0,0,0]
	s_waitcnt lgkmcnt(2)
	v_mfma_scale_f32_16x16x128_f8f6f4 v[74:77], v[2:9], v[190:197], v[74:77], v237, v237 op_sel_hi:[0,0,0]
	v_mfma_scale_f32_16x16x128_f8f6f4 v[78:81], v[10:17], v[190:197], v[78:81], v237, v237 op_sel_hi:[0,0,0]
	s_waitcnt lgkmcnt(0)
	v_mfma_scale_f32_16x16x128_f8f6f4 v[66:69], v[2:9], v[204:211], v[66:69], v237, v237 op_sel_hi:[0,0,0]
	v_mfma_scale_f32_16x16x128_f8f6f4 v[70:73], v[10:17], v[204:211], v[70:73], v237, v237 op_sel_hi:[0,0,0]
	v_mfma_scale_f32_16x16x128_f8f6f4 v[162:165], v[18:25], v[174:181], v[162:165], v237, v237 op_sel_hi:[0,0,0]
	v_mfma_scale_f32_16x16x128_f8f6f4 v[154:157], v[26:33], v[174:181], v[154:157], v237, v237 op_sel_hi:[0,0,0]
	v_mfma_scale_f32_16x16x128_f8f6f4 v[150:153], v[18:25], v[182:189], v[150:153], v237, v237 op_sel_hi:[0,0,0]
	v_mfma_scale_f32_16x16x128_f8f6f4 v[146:149], v[26:33], v[182:189], v[146:149], v237, v237 op_sel_hi:[0,0,0]
	v_mfma_scale_f32_16x16x128_f8f6f4 v[142:145], v[18:25], v[190:197], v[142:145], v237, v237 op_sel_hi:[0,0,0]
	v_mfma_scale_f32_16x16x128_f8f6f4 v[138:141], v[26:33], v[190:197], v[138:141], v237, v237 op_sel_hi:[0,0,0]
	v_mfma_scale_f32_16x16x128_f8f6f4 v[126:129], v[18:25], v[204:211], v[126:129], v237, v237 op_sel_hi:[0,0,0]
	v_mfma_scale_f32_16x16x128_f8f6f4 v[122:125], v[26:33], v[204:211], v[122:125], v237, v237 op_sel_hi:[0,0,0]
	s_setprio 0
	s_barrier
	ds_read_b128 v[18:21], v171
	ds_read_b128 v[22:25], v171 offset:1024
	ds_read_b128 v[26:29], v171 offset:2048
	ds_read_b128 v[30:33], v171 offset:3072
	ds_read_b128 v[10:13], v172
	ds_read_b128 v[14:17], v172 offset:1024
	ds_read_b128 v[2:5], v172 offset:2048
	ds_read_b128 v[6:9], v172 offset:3072
	s_mov_b32 m0, s30
	ds_read_b128 v[174:177], v136 offset:32768
	ds_read_b128 v[178:181], v136 offset:33792
	ds_read_b128 v[182:185], v136 offset:34816
	ds_read_b128 v[186:189], v136 offset:35840
	ds_read_b128 v[190:193], v136 offset:36864
	ds_read_b128 v[194:197], v136 offset:37888
	ds_read_b128 v[204:207], v136 offset:38912
	ds_read_b128 v[208:211], v136 offset:39936
	buffer_load_dwordx4 v131, s[64:67], s62 offen lds
	s_mov_b32 m0, s38
	s_nop 0
	buffer_load_dwordx4 v133, s[64:67], s62 offen lds
	s_add_i32 s62, s62, 0x40000
	s_mov_b32 m0, s40
	s_nop 0
	buffer_load_dwordx4 v131, s[64:67], s62 offen lds
	s_mov_b32 m0, s41
	s_nop 0
	buffer_load_dwordx4 v133, s[64:67], s62 offen lds
	s_waitcnt vmcnt(8)
	s_waitcnt lgkmcnt(0)
	s_barrier
	s_setprio 1
	s_waitcnt lgkmcnt(6)
	v_mfma_scale_f32_16x16x128_f8f6f4 v[62:65], v[18:25], v[174:181], v[62:65], v237, v237 op_sel_hi:[0,0,0]
	v_mfma_scale_f32_16x16x128_f8f6f4 v[118:121], v[26:33], v[174:181], v[118:121], v237, v237 op_sel_hi:[0,0,0]
	s_waitcnt lgkmcnt(4)
	v_mfma_scale_f32_16x16x128_f8f6f4 v[54:57], v[18:25], v[182:189], v[54:57], v237, v237 op_sel_hi:[0,0,0]
	v_mfma_scale_f32_16x16x128_f8f6f4 v[50:53], v[26:33], v[182:189], v[50:53], v237, v237 op_sel_hi:[0,0,0]
	s_waitcnt lgkmcnt(2)
	v_mfma_scale_f32_16x16x128_f8f6f4 v[46:49], v[18:25], v[190:197], v[46:49], v237, v237 op_sel_hi:[0,0,0]
	v_mfma_scale_f32_16x16x128_f8f6f4 v[42:45], v[26:33], v[190:197], v[42:45], v237, v237 op_sel_hi:[0,0,0]
	s_waitcnt lgkmcnt(0)
	v_mfma_scale_f32_16x16x128_f8f6f4 v[98:101], v[18:25], v[204:211], v[98:101], v237, v237 op_sel_hi:[0,0,0]
	v_mfma_scale_f32_16x16x128_f8f6f4 v[34:37], v[26:33], v[204:211], v[34:37], v237, v237 op_sel_hi:[0,0,0]
	v_mfma_scale_f32_16x16x128_f8f6f4 v[58:61], v[10:17], v[174:181], v[58:61], v237, v237 op_sel_hi:[0,0,0]
	v_mfma_scale_f32_16x16x128_f8f6f4 v[114:117], v[2:9], v[174:181], v[114:117], v237, v237 op_sel_hi:[0,0,0]
	v_mfma_scale_f32_16x16x128_f8f6f4 v[110:113], v[10:17], v[182:189], v[110:113], v237, v237 op_sel_hi:[0,0,0]
	v_mfma_scale_f32_16x16x128_f8f6f4 v[106:109], v[2:9], v[182:189], v[106:109], v237, v237 op_sel_hi:[0,0,0]
	v_mfma_scale_f32_16x16x128_f8f6f4 v[166:169], v[10:17], v[190:197], v[166:169], v237, v237 op_sel_hi:[0,0,0]
	v_mfma_scale_f32_16x16x128_f8f6f4 v[102:105], v[2:9], v[190:197], v[102:105], v237, v237 op_sel_hi:[0,0,0]
	v_mfma_scale_f32_16x16x128_f8f6f4 v[158:161], v[10:17], v[204:211], v[158:161], v237, v237 op_sel_hi:[0,0,0]
	v_mfma_scale_f32_16x16x128_f8f6f4 v[38:41], v[2:9], v[204:211], v[38:41], v237, v237 op_sel_hi:[0,0,0]
	s_setprio 0
	s_barrier
	s_mov_b32 m0, s43
	s_or_b32 s62, s61, 0x80
	ds_read_b128 v[174:177], v136 offset:49152
	ds_read_b128 v[178:181], v136 offset:50176
	ds_read_b128 v[182:185], v136 offset:51200
	ds_read_b128 v[186:189], v136 offset:52224
	ds_read_b128 v[190:193], v136 offset:53248
	ds_read_b128 v[194:197], v136 offset:54272
	ds_read_b128 v[204:207], v136 offset:55296
	ds_read_b128 v[208:211], v136 offset:56320
	buffer_load_dwordx4 v132, s[4:7], s62 offen lds
	s_mov_b32 m0, s44
	s_add_i32 s61, s61, 0x40080
	buffer_load_dwordx4 v134, s[4:7], s62 offen lds
	s_mov_b32 m0, s45
	s_nop 0
	buffer_load_dwordx4 v132, s[4:7], s61 offen lds
	s_mov_b32 m0, s46
	s_nop 0
	buffer_load_dwordx4 v134, s[4:7], s61 offen lds
	s_waitcnt vmcnt(6)
	s_waitcnt lgkmcnt(0)
	s_barrier
	s_setprio 1
	s_waitcnt lgkmcnt(6)
	v_mfma_scale_f32_16x16x128_f8f6f4 v[90:93], v[18:25], v[174:181], v[90:93], v237, v237 op_sel_hi:[0,0,0]
	v_mfma_scale_f32_16x16x128_f8f6f4 v[94:97], v[26:33], v[174:181], v[94:97], v237, v237 op_sel_hi:[0,0,0]
	s_waitcnt lgkmcnt(4)
	v_mfma_scale_f32_16x16x128_f8f6f4 v[82:85], v[18:25], v[182:189], v[82:85], v237, v237 op_sel_hi:[0,0,0]
	v_mfma_scale_f32_16x16x128_f8f6f4 v[86:89], v[26:33], v[182:189], v[86:89], v237, v237 op_sel_hi:[0,0,0]
	s_waitcnt lgkmcnt(2)
	v_mfma_scale_f32_16x16x128_f8f6f4 v[74:77], v[18:25], v[190:197], v[74:77], v237, v237 op_sel_hi:[0,0,0]
	v_mfma_scale_f32_16x16x128_f8f6f4 v[78:81], v[26:33], v[190:197], v[78:81], v237, v237 op_sel_hi:[0,0,0]
	s_waitcnt lgkmcnt(0)
	v_mfma_scale_f32_16x16x128_f8f6f4 v[66:69], v[18:25], v[204:211], v[66:69], v237, v237 op_sel_hi:[0,0,0]
	v_mfma_scale_f32_16x16x128_f8f6f4 v[70:73], v[26:33], v[204:211], v[70:73], v237, v237 op_sel_hi:[0,0,0]
	v_mfma_scale_f32_16x16x128_f8f6f4 v[162:165], v[10:17], v[174:181], v[162:165], v237, v237 op_sel_hi:[0,0,0]
	v_mfma_scale_f32_16x16x128_f8f6f4 v[154:157], v[2:9], v[174:181], v[154:157], v237, v237 op_sel_hi:[0,0,0]
	v_mfma_scale_f32_16x16x128_f8f6f4 v[150:153], v[10:17], v[182:189], v[150:153], v237, v237 op_sel_hi:[0,0,0]
	v_mfma_scale_f32_16x16x128_f8f6f4 v[146:149], v[2:9], v[182:189], v[146:149], v237, v237 op_sel_hi:[0,0,0]
	v_mfma_scale_f32_16x16x128_f8f6f4 v[142:145], v[10:17], v[190:197], v[142:145], v237, v237 op_sel_hi:[0,0,0]
	v_mfma_scale_f32_16x16x128_f8f6f4 v[138:141], v[2:9], v[190:197], v[138:141], v237, v237 op_sel_hi:[0,0,0]
	v_mfma_scale_f32_16x16x128_f8f6f4 v[126:129], v[10:17], v[204:211], v[126:129], v237, v237 op_sel_hi:[0,0,0]
	v_mfma_scale_f32_16x16x128_f8f6f4 v[122:125], v[2:9], v[204:211], v[122:125], v237, v237 op_sel_hi:[0,0,0]
	s_setprio 0
	s_barrier
	s_add_i32 s59, s59, 2
	s_addk_i32 s60, 0x100
	s_cmp_gt_u32 s59, 13
	s_cbranch_scc0 .LBB0_1843
	s_branch .Lex_9
.Lfin_9:
	s_add_i32 s72, s63, 0x780
	s_mov_b32 m0, s47
	ds_read_b128 v[174:177], v136
	ds_read_b128 v[178:181], v136 offset:1024
	ds_read_b128 v[182:185], v136 offset:2048
	ds_read_b128 v[186:189], v136 offset:3072
	ds_read_b128 v[190:193], v136 offset:4096
	ds_read_b128 v[194:197], v136 offset:5120
	ds_read_b128 v[204:207], v136 offset:6144
	ds_read_b128 v[208:211], v136 offset:7168
	buffer_load_dwordx4 v131, s[64:67], s72 offen lds
	s_mov_b32 m0, s49
	s_add_i32 s63, s63, 0x40780
	buffer_load_dwordx4 v133, s[64:67], s72 offen lds
	s_mov_b32 m0, s48
	s_nop 0
	buffer_load_dwordx4 v131, s[64:67], s63 offen lds
	s_mov_b32 m0, s50
	s_nop 0
	buffer_load_dwordx4 v133, s[64:67], s63 offen lds
	s_waitcnt vmcnt(8)
	s_waitcnt lgkmcnt(0)
	s_barrier
	s_setprio 1
	s_waitcnt lgkmcnt(6)
	v_mfma_scale_f32_16x16x128_f8f6f4 v[62:65], v[2:9], v[174:181], v[62:65], v237, v237 op_sel_hi:[0,0,0]
	v_mfma_scale_f32_16x16x128_f8f6f4 v[118:121], v[10:17], v[174:181], v[118:121], v237, v237 op_sel_hi:[0,0,0]
	s_waitcnt lgkmcnt(4)
	v_mfma_scale_f32_16x16x128_f8f6f4 v[54:57], v[2:9], v[182:189], v[54:57], v237, v237 op_sel_hi:[0,0,0]
	v_mfma_scale_f32_16x16x128_f8f6f4 v[50:53], v[10:17], v[182:189], v[50:53], v237, v237 op_sel_hi:[0,0,0]
	s_waitcnt lgkmcnt(2)
	v_mfma_scale_f32_16x16x128_f8f6f4 v[46:49], v[2:9], v[190:197], v[46:49], v237, v237 op_sel_hi:[0,0,0]
	v_mfma_scale_f32_16x16x128_f8f6f4 v[42:45], v[10:17], v[190:197], v[42:45], v237, v237 op_sel_hi:[0,0,0]
	s_waitcnt lgkmcnt(0)
	v_mfma_scale_f32_16x16x128_f8f6f4 v[98:101], v[2:9], v[204:211], v[98:101], v237, v237 op_sel_hi:[0,0,0]
	v_mfma_scale_f32_16x16x128_f8f6f4 v[34:37], v[10:17], v[204:211], v[34:37], v237, v237 op_sel_hi:[0,0,0]
	v_mfma_scale_f32_16x16x128_f8f6f4 v[58:61], v[18:25], v[174:181], v[58:61], v237, v237 op_sel_hi:[0,0,0]
	v_mfma_scale_f32_16x16x128_f8f6f4 v[114:117], v[26:33], v[174:181], v[114:117], v237, v237 op_sel_hi:[0,0,0]
	v_mfma_scale_f32_16x16x128_f8f6f4 v[110:113], v[18:25], v[182:189], v[110:113], v237, v237 op_sel_hi:[0,0,0]
	v_mfma_scale_f32_16x16x128_f8f6f4 v[106:109], v[26:33], v[182:189], v[106:109], v237, v237 op_sel_hi:[0,0,0]
	v_mfma_scale_f32_16x16x128_f8f6f4 v[166:169], v[18:25], v[190:197], v[166:169], v237, v237 op_sel_hi:[0,0,0]
	v_mfma_scale_f32_16x16x128_f8f6f4 v[102:105], v[26:33], v[190:197], v[102:105], v237, v237 op_sel_hi:[0,0,0]
	v_mfma_scale_f32_16x16x128_f8f6f4 v[158:161], v[18:25], v[204:211], v[158:161], v237, v237 op_sel_hi:[0,0,0]
	v_mfma_scale_f32_16x16x128_f8f6f4 v[38:41], v[26:33], v[204:211], v[38:41], v237, v237 op_sel_hi:[0,0,0]
	s_setprio 0
	s_barrier
	s_mov_b32 m0, s31
	ds_read_b128 v[174:177], v136 offset:16384
	ds_read_b128 v[178:181], v136 offset:17408
	ds_read_b128 v[182:185], v136 offset:18432
	ds_read_b128 v[186:189], v136 offset:19456
	ds_read_b128 v[190:193], v136 offset:20480
	ds_read_b128 v[194:197], v136 offset:21504
	ds_read_b128 v[204:207], v136 offset:22528
	ds_read_b128 v[208:211], v136 offset:23552
	s_mov_b32 m0, s35
	s_add_i32 s63, s61, 0x40000
	s_mov_b32 m0, s36
	s_nop 0
	s_mov_b32 m0, s37
	s_nop 0
	s_waitcnt vmcnt(0)
	s_waitcnt lgkmcnt(0)
	s_barrier
	s_setprio 1
	s_waitcnt lgkmcnt(6)
	v_mfma_scale_f32_16x16x128_f8f6f4 v[90:93], v[2:9], v[174:181], v[90:93], v237, v237 op_sel_hi:[0,0,0]
	v_mfma_scale_f32_16x16x128_f8f6f4 v[94:97], v[10:17], v[174:181], v[94:97], v237, v237 op_sel_hi:[0,0,0]
	s_waitcnt lgkmcnt(4)
	v_mfma_scale_f32_16x16x128_f8f6f4 v[82:85], v[2:9], v[182:189], v[82:85], v237, v237 op_sel_hi:[0,0,0]
	v_mfma_scale_f32_16x16x128_f8f6f4 v[86:89], v[10:17], v[182:189], v[86:89], v237, v237 op_sel_hi:[0,0,0]
	s_waitcnt lgkmcnt(2)
	v_mfma_scale_f32_16x16x128_f8f6f4 v[74:77], v[2:9], v[190:197], v[74:77], v237, v237 op_sel_hi:[0,0,0]
	v_mfma_scale_f32_16x16x128_f8f6f4 v[78:81], v[10:17], v[190:197], v[78:81], v237, v237 op_sel_hi:[0,0,0]
	s_waitcnt lgkmcnt(0)
	v_mfma_scale_f32_16x16x128_f8f6f4 v[66:69], v[2:9], v[204:211], v[66:69], v237, v237 op_sel_hi:[0,0,0]
	v_mfma_scale_f32_16x16x128_f8f6f4 v[70:73], v[10:17], v[204:211], v[70:73], v237, v237 op_sel_hi:[0,0,0]
	v_mfma_scale_f32_16x16x128_f8f6f4 v[162:165], v[18:25], v[174:181], v[162:165], v237, v237 op_sel_hi:[0,0,0]
	v_mfma_scale_f32_16x16x128_f8f6f4 v[154:157], v[26:33], v[174:181], v[154:157], v237, v237 op_sel_hi:[0,0,0]
	v_mfma_scale_f32_16x16x128_f8f6f4 v[150:153], v[18:25], v[182:189], v[150:153], v237, v237 op_sel_hi:[0,0,0]
	v_mfma_scale_f32_16x16x128_f8f6f4 v[146:149], v[26:33], v[182:189], v[146:149], v237, v237 op_sel_hi:[0,0,0]
	v_mfma_scale_f32_16x16x128_f8f6f4 v[142:145], v[18:25], v[190:197], v[142:145], v237, v237 op_sel_hi:[0,0,0]
	v_mfma_scale_f32_16x16x128_f8f6f4 v[138:141], v[26:33], v[190:197], v[138:141], v237, v237 op_sel_hi:[0,0,0]
	v_mfma_scale_f32_16x16x128_f8f6f4 v[126:129], v[18:25], v[204:211], v[126:129], v237, v237 op_sel_hi:[0,0,0]
	v_mfma_scale_f32_16x16x128_f8f6f4 v[122:125], v[26:33], v[204:211], v[122:125], v237, v237 op_sel_hi:[0,0,0]
	s_setprio 0
	s_barrier
	ds_read_b128 v[18:21], v171
	ds_read_b128 v[22:25], v171 offset:1024
	ds_read_b128 v[26:29], v171 offset:2048
	ds_read_b128 v[30:33], v171 offset:3072
	ds_read_b128 v[10:13], v172
	ds_read_b128 v[14:17], v172 offset:1024
	ds_read_b128 v[2:5], v172 offset:2048
	ds_read_b128 v[6:9], v172 offset:3072
	s_mov_b32 m0, s30
	ds_read_b128 v[174:177], v136 offset:32768
	ds_read_b128 v[178:181], v136 offset:33792
	ds_read_b128 v[182:185], v136 offset:34816
	ds_read_b128 v[186:189], v136 offset:35840
	ds_read_b128 v[190:193], v136 offset:36864
	ds_read_b128 v[194:197], v136 offset:37888
	ds_read_b128 v[204:207], v136 offset:38912
	ds_read_b128 v[208:211], v136 offset:39936
	s_mov_b32 m0, s38
	s_nop 0
	s_add_i32 s62, s62, 0x40000
	s_mov_b32 m0, s40
	s_nop 0
	s_mov_b32 m0, s41
	s_nop 0
	s_waitcnt vmcnt(8)
	s_waitcnt lgkmcnt(0)
	s_barrier
	s_setprio 1
	s_waitcnt lgkmcnt(6)
	v_mfma_scale_f32_16x16x128_f8f6f4 v[62:65], v[18:25], v[174:181], v[62:65], v237, v237 op_sel_hi:[0,0,0]
	v_mfma_scale_f32_16x16x128_f8f6f4 v[118:121], v[26:33], v[174:181], v[118:121], v237, v237 op_sel_hi:[0,0,0]
	s_waitcnt lgkmcnt(4)
	v_mfma_scale_f32_16x16x128_f8f6f4 v[54:57], v[18:25], v[182:189], v[54:57], v237, v237 op_sel_hi:[0,0,0]
	v_mfma_scale_f32_16x16x128_f8f6f4 v[50:53], v[26:33], v[182:189], v[50:53], v237, v237 op_sel_hi:[0,0,0]
	s_waitcnt lgkmcnt(2)
	v_mfma_scale_f32_16x16x128_f8f6f4 v[46:49], v[18:25], v[190:197], v[46:49], v237, v237 op_sel_hi:[0,0,0]
	v_mfma_scale_f32_16x16x128_f8f6f4 v[42:45], v[26:33], v[190:197], v[42:45], v237, v237 op_sel_hi:[0,0,0]
	s_waitcnt lgkmcnt(0)
	v_mfma_scale_f32_16x16x128_f8f6f4 v[98:101], v[18:25], v[204:211], v[98:101], v237, v237 op_sel_hi:[0,0,0]
	v_mfma_scale_f32_16x16x128_f8f6f4 v[34:37], v[26:33], v[204:211], v[34:37], v237, v237 op_sel_hi:[0,0,0]
	v_mfma_scale_f32_16x16x128_f8f6f4 v[58:61], v[10:17], v[174:181], v[58:61], v237, v237 op_sel_hi:[0,0,0]
	v_mfma_scale_f32_16x16x128_f8f6f4 v[114:117], v[2:9], v[174:181], v[114:117], v237, v237 op_sel_hi:[0,0,0]
	v_mfma_scale_f32_16x16x128_f8f6f4 v[110:113], v[10:17], v[182:189], v[110:113], v237, v237 op_sel_hi:[0,0,0]
	v_mfma_scale_f32_16x16x128_f8f6f4 v[106:109], v[2:9], v[182:189], v[106:109], v237, v237 op_sel_hi:[0,0,0]
	v_mfma_scale_f32_16x16x128_f8f6f4 v[166:169], v[10:17], v[190:197], v[166:169], v237, v237 op_sel_hi:[0,0,0]
	v_mfma_scale_f32_16x16x128_f8f6f4 v[102:105], v[2:9], v[190:197], v[102:105], v237, v237 op_sel_hi:[0,0,0]
	v_mfma_scale_f32_16x16x128_f8f6f4 v[158:161], v[10:17], v[204:211], v[158:161], v237, v237 op_sel_hi:[0,0,0]
	v_mfma_scale_f32_16x16x128_f8f6f4 v[38:41], v[2:9], v[204:211], v[38:41], v237, v237 op_sel_hi:[0,0,0]
	s_setprio 0
	s_barrier
	s_mov_b32 m0, s43
	s_or_b32 s62, s61, 0x80
	ds_read_b128 v[174:177], v136 offset:49152
	ds_read_b128 v[178:181], v136 offset:50176
	ds_read_b128 v[182:185], v136 offset:51200
	ds_read_b128 v[186:189], v136 offset:52224
	ds_read_b128 v[190:193], v136 offset:53248
	ds_read_b128 v[194:197], v136 offset:54272
	ds_read_b128 v[204:207], v136 offset:55296
	ds_read_b128 v[208:211], v136 offset:56320
	s_mov_b32 m0, s44
	s_add_i32 s61, s61, 0x40080
	s_mov_b32 m0, s45
	s_nop 0
	s_mov_b32 m0, s46
	s_nop 0
	s_waitcnt vmcnt(6)
	s_waitcnt lgkmcnt(0)
	s_barrier
	s_setprio 1
	s_waitcnt lgkmcnt(6)
	v_mfma_scale_f32_16x16x128_f8f6f4 v[90:93], v[18:25], v[174:181], v[90:93], v237, v237 op_sel_hi:[0,0,0]
	v_mfma_scale_f32_16x16x128_f8f6f4 v[94:97], v[26:33], v[174:181], v[94:97], v237, v237 op_sel_hi:[0,0,0]
	s_waitcnt lgkmcnt(4)
	v_mfma_scale_f32_16x16x128_f8f6f4 v[82:85], v[18:25], v[182:189], v[82:85], v237, v237 op_sel_hi:[0,0,0]
	v_mfma_scale_f32_16x16x128_f8f6f4 v[86:89], v[26:33], v[182:189], v[86:89], v237, v237 op_sel_hi:[0,0,0]
	s_waitcnt lgkmcnt(2)
	v_mfma_scale_f32_16x16x128_f8f6f4 v[74:77], v[18:25], v[190:197], v[74:77], v237, v237 op_sel_hi:[0,0,0]
	v_mfma_scale_f32_16x16x128_f8f6f4 v[78:81], v[26:33], v[190:197], v[78:81], v237, v237 op_sel_hi:[0,0,0]
	s_waitcnt lgkmcnt(0)
	v_mfma_scale_f32_16x16x128_f8f6f4 v[66:69], v[18:25], v[204:211], v[66:69], v237, v237 op_sel_hi:[0,0,0]
	v_mfma_scale_f32_16x16x128_f8f6f4 v[70:73], v[26:33], v[204:211], v[70:73], v237, v237 op_sel_hi:[0,0,0]
	v_mfma_scale_f32_16x16x128_f8f6f4 v[162:165], v[10:17], v[174:181], v[162:165], v237, v237 op_sel_hi:[0,0,0]
	v_mfma_scale_f32_16x16x128_f8f6f4 v[154:157], v[2:9], v[174:181], v[154:157], v237, v237 op_sel_hi:[0,0,0]
	v_mfma_scale_f32_16x16x128_f8f6f4 v[150:153], v[10:17], v[182:189], v[150:153], v237, v237 op_sel_hi:[0,0,0]
	v_mfma_scale_f32_16x16x128_f8f6f4 v[146:149], v[2:9], v[182:189], v[146:149], v237, v237 op_sel_hi:[0,0,0]
	v_mfma_scale_f32_16x16x128_f8f6f4 v[142:145], v[10:17], v[190:197], v[142:145], v237, v237 op_sel_hi:[0,0,0]
	v_mfma_scale_f32_16x16x128_f8f6f4 v[138:141], v[2:9], v[190:197], v[138:141], v237, v237 op_sel_hi:[0,0,0]
	v_mfma_scale_f32_16x16x128_f8f6f4 v[126:129], v[10:17], v[204:211], v[126:129], v237, v237 op_sel_hi:[0,0,0]
	v_mfma_scale_f32_16x16x128_f8f6f4 v[122:125], v[2:9], v[204:211], v[122:125], v237, v237 op_sel_hi:[0,0,0]
	s_setprio 0
	s_barrier
	s_add_i32 s59, s59, 2
	s_addk_i32 s60, 0x100
	s_cmp_gt_u32 s59, 13
.Lex_9:
	s_nop 15
	s_nop 15
	s_and_b64 vcc, exec, s[20:21]
	s_cbranch_vccz .LBB0_1839
	s_mov_b32 s29, s52
	s_mov_b32 s0, s53
	s_mov_b32 s34, s56
	s_mov_b32 s39, s55
	s_mov_b32 s51, s54
	s_branch .LBB0_1839
